# K-loops: per-block priority toggles replaced by one static priority raise for waves 4-7 per GEMM phase (code placement preserved)
# baseline (speedup 1.0000x reference)
; #define G8_STAGE(bufoff, gbase, voff) do { _Pragma("unroll") for (int _i = 0; _i < 2; ++_i) \
;         __builtin_amdgcn_global_load_lds((const unsigned*)((const char*)(gbase) + (voff)[_i]), (LAS unsigned*)(lds + (bufoff) + ldsw + _i * 8192), 16, 0, 0); } while (0)
; #define G8_WAIT_V(n) asm volatile("s_waitcnt vmcnt(" #n ")" ::: "memory")
; #define G8_BAR __builtin_amdgcn_s_barrier()
; template <class Epi, class Sched>
; __device__ __forceinline__ void gemm_phase(LAS unsigned char* lds, const int K, const Sched& S, const Epi& E) {
;     int tid_ = S.tid0; asm volatile("" : "+v"(tid_));
;     const int tid = tid_, wid = __builtin_amdgcn_readfirstlane(tid >> 6), lane = tid & 63, wr = wid >> 2, wc = wid & 3, fr = lane & 15, fq = lane >> 4;
;     const int nt = K / BK;
;     unsigned voffB[2];
; #pragma unroll
;     for (int i = 0; i < 2; ++i) { int R, C; stage_rc(tid * 16 + i * 8192, R, C); const int Rb = Epi::PERM ? ((R & ~31) + perm32(R & 31)) : R;
;         voffB[i] = (unsigned)(Rb * K + C) * 2u; }
;     const size_t kstep = (size_t)(BK * 2);
;     const size_t hstep = (size_t)HALF * K * 2;
;     const unsigned ldsw = (unsigned)wid * 1024u;
;     const int aoff = lds_byte(wr * 64 + fr, fq * 8), boff = lds_byte(wc * 32 + fr, fq * 8);
;     ...
;     Unit cur, nxt; int ui = 0;
;     if (!S.next(0, cur)) return;
;     f32x4 acc[2][2][4][2];
;     E.init(acc, cur, wc, fq);
;     bf16x8 At[4][2], B0[2][2], B1[2][2];
;     unsigned oc[2][2];
;     S.aoff(cur, tid, oc);
;     const char* cA = cur.A; const char* cB = cur.B;
;     G8_STAGE(G8_SB(0, 0), cB, voffB); G8_STAGE(G8_SA(0, 0), cA, oc[0]); G8_STAGE(G8_SB(0, 1), cB + hstep, voffB); G8_STAGE(G8_SA(0, 1), cA, oc[1]);
;     if (wr == 1) G8_BAR;
;     G8_WAIT_V(4); G8_BAR;
;     G8_STAGE(G8_SB(1, 0), cB + kstep, voffB); G8_STAGE(G8_SA(1, 0), cA + kstep, oc[0]); G8_STAGE(G8_SB(1, 1), cB + hstep + kstep, voffB);
;     G8_WAIT_V(6); G8_BAR;
.LBB0_313:
	v_ashrrev_i32_e32 v3, 31, v0
	v_lshrrev_b32_e32 v3, 26, v3
	v_add_u32_e32 v3, v0, v3
	v_ashrrev_i32_e32 v18, 6, v3
	v_bfe_i32 v3, v0, 27, 1
	v_lshlrev_b32_e32 v2, 4, v0
	v_lshrrev_b32_e32 v3, 22, v3
	v_add_u32_e32 v3, v2, v3
	v_and_b32_e32 v3, 0xfffffc00, v3
	v_sub_u32_e32 v3, v2, v3
	v_lshrrev_b32_e32 v4, 4, v3
	v_bitop3_b32 v3, v4, v3, 32 bitop3:0x6c
	v_ashrrev_i32_e32 v5, 31, v3
	v_lshrrev_b32_e32 v5, 26, v5
	v_lshlrev_b32_e32 v4, 3, v18
	v_add_u32_e32 v5, v3, v5
	v_and_b32_e32 v4, -16, v4
	v_ashrrev_i32_e32 v19, 6, v5
	v_add_u32_e32 v10, v19, v4
	v_lshlrev_b32_e32 v4, 5, v18
	v_and_b32_e32 v20, 32, v4
	v_and_b32_e32 v4, 0xc0, v5
	v_sub_u32_e32 v3, v3, v4
	v_ashrrev_i16_sdwa v21, v203, sext(v3) dst_sel:DWORD dst_unused:UNUSED_PAD src0_sel:DWORD src1_sel:BYTE_0
	v_lshlrev_b32_e32 v3, 1, v10
	v_lshrrev_b32_e32 v4, 2, v10
	v_and_b32_e32 v5, 3, v19
	s_mov_b32 s1, 0x1fffe0
	v_add_u32_sdwa v11, v20, sext(v21) dst_sel:DWORD dst_unused:UNUSED_PAD src0_sel:DWORD src1_sel:WORD_0
	v_and_b32_e32 v3, 24, v3
	v_and_b32_e32 v4, 4, v4
	v_and_or_b32 v5, v10, s1, v5
	v_or3_b32 v3, v5, v4, v3
	v_lshlrev_b32_e32 v12, 1, v11
	v_add_u32_e32 v2, 0x2000, v2
	v_lshl_add_u32 v132, v3, 11, v12
	v_ashrrev_i32_e32 v3, 31, v2
	v_lshrrev_b32_e32 v3, 22, v3
	v_add_u32_e32 v3, v2, v3
	v_ashrrev_i32_e32 v22, 10, v3
	v_mul_i32_i24_e32 v3, 0x400, v22
	v_sub_u32_e32 v2, v2, v3
	v_lshrrev_b32_e32 v3, 4, v2
	v_bitop3_b32 v2, v3, v2, 32 bitop3:0x6c
	v_ashrrev_i32_e32 v4, 31, v2
	v_lshrrev_b32_e32 v4, 26, v4
	v_lshlrev_b32_e32 v3, 3, v22
	v_add_u32_e32 v4, v2, v4
	v_and_b32_e32 v3, -16, v3
	v_ashrrev_i32_e32 v23, 6, v4
	v_add_u32_e32 v13, v23, v3
	v_lshlrev_b32_e32 v3, 5, v22
	v_and_b32_e32 v24, 32, v3
	v_and_b32_e32 v3, 0xc0, v4
	s_ashr_i32 s0, s56, 6
	v_sub_u32_e32 v2, v2, v3
	s_and_b32 s5, s0, 3
	v_ashrrev_i16_sdwa v25, v203, sext(v2) dst_sel:DWORD dst_unused:UNUSED_PAD src0_sel:DWORD src1_sel:BYTE_0
	v_lshlrev_b32_e32 v2, 1, v13
	v_lshrrev_b32_e32 v3, 2, v13
	v_and_b32_e32 v4, 3, v23
	s_lshl_b32 s6, s14, 9
	v_add_u32_sdwa v14, v24, sext(v25) dst_sel:DWORD dst_unused:UNUSED_PAD src0_sel:DWORD src1_sel:WORD_0
	v_and_b32_e32 v2, 24, v2
	v_and_b32_e32 v3, 4, v3
	v_and_or_b32 v4, v13, s1, v4
	v_bfe_u32 v26, v0, 4, 2
	s_lshl_b32 s57, s0, 10
	s_lshl_b32 s0, s5, 6
	s_add_i32 s6, s6, 0
	v_or3_b32 v2, v4, v3, v2
	v_lshlrev_b32_e32 v15, 1, v14
	v_lshlrev_b32_e32 v27, 4, v26
	s_add_i32 s6, s6, s0
	v_lshl_add_u32 v134, v2, 11, v15
	v_add_u32_e32 v2, s6, v27
	s_add_i32 s58, s57, 0
	v_add_u32_e32 v2, 0x20000, v2
	s_add_i32 m0, s58, 0x10000
	ds_read_b128 v[6:9], v2
	ds_read_b128 v[2:5], v2 offset:256
	global_load_lds_dwordx4 v132, s[36:37]
	s_add_i32 m0, s58, 0x12000
	s_ashr_i32 s1, s56, 8
	v_lshl_add_u32 v136, v10, 11, v12
	global_load_lds_dwordx4 v134, s[36:37]
	s_mov_b32 m0, s58
	s_add_i32 s59, s58, 0x2000
	v_lshl_add_u32 v140, v13, 11, v15
	global_load_lds_dwordx4 v136, s[2:3]
	s_mov_b32 m0, s59
	s_add_u32 s6, s36, 0x40000
	global_load_lds_dwordx4 v140, s[2:3]
	s_addc_u32 s7, s37, 0
	s_add_i32 m0, s58, 0x14000
	v_lshl_add_u32 v10, v10, 10, v11
	global_load_lds_dwordx4 v132, s[6:7]
	s_add_i32 m0, s58, 0x16000
	s_add_i32 s60, s58, 0x4000
	v_lshl_add_u32 v138, v10, 1, v206
	v_lshl_add_u32 v10, v13, 10, v14
	global_load_lds_dwordx4 v134, s[6:7]
	s_mov_b32 m0, s60
	s_add_i32 s61, s58, 0x6000
	v_lshl_add_u32 v142, v10, 1, v206
	global_load_lds_dwordx4 v138, s[2:3]
	s_mov_b32 m0, s61
	v_mov_b32_e32 v133, v1
	global_load_lds_dwordx4 v142, s[2:3]
	v_mov_b32_e32 v135, v1
	v_mov_b32_e32 v137, v1
	v_mov_b32_e32 v141, v1
	v_lshl_add_u64 v[16:17], s[36:37], 0, v[132:133]
	v_lshl_add_u64 v[14:15], s[36:37], 0, v[134:135]
	v_lshl_add_u64 v[12:13], s[2:3], 0, v[136:137]
	s_cmp_lg_u32 s1, 1
	v_lshl_add_u64 v[10:11], s[2:3], 0, v[140:141]
	s_cbranch_scc1 .LBB0_315
	s_barrier
	s_setprio 1
	s_nop 0
	s_nop 0
	s_nop 0
	s_nop 0
	s_nop 0
	s_nop 0
	s_nop 0
	s_nop 0
	s_nop 0
	s_nop 0
	s_nop 0
	s_nop 0
	s_nop 0
	s_nop 0
	s_nop 0

; #define G8_STAGE(bufoff, gbase, voff) do { _Pragma("unroll") for (int _i = 0; _i < 2; ++_i) \
;         __builtin_amdgcn_global_load_lds((const unsigned*)((const char*)(gbase) + (voff)[_i]), (LAS unsigned*)(lds + (bufoff) + ldsw + _i * 8192), 16, 0, 0); } while (0)
; #define G8_LDA(dst, b, h) do { _Pragma("unroll") for (int m = 0; m < 4; ++m) _Pragma("unroll") for (int k = 0; k < 2; ++k) dst[m][k] = *(const LAS bf16x8*)(lds + G8_SA(b, h) + aoff + m * 2048 + k * 1024); } while (0)
; #define G8_LDB(dst, b, h) do { _Pragma("unroll") for (int n = 0; n < 2; ++n) _Pragma("unroll") for (int k = 0; k < 2; ++k) dst[n][k] = *(const LAS bf16x8*)(lds + G8_SB(b, h) + boff + n * 2048 + k * 1024); } while (0)
; #define G8_MMA(ai, bj, At, Bt) do { __builtin_amdgcn_s_setprio(1); _Pragma("unroll") for (int m = 0; m < 4; ++m) _Pragma("unroll") for (int n = 0; n < 2; ++n) _Pragma("unroll") for (int k = 0; k < 2; ++k) \
;         acc[ai][bj][m][n] = __builtin_amdgcn_mfma_f32_16x16x32_bf16(Bt[n][k], At[m][k], acc[ai][bj][m][n], 0, 0, 0); __builtin_amdgcn_s_setprio(0); } while (0)
; #define G8_WAIT_V(n) asm volatile("s_waitcnt vmcnt(" #n ")" ::: "memory")
; #define G8_WAIT_L(n) asm volatile("s_waitcnt lgkmcnt(" #n ")" ::: "memory")
; #define G8_BAR __builtin_amdgcn_s_barrier()
; #define G8_SCHED __builtin_amdgcn_sched_barrier(0)
; template <class Epi, class Sched>
; __device__ __forceinline__ void gemm_phase(LAS unsigned char* lds, const int K, const Sched& S, const Epi& E) {
;     ...
;             G8_LDB(B0, 0, 0); G8_SCHED; G8_LDA(At, 0, 0); G8_STAGE(G8_SA(1, 1), a1, oc[1]);
;             if (last && has_next) S.aoff(nxt, tid, oc);
;             G8_WAIT_L(8); G8_BAR; G8_WAIT_L(0); G8_MMA(0, 0, At, B0); G8_BAR; G8_SCHED;
;             G8_LDB(B1, 0, 1); G8_STAGE(G8_SB(0, 0), b2, voffB);
;             G8_BAR; G8_WAIT_L(0); G8_MMA(0, 1, At, B1); G8_BAR;
;             G8_LDA(At, 0, 1); G8_STAGE(G8_SA(0, 0), a2, oc[0]);
;             G8_BAR; G8_WAIT_L(0); G8_MMA(1, 0, At, B0); G8_BAR; G8_SCHED;
;             G8_STAGE(G8_SB(0, 1), b2 + hstep, voffB);
;             G8_WAIT_V(6); G8_BAR; G8_MMA(1, 1, At, B1); G8_BAR;
.LBB0_320:
	s_add_u32 s36, s2, 0x100
	s_addc_u32 s37, s3, 0
	s_add_i32 s82, 0, 0x10000
	v_add_u32_e32 v0, s82, v145
	ds_read_b128 v[154:157], v0
	ds_read_b128 v[158:161], v0 offset:1024
	ds_read_b128 v[162:165], v0 offset:2048
	ds_read_b128 v[166:169], v0 offset:3072
	s_cmp_eq_u32 s11, 12
	s_cselect_b32 s49, s43, s37
	s_cselect_b32 s48, s42, s36
	s_cselect_b32 s47, s45, s9
	s_cselect_b32 s46, s44, s5
	v_lshl_add_u64 v[150:151], s[2:3], 0, v[148:149]
	s_add_i32 m0, s58, 0xc000
	ds_read_b128 v[170:173], v153
	ds_read_b128 v[174:177], v153 offset:1024
	ds_read_b128 v[178:181], v153 offset:2048
	ds_read_b128 v[182:185], v153 offset:3072
	ds_read_b128 v[186:189], v153 offset:4096
	ds_read_b128 v[190:193], v153 offset:5120
	ds_read_b128 v[194:197], v153 offset:6144
	ds_read_b128 v[198:201], v153 offset:7168
	global_load_lds_dwordx4 v[150:151], off
	v_lshl_add_u64 v[150:151], s[2:3], 0, v[146:147]
	s_add_i32 m0, s58, 0xe000
	s_nop 0
	global_load_lds_dwordx4 v[150:151], off
	s_waitcnt lgkmcnt(8)
	s_barrier
	s_waitcnt lgkmcnt(0)
	s_nop 0
	s_waitcnt lgkmcnt(0)
	v_mfma_f32_16x16x32_bf16 v[126:129], v[154:157], v[170:173], v[126:129]
	v_mfma_f32_16x16x32_bf16 v[122:125], v[162:165], v[170:173], v[122:125]
	v_mfma_f32_16x16x32_bf16 v[110:113], v[154:157], v[178:181], v[110:113]
	v_mfma_f32_16x16x32_bf16 v[106:109], v[162:165], v[178:181], v[106:109]
	v_mfma_f32_16x16x32_bf16 v[94:97], v[154:157], v[186:189], v[94:97]
	v_mfma_f32_16x16x32_bf16 v[90:93], v[162:165], v[186:189], v[90:93]
	v_mfma_f32_16x16x32_bf16 v[78:81], v[154:157], v[194:197], v[78:81]
	v_mfma_f32_16x16x32_bf16 v[74:77], v[162:165], v[194:197], v[74:77]
	v_mfma_f32_16x16x32_bf16 v[126:129], v[158:161], v[174:177], v[126:129]
	v_mfma_f32_16x16x32_bf16 v[122:125], v[166:169], v[174:177], v[122:125]
	v_mfma_f32_16x16x32_bf16 v[110:113], v[158:161], v[182:185], v[110:113]
	v_mfma_f32_16x16x32_bf16 v[106:109], v[166:169], v[182:185], v[106:109]
	v_mfma_f32_16x16x32_bf16 v[94:97], v[158:161], v[190:193], v[94:97]
	v_mfma_f32_16x16x32_bf16 v[90:93], v[166:169], v[190:193], v[90:93]
	v_mfma_f32_16x16x32_bf16 v[78:81], v[158:161], v[198:201], v[78:81]
	v_mfma_f32_16x16x32_bf16 v[74:77], v[166:169], v[198:201], v[74:77]
	s_nop 0
	s_barrier
	s_add_i32 s83, 0, 0x14000
	s_add_i32 s2, s82, s57
	v_add_u32_e32 v0, s83, v145
	v_lshl_add_u64 v[150:151], s[46:47], 0, v[132:133]
	s_mov_b32 m0, s2
	ds_read_b128 v[216:219], v0
	ds_read_b128 v[220:223], v0 offset:1024
	ds_read_b128 v[224:227], v0 offset:2048
	ds_read_b128 v[228:231], v0 offset:3072
	global_load_lds_dwordx4 v[150:151], off
	v_lshl_add_u64 v[232:233], s[46:47], 0, v[134:135]
	s_add_i32 m0, s2, 0x2000
	s_nop 0
	global_load_lds_dwordx4 v[232:233], off
	s_barrier
	s_waitcnt lgkmcnt(0)
	s_nop 0
	s_waitcnt lgkmcnt(0)
	v_mfma_f32_16x16x32_bf16 v[118:121], v[216:219], v[170:173], v[118:121]
	v_mfma_f32_16x16x32_bf16 v[114:117], v[224:227], v[170:173], v[114:117]
	v_mfma_f32_16x16x32_bf16 v[102:105], v[216:219], v[178:181], v[102:105]
	v_mfma_f32_16x16x32_bf16 v[98:101], v[224:227], v[178:181], v[98:101]
	v_mfma_f32_16x16x32_bf16 v[86:89], v[216:219], v[186:189], v[86:89]
	v_mfma_f32_16x16x32_bf16 v[82:85], v[224:227], v[186:189], v[82:85]
	v_mfma_f32_16x16x32_bf16 v[70:73], v[216:219], v[194:197], v[70:73]
	v_mfma_f32_16x16x32_bf16 v[66:69], v[224:227], v[194:197], v[66:69]
	v_mfma_f32_16x16x32_bf16 v[118:121], v[220:223], v[174:177], v[118:121]
	v_mfma_f32_16x16x32_bf16 v[114:117], v[228:231], v[174:177], v[114:117]
	v_mfma_f32_16x16x32_bf16 v[102:105], v[220:223], v[182:185], v[102:105]
	v_mfma_f32_16x16x32_bf16 v[98:101], v[228:231], v[182:185], v[98:101]
	v_mfma_f32_16x16x32_bf16 v[86:89], v[220:223], v[190:193], v[86:89]
	v_mfma_f32_16x16x32_bf16 v[82:85], v[228:231], v[190:193], v[82:85]
	v_mfma_f32_16x16x32_bf16 v[70:73], v[220:223], v[198:201], v[70:73]
	v_mfma_f32_16x16x32_bf16 v[66:69], v[228:231], v[198:201], v[66:69]
	s_nop 0
	s_mov_b32 m0, s58
	v_lshl_add_u64 v[234:235], s[48:49], 0, v[136:137]
	s_barrier
	ds_read_b128 v[170:173], v153 offset:16384
	ds_read_b128 v[174:177], v153 offset:17408
	ds_read_b128 v[178:181], v153 offset:18432
	ds_read_b128 v[182:185], v153 offset:19456
	ds_read_b128 v[186:189], v153 offset:20480
	ds_read_b128 v[190:193], v153 offset:21504
	ds_read_b128 v[194:197], v153 offset:22528
	ds_read_b128 v[198:201], v153 offset:23552
	global_load_lds_dwordx4 v[234:235], off
	v_lshl_add_u64 v[236:237], s[48:49], 0, v[140:141]
	s_mov_b32 m0, s59
	s_nop 0
	global_load_lds_dwordx4 v[236:237], off
	s_barrier
	s_waitcnt lgkmcnt(0)
	s_nop 0
	s_waitcnt lgkmcnt(0)
	v_mfma_f32_16x16x32_bf16 v[62:65], v[154:157], v[170:173], v[62:65]
	v_mfma_f32_16x16x32_bf16 v[58:61], v[162:165], v[170:173], v[58:61]
	v_mfma_f32_16x16x32_bf16 v[46:49], v[154:157], v[178:181], v[46:49]
	v_mfma_f32_16x16x32_bf16 v[42:45], v[162:165], v[178:181], v[42:45]
	v_mfma_f32_16x16x32_bf16 v[30:33], v[154:157], v[186:189], v[30:33]
	v_mfma_f32_16x16x32_bf16 v[26:29], v[162:165], v[186:189], v[26:29]
	v_mfma_f32_16x16x32_bf16 v[14:17], v[154:157], v[194:197], v[14:17]
	v_mfma_f32_16x16x32_bf16 v[10:13], v[162:165], v[194:197], v[10:13]
	v_mfma_f32_16x16x32_bf16 v[62:65], v[158:161], v[174:177], v[62:65]
	v_mfma_f32_16x16x32_bf16 v[58:61], v[166:169], v[174:177], v[58:61]
	v_mfma_f32_16x16x32_bf16 v[46:49], v[158:161], v[182:185], v[46:49]
	v_mfma_f32_16x16x32_bf16 v[42:45], v[166:169], v[182:185], v[42:45]
	v_mfma_f32_16x16x32_bf16 v[30:33], v[158:161], v[190:193], v[30:33]
	v_mfma_f32_16x16x32_bf16 v[26:29], v[166:169], v[190:193], v[26:29]
	v_mfma_f32_16x16x32_bf16 v[14:17], v[158:161], v[198:201], v[14:17]
	v_mfma_f32_16x16x32_bf16 v[10:13], v[166:169], v[198:201], v[10:13]
	s_nop 0
	s_barrier
; #define G8_STAGE(bufoff, gbase, voff) do { _Pragma("unroll") for (int _i = 0; _i < 2; ++_i) \
;         __builtin_amdgcn_global_load_lds((const unsigned*)((const char*)(gbase) + (voff)[_i]), (LAS unsigned*)(lds + (bufoff) + ldsw + _i * 8192), 16, 0, 0); } while (0)
; #define G8_LDA(dst, b, h) do { _Pragma("unroll") for (int m = 0; m < 4; ++m) _Pragma("unroll") for (int k = 0; k < 2; ++k) dst[m][k] = *(const LAS bf16x8*)(lds + G8_SA(b, h) + aoff + m * 2048 + k * 1024); } while (0)
; #define G8_LDB(dst, b, h) do { _Pragma("unroll") for (int n = 0; n < 2; ++n) _Pragma("unroll") for (int k = 0; k < 2; ++k) dst[n][k] = *(const LAS bf16x8*)(lds + G8_SB(b, h) + boff + n * 2048 + k * 1024); } while (0)
; #define G8_MMA(ai, bj, At, Bt) do { __builtin_amdgcn_s_setprio(1); _Pragma("unroll") for (int m = 0; m < 4; ++m) _Pragma("unroll") for (int n = 0; n < 2; ++n) _Pragma("unroll") for (int k = 0; k < 2; ++k) \
;         acc[ai][bj][m][n] = __builtin_amdgcn_mfma_f32_16x16x32_bf16(Bt[n][k], At[m][k], acc[ai][bj][m][n], 0, 0, 0); __builtin_amdgcn_s_setprio(0); } while (0)
; #define G8_WAIT_V(n) asm volatile("s_waitcnt vmcnt(" #n ")" ::: "memory")
; #define G8_WAIT_L(n) asm volatile("s_waitcnt lgkmcnt(" #n ")" ::: "memory")
; #define G8_BAR __builtin_amdgcn_s_barrier()
; #define G8_SCHED __builtin_amdgcn_sched_barrier(0)
; template <class Epi, class Sched>
; __device__ __forceinline__ void gemm_phase(LAS unsigned char* lds, const int K, const Sched& S, const Epi& E) {
;     ...
;             G8_STAGE(G8_SB(0, 1), b2 + hstep, voffB);
;             G8_WAIT_V(6); G8_BAR; G8_MMA(1, 1, At, B1); G8_BAR;
;             G8_LDB(B0, 1, 0); G8_SCHED; G8_LDA(At, 1, 0); G8_STAGE(G8_SA(0, 1), a2, oc[1]);
;             G8_WAIT_L(8); G8_BAR; G8_WAIT_L(0); G8_MMA(0, 0, At, B0); G8_BAR; G8_SCHED;
;             G8_LDB(B1, 1, 1); G8_STAGE(G8_SB(1, 0), b3, voffB);
;             G8_BAR; G8_WAIT_L(0); G8_MMA(0, 1, At, B1); G8_BAR;
;             G8_LDA(At, 1, 1); G8_STAGE(G8_SA(1, 0), a3, oc[0]);
	s_add_u32 s2, s46, 0x40000
	s_addc_u32 s3, s47, 0
	s_add_i32 s82, s83, s57
	v_lshl_add_u64 v[154:155], s[2:3], 0, v[132:133]
	s_mov_b32 m0, s82
	s_nop 0
	global_load_lds_dwordx4 v[154:155], off
	v_lshl_add_u64 v[154:155], s[2:3], 0, v[134:135]
	s_add_i32 m0, s82, 0x2000
	s_nop 0
	global_load_lds_dwordx4 v[154:155], off
	s_waitcnt vmcnt(6)
	s_barrier
	s_nop 0
	v_mfma_f32_16x16x32_bf16 v[54:57], v[216:219], v[170:173], v[54:57]
	v_mfma_f32_16x16x32_bf16 v[50:53], v[224:227], v[170:173], v[50:53]
	v_mfma_f32_16x16x32_bf16 v[38:41], v[216:219], v[178:181], v[38:41]
	v_mfma_f32_16x16x32_bf16 v[34:37], v[224:227], v[178:181], v[34:37]
	v_mfma_f32_16x16x32_bf16 v[22:25], v[216:219], v[186:189], v[22:25]
	v_mfma_f32_16x16x32_bf16 v[18:21], v[224:227], v[186:189], v[18:21]
	v_mfma_f32_16x16x32_bf16 v[6:9], v[216:219], v[194:197], v[6:9]
	v_mfma_f32_16x16x32_bf16 v[2:5], v[224:227], v[194:197], v[2:5]
	v_mfma_f32_16x16x32_bf16 v[54:57], v[220:223], v[174:177], v[54:57]
	v_mfma_f32_16x16x32_bf16 v[50:53], v[228:231], v[174:177], v[50:53]
	v_mfma_f32_16x16x32_bf16 v[38:41], v[220:223], v[182:185], v[38:41]
	v_mfma_f32_16x16x32_bf16 v[34:37], v[228:231], v[182:185], v[34:37]
	v_mfma_f32_16x16x32_bf16 v[22:25], v[220:223], v[190:193], v[22:25]
	v_mfma_f32_16x16x32_bf16 v[18:21], v[228:231], v[190:193], v[18:21]
	v_mfma_f32_16x16x32_bf16 v[6:9], v[220:223], v[198:201], v[6:9]
	v_mfma_f32_16x16x32_bf16 v[2:5], v[228:231], v[198:201], v[2:5]
	s_nop 0
	s_add_i32 s2, 0, 0x18000
	v_add_u32_e32 v0, s2, v145
	s_barrier
	ds_read_b128 v[154:157], v0
	ds_read_b128 v[158:161], v0 offset:1024
	ds_read_b128 v[162:165], v0 offset:2048
	ds_read_b128 v[166:169], v0 offset:3072
	s_mov_b32 m0, s60
	v_lshl_add_u64 v[216:217], s[48:49], 0, v[138:139]
	ds_read_b128 v[170:173], v153 offset:32768
	ds_read_b128 v[174:177], v153 offset:33792
	ds_read_b128 v[178:181], v153 offset:34816
	ds_read_b128 v[182:185], v153 offset:35840
	ds_read_b128 v[186:189], v153 offset:36864
	ds_read_b128 v[190:193], v153 offset:37888
	ds_read_b128 v[194:197], v153 offset:38912
	ds_read_b128 v[198:201], v153 offset:39936
	global_load_lds_dwordx4 v[216:217], off
	v_lshl_add_u64 v[216:217], s[48:49], 0, v[142:143]
	s_mov_b32 m0, s61
	s_nop 0
	global_load_lds_dwordx4 v[216:217], off
	s_waitcnt lgkmcnt(8)
	s_barrier
	s_waitcnt lgkmcnt(0)
	s_nop 0
	s_waitcnt lgkmcnt(0)
	v_mfma_f32_16x16x32_bf16 v[126:129], v[154:157], v[170:173], v[126:129]
	v_mfma_f32_16x16x32_bf16 v[122:125], v[162:165], v[170:173], v[122:125]
	v_mfma_f32_16x16x32_bf16 v[110:113], v[154:157], v[178:181], v[110:113]
	v_mfma_f32_16x16x32_bf16 v[106:109], v[162:165], v[178:181], v[106:109]
	v_mfma_f32_16x16x32_bf16 v[94:97], v[154:157], v[186:189], v[94:97]
	v_mfma_f32_16x16x32_bf16 v[90:93], v[162:165], v[186:189], v[90:93]
	v_mfma_f32_16x16x32_bf16 v[78:81], v[154:157], v[194:197], v[78:81]
	v_mfma_f32_16x16x32_bf16 v[74:77], v[162:165], v[194:197], v[74:77]
	v_mfma_f32_16x16x32_bf16 v[126:129], v[158:161], v[174:177], v[126:129]
	v_mfma_f32_16x16x32_bf16 v[122:125], v[166:169], v[174:177], v[122:125]
	v_mfma_f32_16x16x32_bf16 v[110:113], v[158:161], v[182:185], v[110:113]
	v_mfma_f32_16x16x32_bf16 v[106:109], v[166:169], v[182:185], v[106:109]
	v_mfma_f32_16x16x32_bf16 v[94:97], v[158:161], v[190:193], v[94:97]
	v_mfma_f32_16x16x32_bf16 v[90:93], v[166:169], v[190:193], v[90:93]
	v_mfma_f32_16x16x32_bf16 v[78:81], v[158:161], v[198:201], v[78:81]
	v_mfma_f32_16x16x32_bf16 v[74:77], v[166:169], v[198:201], v[74:77]
	s_nop 0
	s_barrier
	s_add_i32 s48, 0, 0x1c000
	s_add_i32 s2, s2, s57
	v_add_u32_e32 v0, s48, v145
	v_lshl_add_u64 v[150:151], v[150:151], 0, s[18:19]
	s_mov_b32 m0, s2
	ds_read_b128 v[216:219], v0
	ds_read_b128 v[220:223], v0 offset:1024
	ds_read_b128 v[224:227], v0 offset:2048
	ds_read_b128 v[228:231], v0 offset:3072
	global_load_lds_dwordx4 v[150:151], off
	v_lshl_add_u64 v[150:151], v[232:233], 0, s[18:19]
	s_add_i32 m0, s2, 0x2000
	s_nop 0
	global_load_lds_dwordx4 v[150:151], off
	s_barrier
	s_waitcnt lgkmcnt(0)
	s_nop 0
	s_waitcnt lgkmcnt(0)
	v_mfma_f32_16x16x32_bf16 v[118:121], v[216:219], v[170:173], v[118:121]
	v_mfma_f32_16x16x32_bf16 v[114:117], v[224:227], v[170:173], v[114:117]
	v_mfma_f32_16x16x32_bf16 v[102:105], v[216:219], v[178:181], v[102:105]
	v_mfma_f32_16x16x32_bf16 v[98:101], v[224:227], v[178:181], v[98:101]
	v_mfma_f32_16x16x32_bf16 v[86:89], v[216:219], v[186:189], v[86:89]
	v_mfma_f32_16x16x32_bf16 v[82:85], v[224:227], v[186:189], v[82:85]
	v_mfma_f32_16x16x32_bf16 v[70:73], v[216:219], v[194:197], v[70:73]
	v_mfma_f32_16x16x32_bf16 v[66:69], v[224:227], v[194:197], v[66:69]
	v_mfma_f32_16x16x32_bf16 v[118:121], v[220:223], v[174:177], v[118:121]
	v_mfma_f32_16x16x32_bf16 v[114:117], v[228:231], v[174:177], v[114:117]
	v_mfma_f32_16x16x32_bf16 v[102:105], v[220:223], v[182:185], v[102:105]
	v_mfma_f32_16x16x32_bf16 v[98:101], v[228:231], v[182:185], v[98:101]
	v_mfma_f32_16x16x32_bf16 v[86:89], v[220:223], v[190:193], v[86:89]
	v_mfma_f32_16x16x32_bf16 v[82:85], v[228:231], v[190:193], v[82:85]
	v_mfma_f32_16x16x32_bf16 v[70:73], v[220:223], v[198:201], v[70:73]
	v_mfma_f32_16x16x32_bf16 v[66:69], v[228:231], v[198:201], v[66:69]
	s_nop 0
	s_mov_b32 m0, s64
	v_lshl_add_u64 v[150:151], v[234:235], 0, s[18:19]
	s_barrier
; #define G8_STAGE(bufoff, gbase, voff) do { _Pragma("unroll") for (int _i = 0; _i < 2; ++_i) \
;         __builtin_amdgcn_global_load_lds((const unsigned*)((const char*)(gbase) + (voff)[_i]), (LAS unsigned*)(lds + (bufoff) + ldsw + _i * 8192), 16, 0, 0); } while (0)
; #define G8_LDA(dst, b, h) do { _Pragma("unroll") for (int m = 0; m < 4; ++m) _Pragma("unroll") for (int k = 0; k < 2; ++k) dst[m][k] = *(const LAS bf16x8*)(lds + G8_SA(b, h) + aoff + m * 2048 + k * 1024); } while (0)
; #define G8_MMA(ai, bj, At, Bt) do { __builtin_amdgcn_s_setprio(1); _Pragma("unroll") for (int m = 0; m < 4; ++m) _Pragma("unroll") for (int n = 0; n < 2; ++n) _Pragma("unroll") for (int k = 0; k < 2; ++k) \
;         acc[ai][bj][m][n] = __builtin_amdgcn_mfma_f32_16x16x32_bf16(Bt[n][k], At[m][k], acc[ai][bj][m][n], 0, 0, 0); __builtin_amdgcn_s_setprio(0); } while (0)
; #define G8_WAIT_V(n) asm volatile("s_waitcnt vmcnt(" #n ")" ::: "memory")
; #define G8_WAIT_L(n) asm volatile("s_waitcnt lgkmcnt(" #n ")" ::: "memory")
; template <class Epi, class Sched>
; __device__ __forceinline__ void gemm_phase(LAS unsigned char* lds, const int K, const Sched& S, const Epi& E) {
;     ...
;             G8_LDA(At, 1, 1); G8_STAGE(G8_SA(1, 0), a3, oc[0]);
;             G8_BAR; G8_WAIT_L(0); G8_MMA(1, 0, At, B0); G8_BAR; G8_SCHED;
;             G8_STAGE(G8_SB(1, 1), b3 + hstep, voffB);
;             G8_WAIT_V(6); G8_BAR; G8_MMA(1, 1, At, B1); G8_BAR;
;     __device__ __forceinline__ void operator()(const f32x4 (&acc)[2][2][4][2], const g8::Unit& u, int wr, int wc, int fr, int fq) const {
;         const int pn = u.pn; const int col0 = pn * 256 + wc * 32 + fq * 8;
;         bf16_t* gu = (bf16_t*)(ws + CD_GU); bf16_t* gvT = (bf16_t*)(ws + CD_GVT); bf16_t* gg = (bf16_t*)(ws + CD_GG); bf16_t* xr = (bf16_t*)(ws + CD_XR); float* stats = (float*)(ws + CD_STATS);
; #pragma unroll
;         for (int ai = 0; ai < 2; ++ai)
; #pragma unroll
;             for (int m = 0; m < 4; ++m) {
;                 const int t = u.pm * 256 + ai * 128 + wr * 64 + m * 16 + fr, sq = t & (SEQ - 1), b = t >> 13;
;                 f32x4 x[2][2];
; #pragma unroll
;                 for (int bj = 0; bj < 2; ++bj)
; #pragma unroll
;                     for (int n = 0; n < 2; ++n) { x[bj][n] = acc[ai][bj][m][n];
;                         if (pn < 13) {
;                             x[bj][n] = gelu4(x[bj][n]); } }
	ds_read_b128 v[170:173], v153 offset:49152
	ds_read_b128 v[174:177], v153 offset:50176
	ds_read_b128 v[178:181], v153 offset:51200
	ds_read_b128 v[182:185], v153 offset:52224
	ds_read_b128 v[186:189], v153 offset:53248
	ds_read_b128 v[190:193], v153 offset:54272
	ds_read_b128 v[194:197], v153 offset:55296
	ds_read_b128 v[198:201], v153 offset:56320
	global_load_lds_dwordx4 v[150:151], off
	v_lshl_add_u64 v[150:151], v[236:237], 0, s[18:19]
	s_mov_b32 m0, s65
	s_nop 0
	global_load_lds_dwordx4 v[150:151], off
	s_barrier
	s_waitcnt lgkmcnt(0)
	s_nop 0
	s_waitcnt lgkmcnt(0)
	v_mfma_f32_16x16x32_bf16 v[62:65], v[154:157], v[170:173], v[62:65]
	v_mfma_f32_16x16x32_bf16 v[58:61], v[162:165], v[170:173], v[58:61]
	v_mfma_f32_16x16x32_bf16 v[46:49], v[154:157], v[178:181], v[46:49]
	v_mfma_f32_16x16x32_bf16 v[42:45], v[162:165], v[178:181], v[42:45]
	v_mfma_f32_16x16x32_bf16 v[30:33], v[154:157], v[186:189], v[30:33]
	v_mfma_f32_16x16x32_bf16 v[26:29], v[162:165], v[186:189], v[26:29]
	v_mfma_f32_16x16x32_bf16 v[14:17], v[154:157], v[194:197], v[14:17]
	v_mfma_f32_16x16x32_bf16 v[10:13], v[162:165], v[194:197], v[10:13]
	v_mfma_f32_16x16x32_bf16 v[62:65], v[158:161], v[174:177], v[62:65]
	v_mfma_f32_16x16x32_bf16 v[58:61], v[166:169], v[174:177], v[58:61]
	v_mfma_f32_16x16x32_bf16 v[46:49], v[158:161], v[182:185], v[46:49]
	v_mfma_f32_16x16x32_bf16 v[42:45], v[166:169], v[182:185], v[42:45]
	v_mfma_f32_16x16x32_bf16 v[30:33], v[158:161], v[190:193], v[30:33]
	v_mfma_f32_16x16x32_bf16 v[26:29], v[166:169], v[190:193], v[26:29]
	v_mfma_f32_16x16x32_bf16 v[14:17], v[158:161], v[198:201], v[14:17]
	v_mfma_f32_16x16x32_bf16 v[10:13], v[166:169], v[198:201], v[10:13]
	s_nop 0
	s_barrier
	s_add_u32 s2, s46, 0x40080
	s_addc_u32 s3, s47, 0
	s_add_i32 s46, s48, s57
	v_lshl_add_u64 v[150:151], s[2:3], 0, v[132:133]
	s_mov_b32 m0, s46
	s_nop 0
	global_load_lds_dwordx4 v[150:151], off
	v_lshl_add_u64 v[150:151], s[2:3], 0, v[134:135]
	s_add_i32 m0, s46, 0x2000
	s_nop 0
	global_load_lds_dwordx4 v[150:151], off
	s_waitcnt vmcnt(6)
	s_barrier
	s_nop 0
	v_mfma_f32_16x16x32_bf16 v[54:57], v[216:219], v[170:173], v[54:57]
	v_mfma_f32_16x16x32_bf16 v[50:53], v[224:227], v[170:173], v[50:53]
	v_mfma_f32_16x16x32_bf16 v[38:41], v[216:219], v[178:181], v[38:41]
	v_mfma_f32_16x16x32_bf16 v[34:37], v[224:227], v[178:181], v[34:37]
	v_mfma_f32_16x16x32_bf16 v[22:25], v[216:219], v[186:189], v[22:25]
	v_mfma_f32_16x16x32_bf16 v[18:21], v[224:227], v[186:189], v[18:21]
	v_mfma_f32_16x16x32_bf16 v[6:9], v[216:219], v[194:197], v[6:9]
	v_mfma_f32_16x16x32_bf16 v[2:5], v[224:227], v[194:197], v[2:5]
	v_mfma_f32_16x16x32_bf16 v[54:57], v[220:223], v[174:177], v[54:57]
	v_mfma_f32_16x16x32_bf16 v[50:53], v[228:231], v[174:177], v[50:53]
	v_mfma_f32_16x16x32_bf16 v[38:41], v[220:223], v[182:185], v[38:41]
	v_mfma_f32_16x16x32_bf16 v[34:37], v[228:231], v[182:185], v[34:37]
	v_mfma_f32_16x16x32_bf16 v[22:25], v[220:223], v[190:193], v[22:25]
	v_mfma_f32_16x16x32_bf16 v[18:21], v[228:231], v[190:193], v[18:21]
	v_mfma_f32_16x16x32_bf16 v[6:9], v[220:223], v[198:201], v[6:9]
	v_mfma_f32_16x16x32_bf16 v[2:5], v[228:231], v[198:201], v[2:5]
	s_nop 0
	s_add_i32 s11, s11, 2
	s_add_u32 s5, s5, 0x100
	s_addc_u32 s9, s9, 0
	s_cmp_gt_u32 s11, 13
	s_mov_b64 s[2:3], s[36:37]
	s_barrier
	s_cbranch_scc0 .LBB0_320
	s_nop 0
	s_nop 0
	s_nop 0
	s_nop 0
	s_nop 0
	s_nop 0
	s_nop 0
	s_nop 0
	s_nop 0
	s_nop 0
	s_nop 0
	s_cmp_lt_i32 s14, 13
	s_cselect_b64 s[36:37], -1, 0
	s_and_b64 vcc, exec, s[36:37]
	s_cbranch_vccz .LBB0_325
	v_pk_mul_f32 v[154:155], v[126:127], v[126:127]
	v_pk_mul_f32 v[150:151], v[128:129], v[128:129]
	v_fmamk_f32 v0, v154, 0xbdd2d3e8, v202
	v_mul_f32_e32 v0, v126, v0
	v_exp_f32_e32 v154, v0
	v_fmamk_f32 v0, v155, 0xbdd2d3e8, v202
	v_mul_f32_e32 v0, v127, v0
	v_exp_f32_e32 v155, v0
	v_fmamk_f32 v0, v150, 0xbdd2d3e8, v202
	v_mul_f32_e32 v0, v128, v0
	v_exp_f32_e32 v150, v0
	v_fmamk_f32 v0, v151, 0xbdd2d3e8, v202
	v_mul_f32_e32 v0, v129, v0
	v_exp_f32_e32 v151, v0
	v_pk_add_f32 v[154:155], v[154:155], 1.0 op_sel_hi:[1,0]
	v_pk_add_f32 v[150:151], v[150:151], 1.0 op_sel_hi:[1,0]
	v_rcp_f32_e32 v154, v154
	v_rcp_f32_e32 v155, v155
	v_rcp_f32_e32 v150, v150
	v_rcp_f32_e32 v151, v151
	v_pk_mul_f32 v[126:127], v[126:127], v[154:155]
	v_pk_mul_f32 v[128:129], v[128:129], v[150:151]
	v_cndmask_b32_e64 v0, 0, 1, s[36:37]
	v_cmp_ne_u32_e64 s[2:3], 1, v0
	s_andn2_b64 vcc, exec, s[36:37]
	s_cbranch_vccz .LBB0_326

; #define G8_WAIT_V(n) asm volatile("s_waitcnt vmcnt(" #n ")" ::: "memory")
; #define G8_BAR __builtin_amdgcn_s_barrier()
; template <class Epi, class Sched>
; __device__ __forceinline__ void gemm_phase(LAS unsigned char* lds, const int K, const Sched& S, const Epi& E) {
;     ...
;     G8_WAIT_V(0);
;     if (wr == 0) G8_BAR;
;     G8_BAR;
.LBB0_437:
	s_barrier
	s_setprio 0
	s_nop 0
	s_nop 0
	s_nop 0
	s_nop 0
	s_nop 0
	s_nop 0
	s_nop 0
	s_nop 0
	s_nop 0
	s_nop 0
	s_nop 0
	s_nop 0
	s_nop 0
	s_nop 0
	s_nop 0
	s_add_i32 s0, s46, 1
	s_cmp_ge_i32 s0, s31
	s_mov_b64 s[24:25], 0
	s_cbranch_scc0 .LBB0_301

; #define LAS __attribute__((address_space(3)))
; #define G8_WAIT_V(n) asm volatile("s_waitcnt vmcnt(" #n ")" ::: "memory")
; #define G8_BAR __builtin_amdgcn_s_barrier()
; template <class Epi, class Sched>
; __device__ __forceinline__ void gemm_phase(LAS unsigned char* lds, const int K, const Sched& S, const Epi& E) {
;     int tid_ = S.tid0; asm volatile("" : "+v"(tid_));
;     const int tid = tid_, wid = __builtin_amdgcn_readfirstlane(tid >> 6), lane = tid & 63, wr = wid >> 2, wc = wid & 3, fr = lane & 15, fq = lane >> 4;
;     const int nt = K / BK;
;     unsigned voffB[2];
; #pragma unroll
;     for (int i = 0; i < 2; ++i) { int R, C; stage_rc(tid * 16 + i * 8192, R, C); const int Rb = Epi::PERM ? ((R & ~31) + perm32(R & 31)) : R;
;         voffB[i] = (unsigned)(Rb * K + C) * 2u; }
;     const size_t kstep = (size_t)(BK * 2);
;     const size_t hstep = (size_t)HALF * K * 2;
;     const unsigned ldsw = (unsigned)wid * 1024u;
;     const int aoff = lds_byte(wr * 64 + fr, fq * 8), boff = lds_byte(wc * 32 + fr, fq * 8);
;     ...
;     Unit cur, nxt; int ui = 0;
;     if (!S.next(0, cur)) return;
;     f32x4 acc[2][2][4][2];
;     E.init(acc, cur, wc, fq);
;     bf16x8 At[4][2], B0[2][2], B1[2][2];
;     unsigned oc[2][2];
;     S.aoff(cur, tid, oc);
;     const char* cA = cur.A; const char* cB = cur.B;
;     G8_STAGE(G8_SB(0, 0), cB, voffB); G8_STAGE(G8_SA(0, 0), cA, oc[0]); G8_STAGE(G8_SB(0, 1), cB + hstep, voffB); G8_STAGE(G8_SA(0, 1), cA, oc[1]);
;     if (wr == 1) G8_BAR;
;     G8_WAIT_V(4); G8_BAR;
;     G8_STAGE(G8_SB(1, 0), cB + kstep, voffB); G8_STAGE(G8_SA(1, 0), cA + kstep, oc[0]); G8_STAGE(G8_SB(1, 1), cB + hstep + kstep, voffB);
;     G8_WAIT_V(6); G8_BAR;
;     __device__ __forceinline__ void init(f32x4 (&acc)[2][2][4][2], const g8::Unit& u, int wc, int fq) const {
;         const int colp = u.pn * 256 + wc * 32 + fq * 8;
; #pragma unroll
;         for (int b = 0; b < 2; ++b)
; #pragma unroll
;             for (int n = 0; n < 2; ++n) { const u32x2 bw = *(const LAS u32x2*)(biasL + colp + b * 128 + 4 * n);
;                 const f32x4 bv = (f32x4){__uint_as_float(bw[0] << 16), __uint_as_float(bw[0] & 0xffff0000u), __uint_as_float(bw[1] << 16), __uint_as_float(bw[1] & 0xffff0000u)};
; #pragma unroll
;                 for (int a = 0; a < 2; ++a)
; #pragma unroll
;                     for (int m = 0; m < 4; ++m) acc[a][b][m][n] = bv; } }
.LBB0_480:
	v_ashrrev_i32_e32 v0, 31, v18
	v_lshrrev_b32_e32 v0, 26, v0
	v_add_u32_e32 v0, v18, v0
	v_ashrrev_i32_e32 v19, 6, v0
	v_bfe_i32 v0, v18, 27, 1
	v_lshlrev_b32_e32 v2, 4, v18
	v_lshrrev_b32_e32 v0, 22, v0
	v_add_u32_e32 v0, v2, v0
	v_and_b32_e32 v0, 0xfffffc00, v0
	v_sub_u32_e32 v0, v2, v0
	v_lshrrev_b32_e32 v3, 4, v0
	v_bitop3_b32 v0, v3, v0, 32 bitop3:0x6c
	v_ashrrev_i32_e32 v4, 31, v0
	v_lshrrev_b32_e32 v4, 26, v4
	v_lshlrev_b32_e32 v3, 3, v19
	v_add_u32_e32 v4, v0, v4
	v_and_b32_e32 v3, -16, v3
	v_ashrrev_i32_e32 v20, 6, v4
	v_add_u32_e32 v10, v20, v3
	v_lshlrev_b32_e32 v3, 5, v19
	v_and_b32_e32 v21, 32, v3
	v_and_b32_e32 v3, 0xc0, v4
	v_sub_u32_e32 v0, v0, v3
	v_ashrrev_i16_sdwa v22, v203, sext(v0) dst_sel:DWORD dst_unused:UNUSED_PAD src0_sel:DWORD src1_sel:BYTE_0
	v_lshlrev_b32_e32 v0, 1, v10
	v_lshrrev_b32_e32 v3, 2, v10
	v_and_b32_e32 v4, 3, v20
	s_mov_b32 s4, 0x1fffe0
	v_and_b32_e32 v0, 24, v0
	v_and_b32_e32 v3, 4, v3
	v_and_or_b32 v4, v10, s4, v4
	v_add_u32_e32 v2, 0x2000, v2
	v_or3_b32 v0, v4, v3, v0
	v_ashrrev_i32_e32 v3, 31, v2
	v_lshrrev_b32_e32 v3, 22, v3
	v_add_u32_e32 v3, v2, v3
	v_ashrrev_i32_e32 v23, 10, v3
	v_mul_i32_i24_e32 v3, 0x400, v23
	v_sub_u32_e32 v2, v2, v3
	v_lshrrev_b32_e32 v3, 4, v2
	v_bitop3_b32 v2, v3, v2, 32 bitop3:0x6c
	v_ashrrev_i32_e32 v4, 31, v2
	v_lshrrev_b32_e32 v4, 26, v4
	v_lshlrev_b32_e32 v3, 3, v23
	v_add_u32_e32 v4, v2, v4
	v_and_b32_e32 v3, -16, v3
	v_ashrrev_i32_e32 v24, 6, v4
	v_add_u32_e32 v13, v24, v3
	v_lshlrev_b32_e32 v3, 5, v23
	v_and_b32_e32 v25, 32, v3
	v_and_b32_e32 v3, 0xc0, v4
	s_ashr_i32 s5, s64, 6
	v_sub_u32_e32 v2, v2, v3
	s_and_b32 s3, s5, 3
	v_ashrrev_i16_sdwa v26, v203, sext(v2) dst_sel:DWORD dst_unused:UNUSED_PAD src0_sel:DWORD src1_sel:BYTE_0
	v_lshlrev_b32_e32 v2, 1, v13
	v_lshrrev_b32_e32 v3, 2, v13
	v_and_b32_e32 v4, 3, v24
	s_lshl_b32 s65, s5, 10
	s_lshl_b32 s5, s94, 9
	v_add_u32_sdwa v14, v25, sext(v26) dst_sel:DWORD dst_unused:UNUSED_PAD src0_sel:DWORD src1_sel:WORD_0
	v_and_b32_e32 v2, 24, v2
	v_and_b32_e32 v3, 4, v3
	v_and_or_b32 v4, v13, s4, v4
	v_bfe_u32 v139, v18, 4, 2
	s_lshl_b32 s75, s3, 6
	s_add_i32 s5, s5, 0
	v_add_u32_sdwa v11, v21, sext(v22) dst_sel:DWORD dst_unused:UNUSED_PAD src0_sel:DWORD src1_sel:WORD_0
	v_or3_b32 v2, v4, v3, v2
	v_lshlrev_b32_e32 v15, 1, v14
	v_lshlrev_b32_e32 v27, 4, v139
	s_add_i32 s5, s5, s75
	v_lshlrev_b32_e32 v12, 1, v11
	v_lshl_add_u32 v140, v2, 11, v15
	v_add_u32_e32 v2, s5, v27
	s_add_i32 s76, s65, 0
	v_lshl_add_u32 v0, v0, 11, v12
	v_add_u32_e32 v6, 0x20000, v2
	s_add_i32 m0, s76, 0x10000
	ds_read_b128 v[2:5], v6
	ds_read_b128 v[6:9], v6 offset:256
	global_load_lds_dwordx4 v0, s[12:13]
	s_add_i32 m0, s76, 0x12000
	s_ashr_i32 s4, s64, 8
	v_lshl_add_u32 v142, v10, 11, v12
	global_load_lds_dwordx4 v140, s[12:13]
	s_mov_b32 m0, s76
	s_add_i32 s77, s76, 0x2000
	v_lshl_add_u32 v146, v13, 11, v15
	global_load_lds_dwordx4 v142, s[0:1]
	s_mov_b32 m0, s77
	s_add_u32 s6, s12, 0x40000
	global_load_lds_dwordx4 v146, s[0:1]
	s_addc_u32 s7, s13, 0
	s_add_i32 m0, s76, 0x14000
	v_lshl_add_u32 v10, v10, 10, v11
	global_load_lds_dwordx4 v0, s[6:7]
	s_add_i32 m0, s76, 0x16000
	s_add_i32 s78, s76, 0x4000
	v_lshl_add_u32 v144, v10, 1, v206
	v_lshl_add_u32 v10, v13, 10, v14
	global_load_lds_dwordx4 v140, s[6:7]
	s_mov_b32 m0, s78
	s_add_i32 s79, s76, 0x6000
	v_lshl_add_u32 v148, v10, 1, v206
	global_load_lds_dwordx4 v144, s[0:1]
	s_mov_b32 m0, s79
	v_mov_b32_e32 v141, v1
	global_load_lds_dwordx4 v148, s[0:1]
	v_mov_b32_e32 v143, v1
	v_mov_b32_e32 v147, v1
	v_lshl_add_u64 v[16:17], s[12:13], 0, v[0:1]
	v_lshl_add_u64 v[14:15], s[12:13], 0, v[140:141]
	v_lshl_add_u64 v[12:13], s[0:1], 0, v[142:143]
	s_cmp_lg_u32 s4, 1
	v_lshl_add_u64 v[10:11], s[0:1], 0, v[146:147]
	s_cbranch_scc1 .LBB0_482
	s_barrier
	s_setprio 1
	s_nop 0
	s_nop 0
	s_nop 0
	s_nop 0
	s_nop 0
	s_nop 0
	s_nop 0
	s_nop 0
	s_nop 0
	s_nop 0
	s_nop 0
	s_nop 0
	s_nop 0
	s_nop 0
	s_nop 0

; #define G8_STAGE(bufoff, gbase, voff) do { _Pragma("unroll") for (int _i = 0; _i < 2; ++_i) \
;         __builtin_amdgcn_global_load_lds((const unsigned*)((const char*)(gbase) + (voff)[_i]), (LAS unsigned*)(lds + (bufoff) + ldsw + _i * 8192), 16, 0, 0); } while (0)
; #define G8_LDA(dst, b, h) do { _Pragma("unroll") for (int m = 0; m < 4; ++m) _Pragma("unroll") for (int k = 0; k < 2; ++k) dst[m][k] = *(const LAS bf16x8*)(lds + G8_SA(b, h) + aoff + m * 2048 + k * 1024); } while (0)
; #define G8_LDB(dst, b, h) do { _Pragma("unroll") for (int n = 0; n < 2; ++n) _Pragma("unroll") for (int k = 0; k < 2; ++k) dst[n][k] = *(const LAS bf16x8*)(lds + G8_SB(b, h) + boff + n * 2048 + k * 1024); } while (0)
; #define G8_MMA(ai, bj, At, Bt) do { __builtin_amdgcn_s_setprio(1); _Pragma("unroll") for (int m = 0; m < 4; ++m) _Pragma("unroll") for (int n = 0; n < 2; ++n) _Pragma("unroll") for (int k = 0; k < 2; ++k) \
;         acc[ai][bj][m][n] = __builtin_amdgcn_mfma_f32_16x16x32_bf16(Bt[n][k], At[m][k], acc[ai][bj][m][n], 0, 0, 0); __builtin_amdgcn_s_setprio(0); } while (0)
; #define G8_WAIT_L(n) asm volatile("s_waitcnt lgkmcnt(" #n ")" ::: "memory")
; #define G8_BAR __builtin_amdgcn_s_barrier()
; template <class Epi, class Sched>
; __device__ __forceinline__ void gemm_phase(LAS unsigned char* lds, const int K, const Sched& S, const Epi& E) {
;     ...
;         const bool has_next = S.next(ui + 1, nxt);
;         const char* nA = has_next ? nxt.A : cA; const char* nB = has_next ? nxt.B : cB;
; #pragma unroll 1
;         for (int t = 0; t < nt; t += 2) {
;             const bool last = (t == nt - 2);
;             const char* a1 = cA + (size_t)(t + 1) * kstep;
;             const char* a2 = last ? nA : cA + (size_t)(t + 2) * kstep; const char* b2 = last ? nB : cB + (size_t)(t + 2) * kstep;
;             const char* a3 = a2 + kstep; const char* b3 = b2 + kstep;
;             G8_LDB(B0, 0, 0); G8_SCHED; G8_LDA(At, 0, 0); G8_STAGE(G8_SA(1, 1), a1, oc[1]);
;             if (last && has_next) S.aoff(nxt, tid, oc);
;             G8_WAIT_L(8); G8_BAR; G8_WAIT_L(0); G8_MMA(0, 0, At, B0); G8_BAR; G8_SCHED;
;             G8_LDB(B1, 0, 1); G8_STAGE(G8_SB(0, 0), b2, voffB);
;             G8_BAR; G8_WAIT_L(0); G8_MMA(0, 1, At, B1); G8_BAR;
;             G8_LDA(At, 0, 1); G8_STAGE(G8_SA(0, 0), a2, oc[0]);
;             G8_BAR; G8_WAIT_L(0); G8_MMA(1, 0, At, B0); G8_BAR; G8_SCHED;
.LBB0_487:
	s_add_u32 s12, s0, 0x100
	s_addc_u32 s13, s1, 0
	s_add_i32 s49, 0, 0x10000
	v_add_u32_e32 v158, s49, v165
	ds_read_b128 v[130:133], v158
	ds_read_b128 v[134:137], v158 offset:1024
	ds_read_b128 v[154:157], v158 offset:2048
	ds_read_b128 v[158:161], v158 offset:3072
	s_cmp_eq_u32 s47, 12
	s_cselect_b32 s43, s23, s13
	s_cselect_b32 s42, s22, s12
	s_cselect_b32 s39, s37, s14
	s_cselect_b32 s38, s36, s3
	v_lshl_add_u64 v[162:163], s[0:1], 0, v[152:153]
	s_add_i32 m0, s76, 0xc000
	ds_read_b128 v[168:171], v167
	ds_read_b128 v[172:175], v167 offset:1024
	ds_read_b128 v[176:179], v167 offset:2048
	ds_read_b128 v[180:183], v167 offset:3072
	ds_read_b128 v[184:187], v167 offset:4096
	ds_read_b128 v[188:191], v167 offset:5120
	ds_read_b128 v[192:195], v167 offset:6144
	ds_read_b128 v[196:199], v167 offset:7168
	global_load_lds_dwordx4 v[162:163], off
	v_lshl_add_u64 v[162:163], s[0:1], 0, v[150:151]
	s_add_i32 m0, s76, 0xe000
	s_nop 0
	global_load_lds_dwordx4 v[162:163], off
	s_waitcnt lgkmcnt(8)
	s_barrier
	s_waitcnt lgkmcnt(0)
	s_nop 0
	s_waitcnt lgkmcnt(0)
	v_mfma_f32_16x16x32_bf16 v[126:129], v[130:133], v[168:171], v[126:129]
	v_mfma_f32_16x16x32_bf16 v[118:121], v[154:157], v[168:171], v[118:121]
	v_mfma_f32_16x16x32_bf16 v[110:113], v[130:133], v[176:179], v[110:113]
	v_mfma_f32_16x16x32_bf16 v[102:105], v[154:157], v[176:179], v[102:105]
	v_mfma_f32_16x16x32_bf16 v[94:97], v[130:133], v[184:187], v[94:97]
	v_mfma_f32_16x16x32_bf16 v[86:89], v[154:157], v[184:187], v[86:89]
	v_mfma_f32_16x16x32_bf16 v[78:81], v[130:133], v[192:195], v[78:81]
	v_mfma_f32_16x16x32_bf16 v[70:73], v[154:157], v[192:195], v[70:73]
	v_mfma_f32_16x16x32_bf16 v[126:129], v[134:137], v[172:175], v[126:129]
	v_mfma_f32_16x16x32_bf16 v[118:121], v[158:161], v[172:175], v[118:121]
	v_mfma_f32_16x16x32_bf16 v[110:113], v[134:137], v[180:183], v[110:113]
	v_mfma_f32_16x16x32_bf16 v[102:105], v[158:161], v[180:183], v[102:105]
	v_mfma_f32_16x16x32_bf16 v[94:97], v[134:137], v[188:191], v[94:97]
	v_mfma_f32_16x16x32_bf16 v[86:89], v[158:161], v[188:191], v[86:89]
	v_mfma_f32_16x16x32_bf16 v[78:81], v[134:137], v[196:199], v[78:81]
	v_mfma_f32_16x16x32_bf16 v[70:73], v[158:161], v[196:199], v[70:73]
	s_nop 0
	s_barrier
	s_add_i32 s54, 0, 0x14000
	v_add_u32_e32 v162, s54, v165
	s_add_i32 s0, s49, s65
	ds_read_b128 v[216:219], v162
	ds_read_b128 v[220:223], v162 offset:1024
	ds_read_b128 v[224:227], v162 offset:2048
	ds_read_b128 v[228:231], v162 offset:3072
	v_lshl_add_u64 v[162:163], s[38:39], 0, v[0:1]
	s_mov_b32 m0, s0
	v_lshl_add_u64 v[200:201], s[38:39], 0, v[140:141]
	global_load_lds_dwordx4 v[162:163], off
	s_add_i32 m0, s0, 0x2000
	s_nop 0
	global_load_lds_dwordx4 v[200:201], off
	s_barrier
	s_waitcnt lgkmcnt(0)
	s_nop 0
	s_waitcnt lgkmcnt(0)
	v_mfma_f32_16x16x32_bf16 v[122:125], v[216:219], v[168:171], v[122:125]
	v_mfma_f32_16x16x32_bf16 v[114:117], v[224:227], v[168:171], v[114:117]
	v_mfma_f32_16x16x32_bf16 v[106:109], v[216:219], v[176:179], v[106:109]
	v_mfma_f32_16x16x32_bf16 v[98:101], v[224:227], v[176:179], v[98:101]
	v_mfma_f32_16x16x32_bf16 v[90:93], v[216:219], v[184:187], v[90:93]
	v_mfma_f32_16x16x32_bf16 v[82:85], v[224:227], v[184:187], v[82:85]
	v_mfma_f32_16x16x32_bf16 v[74:77], v[216:219], v[192:195], v[74:77]
	v_mfma_f32_16x16x32_bf16 v[66:69], v[224:227], v[192:195], v[66:69]
	v_mfma_f32_16x16x32_bf16 v[122:125], v[220:223], v[172:175], v[122:125]
	v_mfma_f32_16x16x32_bf16 v[114:117], v[228:231], v[172:175], v[114:117]
	v_mfma_f32_16x16x32_bf16 v[106:109], v[220:223], v[180:183], v[106:109]
	v_mfma_f32_16x16x32_bf16 v[98:101], v[228:231], v[180:183], v[98:101]
	v_mfma_f32_16x16x32_bf16 v[90:93], v[220:223], v[188:191], v[90:93]
	v_mfma_f32_16x16x32_bf16 v[82:85], v[228:231], v[188:191], v[82:85]
	v_mfma_f32_16x16x32_bf16 v[74:77], v[220:223], v[196:199], v[74:77]
	v_mfma_f32_16x16x32_bf16 v[66:69], v[228:231], v[196:199], v[66:69]
	s_nop 0
	s_mov_b32 m0, s76
	v_lshl_add_u64 v[232:233], s[42:43], 0, v[142:143]
	s_barrier
	ds_read_b128 v[168:171], v167 offset:16384
	ds_read_b128 v[172:175], v167 offset:17408
	ds_read_b128 v[176:179], v167 offset:18432
	ds_read_b128 v[180:183], v167 offset:19456
	ds_read_b128 v[184:187], v167 offset:20480
	ds_read_b128 v[188:191], v167 offset:21504
	ds_read_b128 v[192:195], v167 offset:22528
	ds_read_b128 v[196:199], v167 offset:23552
	global_load_lds_dwordx4 v[232:233], off
	v_lshl_add_u64 v[234:235], s[42:43], 0, v[146:147]
	s_mov_b32 m0, s77
	s_nop 0
	global_load_lds_dwordx4 v[234:235], off
	s_barrier
	s_waitcnt lgkmcnt(0)
	s_nop 0
	s_waitcnt lgkmcnt(0)
	v_mfma_f32_16x16x32_bf16 v[62:65], v[130:133], v[168:171], v[62:65]
	v_mfma_f32_16x16x32_bf16 v[54:57], v[154:157], v[168:171], v[54:57]
	v_mfma_f32_16x16x32_bf16 v[46:49], v[130:133], v[176:179], v[46:49]
	v_mfma_f32_16x16x32_bf16 v[38:41], v[154:157], v[176:179], v[38:41]
	v_mfma_f32_16x16x32_bf16 v[30:33], v[130:133], v[184:187], v[30:33]
	v_mfma_f32_16x16x32_bf16 v[22:25], v[154:157], v[184:187], v[22:25]
	v_mfma_f32_16x16x32_bf16 v[10:13], v[130:133], v[192:195], v[10:13]
	v_mfma_f32_16x16x32_bf16 v[2:5], v[154:157], v[192:195], v[2:5]
	v_mfma_f32_16x16x32_bf16 v[62:65], v[134:137], v[172:175], v[62:65]
	v_mfma_f32_16x16x32_bf16 v[54:57], v[158:161], v[172:175], v[54:57]
	v_mfma_f32_16x16x32_bf16 v[46:49], v[134:137], v[180:183], v[46:49]
	v_mfma_f32_16x16x32_bf16 v[38:41], v[158:161], v[180:183], v[38:41]
	v_mfma_f32_16x16x32_bf16 v[30:33], v[134:137], v[188:191], v[30:33]
	v_mfma_f32_16x16x32_bf16 v[22:25], v[158:161], v[188:191], v[22:25]
	v_mfma_f32_16x16x32_bf16 v[10:13], v[134:137], v[196:199], v[10:13]
	v_mfma_f32_16x16x32_bf16 v[2:5], v[158:161], v[196:199], v[2:5]
	s_nop 0
	s_barrier
; #define G8_STAGE(bufoff, gbase, voff) do { _Pragma("unroll") for (int _i = 0; _i < 2; ++_i) \
;         __builtin_amdgcn_global_load_lds((const unsigned*)((const char*)(gbase) + (voff)[_i]), (LAS unsigned*)(lds + (bufoff) + ldsw + _i * 8192), 16, 0, 0); } while (0)
; #define G8_LDA(dst, b, h) do { _Pragma("unroll") for (int m = 0; m < 4; ++m) _Pragma("unroll") for (int k = 0; k < 2; ++k) dst[m][k] = *(const LAS bf16x8*)(lds + G8_SA(b, h) + aoff + m * 2048 + k * 1024); } while (0)
; #define G8_LDB(dst, b, h) do { _Pragma("unroll") for (int n = 0; n < 2; ++n) _Pragma("unroll") for (int k = 0; k < 2; ++k) dst[n][k] = *(const LAS bf16x8*)(lds + G8_SB(b, h) + boff + n * 2048 + k * 1024); } while (0)
; #define G8_MMA(ai, bj, At, Bt) do { __builtin_amdgcn_s_setprio(1); _Pragma("unroll") for (int m = 0; m < 4; ++m) _Pragma("unroll") for (int n = 0; n < 2; ++n) _Pragma("unroll") for (int k = 0; k < 2; ++k) \
;         acc[ai][bj][m][n] = __builtin_amdgcn_mfma_f32_16x16x32_bf16(Bt[n][k], At[m][k], acc[ai][bj][m][n], 0, 0, 0); __builtin_amdgcn_s_setprio(0); } while (0)
; #define G8_WAIT_V(n) asm volatile("s_waitcnt vmcnt(" #n ")" ::: "memory")
; #define G8_WAIT_L(n) asm volatile("s_waitcnt lgkmcnt(" #n ")" ::: "memory")
; #define G8_BAR __builtin_amdgcn_s_barrier()
; #define G8_SCHED __builtin_amdgcn_sched_barrier(0)
; template <class Epi, class Sched>
; __device__ __forceinline__ void gemm_phase(LAS unsigned char* lds, const int K, const Sched& S, const Epi& E) {
;     ...
;             G8_STAGE(G8_SB(0, 1), b2 + hstep, voffB);
;             G8_WAIT_V(6); G8_BAR; G8_MMA(1, 1, At, B1); G8_BAR;
;             G8_LDB(B0, 1, 0); G8_SCHED; G8_LDA(At, 1, 0); G8_STAGE(G8_SA(0, 1), a2, oc[1]);
;             G8_WAIT_L(8); G8_BAR; G8_WAIT_L(0); G8_MMA(0, 0, At, B0); G8_BAR; G8_SCHED;
;             G8_LDB(B1, 1, 1); G8_STAGE(G8_SB(1, 0), b3, voffB);
;             G8_BAR; G8_WAIT_L(0); G8_MMA(0, 1, At, B1); G8_BAR;
;             G8_LDA(At, 1, 1); G8_STAGE(G8_SA(1, 0), a3, oc[0]);
	s_add_u32 s0, s38, 0x40000
	s_addc_u32 s1, s39, 0
	s_add_i32 s49, s54, s65
	v_lshl_add_u64 v[130:131], s[0:1], 0, v[0:1]
	s_mov_b32 m0, s49
	s_nop 0
	global_load_lds_dwordx4 v[130:131], off
	v_lshl_add_u64 v[130:131], s[0:1], 0, v[140:141]
	s_add_i32 m0, s49, 0x2000
	s_nop 0
	global_load_lds_dwordx4 v[130:131], off
	s_waitcnt vmcnt(6)
	s_barrier
	s_nop 0
	v_mfma_f32_16x16x32_bf16 v[58:61], v[216:219], v[168:171], v[58:61]
	v_mfma_f32_16x16x32_bf16 v[50:53], v[224:227], v[168:171], v[50:53]
	v_mfma_f32_16x16x32_bf16 v[42:45], v[216:219], v[176:179], v[42:45]
	v_mfma_f32_16x16x32_bf16 v[34:37], v[224:227], v[176:179], v[34:37]
	v_mfma_f32_16x16x32_bf16 v[26:29], v[216:219], v[184:187], v[26:29]
	v_mfma_f32_16x16x32_bf16 v[18:21], v[224:227], v[184:187], v[18:21]
	v_mfma_f32_16x16x32_bf16 v[14:17], v[216:219], v[192:195], v[14:17]
	v_mfma_f32_16x16x32_bf16 v[6:9], v[224:227], v[192:195], v[6:9]
	v_mfma_f32_16x16x32_bf16 v[58:61], v[220:223], v[172:175], v[58:61]
	v_mfma_f32_16x16x32_bf16 v[50:53], v[228:231], v[172:175], v[50:53]
	v_mfma_f32_16x16x32_bf16 v[42:45], v[220:223], v[180:183], v[42:45]
	v_mfma_f32_16x16x32_bf16 v[34:37], v[228:231], v[180:183], v[34:37]
	v_mfma_f32_16x16x32_bf16 v[26:29], v[220:223], v[188:191], v[26:29]
	v_mfma_f32_16x16x32_bf16 v[18:21], v[228:231], v[188:191], v[18:21]
	v_mfma_f32_16x16x32_bf16 v[14:17], v[220:223], v[196:199], v[14:17]
	v_mfma_f32_16x16x32_bf16 v[6:9], v[228:231], v[196:199], v[6:9]
	s_nop 0
	s_add_i32 s0, 0, 0x18000
	v_add_u32_e32 v158, s0, v165
	s_barrier
	ds_read_b128 v[130:133], v158
	ds_read_b128 v[134:137], v158 offset:1024
	ds_read_b128 v[154:157], v158 offset:2048
	ds_read_b128 v[158:161], v158 offset:3072
	s_mov_b32 m0, s78
	v_lshl_add_u64 v[216:217], s[42:43], 0, v[144:145]
	ds_read_b128 v[168:171], v167 offset:32768
	ds_read_b128 v[172:175], v167 offset:33792
	ds_read_b128 v[176:179], v167 offset:34816
	ds_read_b128 v[180:183], v167 offset:35840
	ds_read_b128 v[184:187], v167 offset:36864
	ds_read_b128 v[188:191], v167 offset:37888
	ds_read_b128 v[192:195], v167 offset:38912
	ds_read_b128 v[196:199], v167 offset:39936
	global_load_lds_dwordx4 v[216:217], off
	v_lshl_add_u64 v[216:217], s[42:43], 0, v[148:149]
	s_mov_b32 m0, s79
	s_nop 0
	global_load_lds_dwordx4 v[216:217], off
	s_waitcnt lgkmcnt(8)
	s_barrier
	s_waitcnt lgkmcnt(0)
	s_nop 0
	s_waitcnt lgkmcnt(0)
	v_mfma_f32_16x16x32_bf16 v[126:129], v[130:133], v[168:171], v[126:129]
	v_mfma_f32_16x16x32_bf16 v[118:121], v[154:157], v[168:171], v[118:121]
	v_mfma_f32_16x16x32_bf16 v[110:113], v[130:133], v[176:179], v[110:113]
	v_mfma_f32_16x16x32_bf16 v[102:105], v[154:157], v[176:179], v[102:105]
	v_mfma_f32_16x16x32_bf16 v[94:97], v[130:133], v[184:187], v[94:97]
	v_mfma_f32_16x16x32_bf16 v[86:89], v[154:157], v[184:187], v[86:89]
	v_mfma_f32_16x16x32_bf16 v[78:81], v[130:133], v[192:195], v[78:81]
	v_mfma_f32_16x16x32_bf16 v[70:73], v[154:157], v[192:195], v[70:73]
	v_mfma_f32_16x16x32_bf16 v[126:129], v[134:137], v[172:175], v[126:129]
	v_mfma_f32_16x16x32_bf16 v[118:121], v[158:161], v[172:175], v[118:121]
	v_mfma_f32_16x16x32_bf16 v[110:113], v[134:137], v[180:183], v[110:113]
	v_mfma_f32_16x16x32_bf16 v[102:105], v[158:161], v[180:183], v[102:105]
	v_mfma_f32_16x16x32_bf16 v[94:97], v[134:137], v[188:191], v[94:97]
	v_mfma_f32_16x16x32_bf16 v[86:89], v[158:161], v[188:191], v[86:89]
	v_mfma_f32_16x16x32_bf16 v[78:81], v[134:137], v[196:199], v[78:81]
	v_mfma_f32_16x16x32_bf16 v[70:73], v[158:161], v[196:199], v[70:73]
	s_nop 0
	s_barrier
	s_add_i32 s42, 0, 0x1c000
	s_add_i32 s0, s0, s65
	v_add_u32_e32 v213, s42, v165
	v_lshl_add_u64 v[162:163], v[162:163], 0, s[18:19]
	s_mov_b32 m0, s0
	ds_read_b128 v[216:219], v213
	ds_read_b128 v[220:223], v213 offset:1024
	ds_read_b128 v[224:227], v213 offset:2048
	ds_read_b128 v[228:231], v213 offset:3072
	global_load_lds_dwordx4 v[162:163], off
	v_lshl_add_u64 v[162:163], v[200:201], 0, s[18:19]
	s_add_i32 m0, s0, 0x2000
	s_nop 0
	global_load_lds_dwordx4 v[162:163], off
	s_barrier
	s_waitcnt lgkmcnt(0)
	s_nop 0
	s_waitcnt lgkmcnt(0)
	v_mfma_f32_16x16x32_bf16 v[122:125], v[216:219], v[168:171], v[122:125]
	v_mfma_f32_16x16x32_bf16 v[114:117], v[224:227], v[168:171], v[114:117]
	v_mfma_f32_16x16x32_bf16 v[106:109], v[216:219], v[176:179], v[106:109]
	v_mfma_f32_16x16x32_bf16 v[98:101], v[224:227], v[176:179], v[98:101]
	v_mfma_f32_16x16x32_bf16 v[90:93], v[216:219], v[184:187], v[90:93]
	v_mfma_f32_16x16x32_bf16 v[82:85], v[224:227], v[184:187], v[82:85]
	v_mfma_f32_16x16x32_bf16 v[74:77], v[216:219], v[192:195], v[74:77]
	v_mfma_f32_16x16x32_bf16 v[66:69], v[224:227], v[192:195], v[66:69]
	v_mfma_f32_16x16x32_bf16 v[122:125], v[220:223], v[172:175], v[122:125]
	v_mfma_f32_16x16x32_bf16 v[114:117], v[228:231], v[172:175], v[114:117]
	v_mfma_f32_16x16x32_bf16 v[106:109], v[220:223], v[180:183], v[106:109]
	v_mfma_f32_16x16x32_bf16 v[98:101], v[228:231], v[180:183], v[98:101]
	v_mfma_f32_16x16x32_bf16 v[90:93], v[220:223], v[188:191], v[90:93]
	v_mfma_f32_16x16x32_bf16 v[82:85], v[228:231], v[188:191], v[82:85]
	v_mfma_f32_16x16x32_bf16 v[74:77], v[220:223], v[196:199], v[74:77]
	v_mfma_f32_16x16x32_bf16 v[66:69], v[228:231], v[196:199], v[66:69]
	s_nop 0
	s_mov_b32 m0, s81
	v_lshl_add_u64 v[162:163], v[232:233], 0, s[18:19]
	s_barrier
	ds_read_b128 v[168:171], v167 offset:49152
	ds_read_b128 v[172:175], v167 offset:50176
	ds_read_b128 v[176:179], v167 offset:51200
	ds_read_b128 v[180:183], v167 offset:52224
	ds_read_b128 v[184:187], v167 offset:53248
	ds_read_b128 v[188:191], v167 offset:54272
	ds_read_b128 v[192:195], v167 offset:55296
	ds_read_b128 v[196:199], v167 offset:56320
	global_load_lds_dwordx4 v[162:163], off
	v_lshl_add_u64 v[162:163], v[234:235], 0, s[18:19]
	s_mov_b32 m0, s82
	s_nop 0
	global_load_lds_dwordx4 v[162:163], off
	s_barrier
; #define G8_WAIT_V(n) asm volatile("s_waitcnt vmcnt(" #n ")" ::: "memory")
; #define G8_WAIT_L(n) asm volatile("s_waitcnt lgkmcnt(" #n ")" ::: "memory")
; #define G8_BAR __builtin_amdgcn_s_barrier()
; #define G8_SCHED __builtin_amdgcn_sched_barrier(0)
; template <class Epi, class Sched>
; __device__ __forceinline__ void gemm_phase(LAS unsigned char* lds, const int K, const Sched& S, const Epi& E) {
;     ...
;             G8_BAR; G8_WAIT_L(0); G8_MMA(1, 0, At, B0); G8_BAR; G8_SCHED;
;             G8_STAGE(G8_SB(1, 1), b3 + hstep, voffB);
;             G8_WAIT_V(6); G8_BAR; G8_MMA(1, 1, At, B1); G8_BAR;
;     __device__ __forceinline__ void operator()(const f32x4 (&acc)[2][2][4][2], const g8::Unit& u, int wr, int wc, int fr_, int fq_) const {
;         int fr = fr_, fq = fq_; asm volatile("" : "+v"(fr), "+v"(fq));
;         const int pn = u.pn; const int colp = pn * 256 + wc * 32 + fq * 8;
;         bf16_t* qb = (bf16_t*)(ws + AB_QB); bf16_t* kb = (bf16_t*)(ws + AB_KB); bf16_t* vT = (bf16_t*)(ws + AB_VT); bf16_t* rqb = (bf16_t*)(ws + AB_RQB); bf16_t* rkb = (bf16_t*)(ws + AB_RKB);
;         bf16_t* rkdT = (bf16_t*)(ws + AB_RKDT); bf16_t* rvT = (bf16_t*)(ws + AB_RVT); bf16_t* rgb = (bf16_t*)(ws + AB_RGB);
;         const float frqA0 = exp2f(-(float)(fq * 8) * (13.287712379549449f / 32.f)) * 0.15915494309189535f;
;         const float frqR0 = exp2f(-(float)((wc & 1) * 32 + fq * 8) * (13.287712379549449f / 63.f)) * 0.15915494309189535f;
;         constexpr float RA[8] = {1.f, 0.7498942093324559f, 0.5623413251903491f, 0.4216965034285822f, 0.31622776601683794f, 0.23713737056616552f, 0.1778279410038923f, 0.1333521432163324f};
;         constexpr float RR[8] = {1.f, 0.8639884494839686f, 0.746476040841712f, 0.6449466771037624f, 0.5572264795507174f, 0.4814372420784346f, 0.4159562163071847f, 0.35938136638046275f};
; #pragma unroll
;         for (int ai = 0; ai < 2; ++ai)
; #pragma unroll
;             for (int m = 0; m < 4; ++m) {
;                 const int t = u.pm * 256 + ai * 128 + wr * 64 + m * 16 + fr, sq = t & (SEQ - 1), b = t >> 13;
;                 f32x4 x[2][2];
; #pragma unroll
;                 for (int bj = 0; bj < 2; ++bj)
; #pragma unroll
;                     for (int n = 0; n < 2; ++n) x[bj][n] = acc[ai][bj][m][n];
;                 if (pn < 4 || (pn == 4 && wc < 2)) {
;                     const int j0 = fq * 8; const float sc = pn < 4 ? 0.125f : 1.f;
	s_waitcnt lgkmcnt(0)
	s_nop 0
	s_waitcnt lgkmcnt(0)
	v_mfma_f32_16x16x32_bf16 v[62:65], v[130:133], v[168:171], v[62:65]
	v_mfma_f32_16x16x32_bf16 v[54:57], v[154:157], v[168:171], v[54:57]
	v_mfma_f32_16x16x32_bf16 v[46:49], v[130:133], v[176:179], v[46:49]
	v_mfma_f32_16x16x32_bf16 v[38:41], v[154:157], v[176:179], v[38:41]
	v_mfma_f32_16x16x32_bf16 v[30:33], v[130:133], v[184:187], v[30:33]
	v_mfma_f32_16x16x32_bf16 v[22:25], v[154:157], v[184:187], v[22:25]
	v_mfma_f32_16x16x32_bf16 v[10:13], v[130:133], v[192:195], v[10:13]
	v_mfma_f32_16x16x32_bf16 v[2:5], v[154:157], v[192:195], v[2:5]
	v_mfma_f32_16x16x32_bf16 v[62:65], v[134:137], v[172:175], v[62:65]
	v_mfma_f32_16x16x32_bf16 v[54:57], v[158:161], v[172:175], v[54:57]
	v_mfma_f32_16x16x32_bf16 v[46:49], v[134:137], v[180:183], v[46:49]
	v_mfma_f32_16x16x32_bf16 v[38:41], v[158:161], v[180:183], v[38:41]
	v_mfma_f32_16x16x32_bf16 v[30:33], v[134:137], v[188:191], v[30:33]
	v_mfma_f32_16x16x32_bf16 v[22:25], v[158:161], v[188:191], v[22:25]
	v_mfma_f32_16x16x32_bf16 v[10:13], v[134:137], v[196:199], v[10:13]
	v_mfma_f32_16x16x32_bf16 v[2:5], v[158:161], v[196:199], v[2:5]
	s_nop 0
	s_barrier
	s_add_u32 s0, s38, 0x40080
	s_addc_u32 s1, s39, 0
	s_add_i32 s38, s42, s65
	v_lshl_add_u64 v[130:131], s[0:1], 0, v[0:1]
	s_mov_b32 m0, s38
	s_nop 0
	global_load_lds_dwordx4 v[130:131], off
	v_lshl_add_u64 v[130:131], s[0:1], 0, v[140:141]
	s_add_i32 m0, s38, 0x2000
	s_nop 0
	global_load_lds_dwordx4 v[130:131], off
	s_waitcnt vmcnt(6)
	s_barrier
	s_nop 0
	v_mfma_f32_16x16x32_bf16 v[58:61], v[216:219], v[168:171], v[58:61]
	v_mfma_f32_16x16x32_bf16 v[50:53], v[224:227], v[168:171], v[50:53]
	v_mfma_f32_16x16x32_bf16 v[42:45], v[216:219], v[176:179], v[42:45]
	v_mfma_f32_16x16x32_bf16 v[34:37], v[224:227], v[176:179], v[34:37]
	v_mfma_f32_16x16x32_bf16 v[26:29], v[216:219], v[184:187], v[26:29]
	v_mfma_f32_16x16x32_bf16 v[18:21], v[224:227], v[184:187], v[18:21]
	v_mfma_f32_16x16x32_bf16 v[14:17], v[216:219], v[192:195], v[14:17]
	v_mfma_f32_16x16x32_bf16 v[6:9], v[224:227], v[192:195], v[6:9]
	v_mfma_f32_16x16x32_bf16 v[58:61], v[220:223], v[172:175], v[58:61]
	v_mfma_f32_16x16x32_bf16 v[50:53], v[228:231], v[172:175], v[50:53]
	v_mfma_f32_16x16x32_bf16 v[42:45], v[220:223], v[180:183], v[42:45]
	v_mfma_f32_16x16x32_bf16 v[34:37], v[228:231], v[180:183], v[34:37]
	v_mfma_f32_16x16x32_bf16 v[26:29], v[220:223], v[188:191], v[26:29]
	v_mfma_f32_16x16x32_bf16 v[18:21], v[228:231], v[188:191], v[18:21]
	v_mfma_f32_16x16x32_bf16 v[14:17], v[220:223], v[196:199], v[14:17]
	v_mfma_f32_16x16x32_bf16 v[6:9], v[228:231], v[196:199], v[6:9]
	s_nop 0
	s_add_i32 s47, s47, 2
	s_add_u32 s3, s3, 0x100
	s_addc_u32 s14, s14, 0
	s_cmp_gt_u32 s47, 13
	s_mov_b64 s[0:1], s[12:13]
	s_barrier
	s_cbranch_scc0 .LBB0_487
	s_nop 0
	s_nop 0
	s_nop 0
	s_nop 0
	s_nop 0
	s_nop 0
	s_nop 0
	s_nop 0
	s_nop 0
	s_nop 0
	s_lshl_b32 s2, s2, 8
	s_add_i32 s2, s2, s80
	s_cmp_lt_i32 s94, 4
	s_cselect_b64 s[36:37], -1, 0
	s_cmp_lg_u32 s94, 4
	v_mov_b32_e32 v131, v164
	v_mov_b32_e32 v130, v139
	s_cselect_b64 s[12:13], -1, 0
	s_cmp_eq_u32 s94, 4
	s_nop 0
	v_add_u32_e32 v160, s2, v131
	s_cselect_b64 s[2:3], -1, 0
	s_and_b64 s[2:3], s[2:3], s[10:11]
	s_cmp_gt_u32 s94, 8
	s_cselect_b64 s[56:57], -1, 0
	s_cmp_gt_u32 s94, 12
	s_cselect_b64 s[54:55], -1, 0
	s_lshl_b32 s42, s94, 8
	s_add_i32 s14, s42, 0xfffff300
	v_lshlrev_b32_e32 v130, 3, v130
	s_lshl_b64 s[22:23], s[14:15], 1
	v_add_u32_e32 v132, s85, v130
	s_add_u32 s22, s87, s22
	v_cvt_f32_i32_e32 v133, v132
	s_addc_u32 s23, s88, s23
	s_add_i32 s14, s86, s42
	s_cmp_gt_u32 s94, 6
	v_add_u32_e32 v171, s14, v130
	s_cselect_b64 s[38:39], -1, 0
	s_lshl_b32 s14, s94, 1
	s_and_b32 s14, s14, 2
	v_mul_f32_e32 v134, 0xbe57fa62, v133
	s_or_b32 s14, s14, s89
	v_cmp_gt_f32_e32 vcc, s66, v134
	v_ashrrev_i32_e32 v131, 31, v130
	s_lshl_b32 s14, s14, 7
	v_cvt_f32_i32_e32 v172, v130
	v_cndmask_b32_e32 v134, 0, v207, vcc
	v_lshlrev_b64 v[162:163], 1, v[130:131]
	s_xor_b32 s14, s14, 0x100
	v_fmac_f32_e32 v134, 0xbe57fa62, v133
	v_lshl_add_u64 v[158:159], s[22:23], 0, v[162:163]
	s_and_b64 s[22:23], s[38:39], exec
	v_exp_f32_e32 v133, v134
	s_mov_b32 s22, 0x3d420000
	s_cselect_b32 s22, s22, 0x3c420000
	v_mul_f32_e32 v134, 0xbed49a78, v172
	s_add_u32 s22, s40, s22
	v_cmp_gt_f32_e64 s[0:1], s66, v134
	v_cndmask_b32_e32 v134, 0, v208, vcc
	v_add_u32_e32 v170, s14, v132
	s_addc_u32 s23, s41, 0
	s_lshl_b32 s14, s14, 1
	v_ldexp_f32 v133, v133, v134
	s_add_u32 s22, s22, s14
	v_mul_f32_e32 v169, 0.15915494, v133
	s_addc_u32 s23, s23, 0
	v_ashrrev_i32_e32 v133, 31, v132
	v_lshl_add_u64 v[154:155], v[132:133], 1, s[22:23]
	s_or_b32 s22, s42, s75
	s_ashr_i32 s23, s22, 31
	s_lshl_b64 s[22:23], s[22:23], 1
	s_add_u32 s42, s83, s22
	v_mov_b32_e32 v131, 0x3db504f3
	s_addc_u32 s43, s84, s23
	s_nor_b64 s[22:23], s[36:37], s[2:3]
	v_cndmask_b32_e64 v156, 1.0, v131, s[38:39]
	v_add_u32_e32 v168, s90, v130
	v_and_b32_e32 v173, 0x1fff, v160
	s_mov_b64 s[2:3], -1
	s_and_b64 vcc, exec, s[22:23]
	s_cbranch_vccz .LBB0_506
; __device__ __forceinline__ unsigned pk2(float lo, float hi) { unsigned r; asm("v_cvt_pk_bf16_f32 %0, %1, %2" : "=v"(r) : "v"(lo), "v"(hi)); return r; }
; __device__ __forceinline__ f32x4 silu4(const f32x4 x) { const f32x4 t = x * (-1.4426950408889634f); f32x4 d;
; #pragma unroll
;     for (int e = 0; e < 4; ++e) d[e] = __builtin_amdgcn_exp2f(t[e]);
;     d = d + 1.f;
; #pragma unroll
;     for (int e = 0; e < 4; ++e) d[e] = __builtin_amdgcn_rcpf(d[e]);
;     return x * d; }
;     __device__ __forceinline__ void operator()(const f32x4 (&acc)[2][2][4][2], const g8::Unit& u, int wr, int wc, int fr_, int fq_) const {
;     ...
;                 } else {
; #pragma unroll
;                     for (int bj = 0; bj < 2; ++bj) { u32x4 w;
; #pragma unroll
;                         for (int n = 0; n < 2; ++n) { const f32x4 sv = silu4(x[bj][n]); w[2 * n] = pk2(sv[0], sv[1]); w[2 * n + 1] = pk2(sv[2], sv[3]); }
;                         *(u32x4*)(rgb + (size_t)t * 1024 + (pn - 13) * 256 + bj * 128 + wc * 32 + fq * 8) = w; }
	v_ashrrev_i32_e32 v174, 13, v160
	s_and_b64 vcc, exec, s[12:13]
	s_cbranch_vccz .LBB0_503
	s_and_b64 vcc, exec, s[56:57]
	s_cbranch_vccz .LBB0_496
	s_andn2_b64 vcc, exec, s[54:55]
	s_cbranch_vccnz .LBB0_493
	v_mul_f32_e32 v132, 0xbfb8aa3b, v126
	v_mul_f32_e32 v133, 0xbfb8aa3b, v127
	v_mul_f32_e32 v134, 0xbfb8aa3b, v128
	v_mul_f32_e32 v135, 0xbfb8aa3b, v129
	v_exp_f32_e32 v132, v132
	v_exp_f32_e32 v133, v133
	v_exp_f32_e32 v134, v134
	v_exp_f32_e32 v135, v135
	v_mul_f32_e32 v136, 0xbfb8aa3b, v120
	v_pk_add_f32 v[132:133], v[132:133], 1.0 op_sel_hi:[1,0]
	v_mul_f32_e32 v137, 0xbfb8aa3b, v121
	v_pk_add_f32 v[134:135], v[134:135], 1.0 op_sel_hi:[1,0]
	v_rcp_f32_e32 v132, v132
	v_rcp_f32_e32 v133, v133
	v_rcp_f32_e32 v134, v134
	v_rcp_f32_e32 v135, v135
	v_exp_f32_e32 v136, v136
	v_pk_mul_f32 v[132:133], v[126:127], v[132:133]
	v_exp_f32_e32 v137, v137
	v_pk_mul_f32 v[134:135], v[128:129], v[134:135]
	v_cvt_pk_bf16_f32 v132, v132, v133
	v_ashrrev_i32_e32 v161, 31, v160
	v_cvt_pk_bf16_f32 v133, v134, v135
	v_mul_f32_e32 v134, 0xbfb8aa3b, v118
	v_mul_f32_e32 v135, 0xbfb8aa3b, v119
	v_exp_f32_e32 v134, v134
	v_exp_f32_e32 v135, v135
	v_pk_add_f32 v[136:137], v[136:137], 1.0 op_sel_hi:[1,0]
	v_lshlrev_b64 v[130:131], 11, v[160:161]
	v_rcp_f32_e32 v136, v136
	v_pk_add_f32 v[134:135], v[134:135], 1.0 op_sel_hi:[1,0]
	v_rcp_f32_e32 v137, v137
	v_rcp_f32_e32 v134, v134
	v_rcp_f32_e32 v135, v135
	v_lshl_add_u64 v[130:131], v[158:159], 0, v[130:131]
	v_pk_mul_f32 v[136:137], v[120:121], v[136:137]
	s_mov_b64 s[2:3], 0
	v_pk_mul_f32 v[134:135], v[118:119], v[134:135]
	s_nop 0
	v_cvt_pk_bf16_f32 v134, v134, v135
	v_cvt_pk_bf16_f32 v135, v136, v137
	global_store_dwordx4 v[130:131], v[132:135], off
	v_mul_f32_e32 v136, 0xbfb8aa3b, v116
	v_mul_f32_e32 v137, 0xbfb8aa3b, v117
	v_mul_f32_e32 v132, 0xbfb8aa3b, v122
	v_mul_f32_e32 v133, 0xbfb8aa3b, v123
	v_mul_f32_e32 v134, 0xbfb8aa3b, v124
	v_mul_f32_e32 v135, 0xbfb8aa3b, v125
	v_exp_f32_e32 v132, v132
	v_exp_f32_e32 v133, v133
	v_exp_f32_e32 v134, v134
	v_exp_f32_e32 v135, v135
	v_exp_f32_e32 v136, v136
	v_pk_add_f32 v[132:133], v[132:133], 1.0 op_sel_hi:[1,0]
	v_exp_f32_e32 v137, v137
	v_pk_add_f32 v[134:135], v[134:135], 1.0 op_sel_hi:[1,0]
	v_rcp_f32_e32 v132, v132
	v_rcp_f32_e32 v133, v133
	v_rcp_f32_e32 v134, v134
	v_rcp_f32_e32 v135, v135
	v_pk_add_f32 v[136:137], v[136:137], 1.0 op_sel_hi:[1,0]
	v_pk_mul_f32 v[132:133], v[122:123], v[132:133]
	v_rcp_f32_e32 v136, v136
	v_pk_mul_f32 v[134:135], v[124:125], v[134:135]
	v_cvt_pk_bf16_f32 v132, v132, v133
	v_rcp_f32_e32 v137, v137
	v_cvt_pk_bf16_f32 v133, v134, v135
	v_mul_f32_e32 v134, 0xbfb8aa3b, v114
	v_mul_f32_e32 v135, 0xbfb8aa3b, v115
	v_exp_f32_e32 v134, v134
	v_exp_f32_e32 v135, v135
	v_pk_mul_f32 v[136:137], v[116:117], v[136:137]
	v_pk_add_f32 v[134:135], v[134:135], 1.0 op_sel_hi:[1,0]
	s_nop 0
	v_rcp_f32_e32 v134, v134
	v_rcp_f32_e32 v135, v135
	s_nop 0
	v_pk_mul_f32 v[134:135], v[114:115], v[134:135]
	s_nop 0
	v_cvt_pk_bf16_f32 v134, v134, v135
	v_cvt_pk_bf16_f32 v135, v136, v137
	global_store_dwordx4 v[130:131], v[132:135], off offset:256

; #define G8_WAIT_V(n) asm volatile("s_waitcnt vmcnt(" #n ")" ::: "memory")
; #define G8_BAR __builtin_amdgcn_s_barrier()
; template <class Epi, class Sched>
; __device__ __forceinline__ void gemm_phase(LAS unsigned char* lds, const int K, const Sched& S, const Epi& E) {
;     ...
;     G8_WAIT_V(0);
;     if (wr == 0) G8_BAR;
;     G8_BAR;
.LBB0_652:
	v_readlane_b32 s76, v254, 35
	v_readlane_b32 s84, v254, 23
	v_readlane_b32 s77, v254, 36
	s_movk_i32 s75, 0xa00
	s_mov_b32 s78, 0x900000
	s_barrier
	s_setprio 0
	s_nop 0
	s_nop 0
	s_nop 0
	s_nop 0
	s_nop 0
	s_nop 0
	s_nop 0
	s_nop 0
	s_nop 0
	s_nop 0
	s_nop 0
	s_nop 0
	s_nop 0
	s_nop 0
	s_nop 0
	s_add_i32 s0, s46, 1
	s_cmp_ge_i32 s0, s31
	s_mov_b32 s94, s96
	s_cbranch_scc1 .LBB0_740

; #define G8_STAGE(bufoff, gbase, voff) do { _Pragma("unroll") for (int _i = 0; _i < 2; ++_i) \
;         __builtin_amdgcn_global_load_lds((const unsigned*)((const char*)(gbase) + (voff)[_i]), (LAS unsigned*)(lds + (bufoff) + ldsw + _i * 8192), 16, 0, 0); } while (0)
; #define G8_WAIT_V(n) asm volatile("s_waitcnt vmcnt(" #n ")" ::: "memory")
;     __device__ __forceinline__ void init(f32x4 (&acc)[2][2][4][2], const Unit& u, int wc, int fq) const {
;         const int col0 = u.pn * BM + wc * 32 + 8 * fq;
; #pragma unroll
;         for (int b = 0; b < 2; ++b)
; #pragma unroll
;             for (int n = 0; n < 2; ++n) { const f32x4 bv = *(const f32x4*)(bias + col0 + b * HALF + 4 * n);
; #pragma unroll
;                 for (int a = 0; a < 2; ++a)
; #pragma unroll
;                     for (int m = 0; m < 4; ++m) acc[a][b][m][n] = bv; } }
; template <class Epi, class Sched>
; __device__ __forceinline__ void gemm_phase(LAS unsigned char* lds, const int K, const Sched& S, const Epi& E) {
;     int tid_ = S.tid0; asm volatile("" : "+v"(tid_));
;     const int tid = tid_, wid = __builtin_amdgcn_readfirstlane(tid >> 6), lane = tid & 63, wr = wid >> 2, wc = wid & 3, fr = lane & 15, fq = lane >> 4;
;     const int nt = K / BK;
;     unsigned voffB[2];
; #pragma unroll
;     for (int i = 0; i < 2; ++i) { int R, C; stage_rc(tid * 16 + i * 8192, R, C); const int Rb = Epi::PERM ? ((R & ~31) + perm32(R & 31)) : R;
;         voffB[i] = (unsigned)(Rb * K + C) * 2u; }
;     const size_t kstep = (size_t)(BK * 2);
;     const size_t hstep = (size_t)HALF * K * 2;
;     const unsigned ldsw = (unsigned)wid * 1024u;
;     const int aoff = lds_byte(wr * 64 + fr, fq * 8), boff = lds_byte(wc * 32 + fr, fq * 8);
;     ...
;     Unit cur, nxt; int ui = 0;
;     if (!S.next(0, cur)) return;
;     f32x4 acc[2][2][4][2];
;     E.init(acc, cur, wc, fq);
;     bf16x8 At[4][2], B0[2][2], B1[2][2];
;     unsigned oc[2][2];
;     S.aoff(cur, tid, oc);
;     const char* cA = cur.A; const char* cB = cur.B;
;     G8_STAGE(G8_SB(0, 0), cB, voffB); G8_STAGE(G8_SA(0, 0), cA, oc[0]); G8_STAGE(G8_SB(0, 1), cB + hstep, voffB); G8_STAGE(G8_SA(0, 1), cA, oc[1]);
;     if (wr == 1) G8_BAR;
;     G8_WAIT_V(4); G8_BAR;
;     G8_STAGE(G8_SB(1, 0), cB + kstep, voffB); G8_STAGE(G8_SA(1, 0), cA + kstep, oc[0]); G8_STAGE(G8_SB(1, 1), cB + hstep + kstep, voffB);
;     G8_WAIT_V(6); G8_BAR;
.LBB0_2241:
	v_bfe_i32 v3, v18, 27, 1
	v_lshlrev_b32_e32 v2, 4, v18
	v_lshrrev_b32_e32 v3, 22, v3
	v_add_u32_e32 v3, v2, v3
	v_and_b32_e32 v3, 0xfffffc00, v3
	v_sub_u32_e32 v3, v2, v3
	v_ashrrev_i32_e32 v0, 31, v18
	v_lshrrev_b32_e32 v4, 4, v3
	v_lshrrev_b32_e32 v0, 26, v0
	v_bitop3_b32 v3, v4, v3, 32 bitop3:0x6c
	v_add_u32_e32 v0, v18, v0
	v_ashrrev_i32_e32 v5, 31, v3
	v_ashrrev_i32_e32 v0, 6, v0
	v_lshrrev_b32_e32 v5, 26, v5
	v_lshlrev_b32_e32 v4, 3, v0
	v_add_u32_e32 v5, v3, v5
	v_lshlrev_b32_e32 v0, 5, v0
	v_and_b32_e32 v19, 32, v0
	v_and_b32_e32 v0, 0xc0, v5
	s_add_u32 s38, s0, 0x5ac20000
	v_and_b32_e32 v4, -16, v4
	v_ashrrev_i32_e32 v6, 6, v5
	v_sub_u32_e32 v0, v3, v0
	s_addc_u32 s39, s1, 0
	v_add_u32_e32 v24, v6, v4
	v_ashrrev_i16_sdwa v0, v203, sext(v0) dst_sel:DWORD dst_unused:UNUSED_PAD src0_sel:DWORD src1_sel:BYTE_0
	s_add_u32 s40, s0, s7
	v_bfe_i32 v20, v0, 0, 16
	v_lshlrev_b32_e32 v0, 1, v24
	v_lshrrev_b32_e32 v3, 2, v24
	v_and_b32_e32 v4, 3, v6
	s_mov_b32 s7, 0x7fffffe0
	v_and_b32_e32 v0, 24, v0
	v_and_b32_e32 v3, 4, v3
	v_and_or_b32 v4, v24, s7, v4
	v_add_u32_e32 v2, 0x2000, v2
	v_or3_b32 v0, v4, v3, v0
	v_ashrrev_i32_e32 v3, 31, v2
	v_lshrrev_b32_e32 v3, 22, v3
	v_add_u32_e32 v3, v2, v3
	v_ashrrev_i32_e32 v3, 10, v3
	v_mul_i32_i24_e32 v4, 0x400, v3
	v_sub_u32_e32 v2, v2, v4
	v_lshrrev_b32_e32 v4, 4, v2
	v_bitop3_b32 v2, v4, v2, 32 bitop3:0x6c
	v_ashrrev_i32_e32 v5, 31, v2
	v_lshrrev_b32_e32 v5, 26, v5
	v_lshlrev_b32_e32 v4, 3, v3
	v_add_u32_e32 v5, v2, v5
	s_addc_u32 s41, s1, 0
	s_ashr_i32 s5, s36, 6
	v_and_b32_e32 v4, -16, v4
	v_ashrrev_i32_e32 v6, 6, v5
	v_add_u32_e32 v26, v6, v4
	v_and_b32_e32 v4, 3, v6
	s_lshl_b32 s43, s5, 10
	s_lshl_b32 s5, s5, 5
	s_waitcnt lgkmcnt(0)
	s_lshl_b32 s14, s94, 10
	v_and_or_b32 v4, v26, s7, v4
	s_ashr_i32 s8, s36, 8
	s_lshl_b32 s42, s6, 8
	s_and_b32 s7, s5, 0x60
	s_lshl_b64 s[10:11], s[14:15], 2
	s_add_u32 s2, s2, s10
	s_addc_u32 s3, s3, s11
	s_add_i32 s4, s9, s4
	s_ashr_i32 s5, s4, 31
	s_lshr_b32 s5, s5, 27
	s_add_i32 s5, s4, s5
	s_ashr_i32 s9, s5, 5
	s_and_b32 s5, s5, 0xffe0
	s_sub_i32 s4, s4, s5
	s_bfe_i32 s5, s4, 0x80000
	s_bfe_u32 s5, s5, 0x3000c
	s_add_i32 s5, s4, s5
	v_lshlrev_b32_e32 v3, 5, v3
	s_bfe_i32 s10, s5, 0x80000
	s_and_b32 s5, s5, 0xf8
	v_and_b32_e32 v21, 32, v3
	v_and_b32_e32 v3, 0xc0, v5
	s_sub_i32 s4, s4, s5
	v_sub_u32_e32 v2, v2, v3
	s_lshl_b32 s9, s9, 3
	s_sext_i32_i8 s4, s4
	v_ashrrev_i16_sdwa v2, v203, sext(v2) dst_sel:DWORD dst_unused:UNUSED_PAD src0_sel:DWORD src1_sel:BYTE_0
	s_sext_i32_i16 s10, s10
	s_add_i32 s56, s9, s4
	s_lshl_b32 s14, s6, 9
	v_bfe_i32 v22, v2, 0, 16
	v_lshlrev_b32_e32 v2, 1, v26
	v_lshrrev_b32_e32 v3, 2, v26
	s_ashr_i32 s57, s10, 3
	s_mul_i32 s5, s56, s14
	v_and_b32_e32 v2, 24, v2
	v_and_b32_e32 v3, 4, v3
	s_mul_hi_i32 s4, s56, s14
	s_add_u32 s12, s38, s5
	v_or3_b32 v2, v4, v3, v2
	s_addc_u32 s13, s39, s4
	s_mul_i32 s5, s57, s14
	v_add_u32_e32 v27, v21, v22
	v_mul_lo_u32 v2, v2, s6
	s_mul_hi_i32 s4, s57, s14
	s_add_u32 s22, s40, s5
	v_add_lshl_u32 v130, v2, v27, 1
	v_lshrrev_b32_e32 v2, 1, v18
	s_addc_u32 s23, s41, s4
	s_lshl_b32 s4, s57, 8
	v_and_b32_e32 v23, 24, v2
	s_or_b32 s4, s4, s7
	v_or_b32_e32 v2, s4, v23
	v_add_u32_e32 v25, v19, v20
	v_mul_lo_u32 v0, v0, s6
	v_ashrrev_i32_e32 v3, 31, v2
	s_add_i32 s44, s43, 0
	v_add_lshl_u32 v0, v0, v25, 1
	v_lshl_add_u64 v[6:7], v[2:3], 2, s[2:3]
	v_mul_lo_u32 v24, v24, s6
	s_lshl_b32 s4, s6, 7
	s_add_i32 m0, s44, 0x10000
	global_load_dwordx4 v[10:13], v[6:7], off offset:16
	global_load_dwordx4 v[14:17], v[6:7], off
	global_load_dwordx4 v[2:5], v[6:7], off offset:528
	s_nop 0
	global_load_dwordx4 v[6:9], v[6:7], off offset:512
	v_add_lshl_u32 v132, v25, v24, 1
	v_add_u32_e32 v24, s4, v24
	global_load_lds_dwordx4 v0, s[22:23]
	s_add_i32 m0, s44, 0x12000
	v_add_lshl_u32 v134, v25, v24, 1
	v_mul_lo_u32 v25, v26, s6
	global_load_lds_dwordx4 v130, s[22:23]
	s_mov_b32 m0, s44
	s_add_i32 s45, s44, 0x2000
	v_add_lshl_u32 v136, v27, v25, 1
	v_add_u32_e32 v25, s4, v25
	global_load_lds_dwordx4 v132, s[12:13]
	s_mov_b32 m0, s45
	s_add_u32 s4, s22, s42
	global_load_lds_dwordx4 v136, s[12:13]
	s_addc_u32 s5, s23, 0
	s_add_i32 m0, s44, 0x14000
	s_add_i32 s46, s44, 0x4000
	global_load_lds_dwordx4 v0, s[4:5]
	s_add_i32 m0, s44, 0x16000
	s_add_i32 s47, s44, 0x6000
	global_load_lds_dwordx4 v130, s[4:5]
	s_mov_b32 m0, s46
	v_add_lshl_u32 v138, v27, v25, 1
	global_load_lds_dwordx4 v134, s[12:13]
	s_mov_b32 m0, s47
	s_cmp_lg_u32 s8, 1
	global_load_lds_dwordx4 v138, s[12:13]
	s_cbranch_scc1 .LBB0_2243
	s_barrier
	s_setprio 1
	s_nop 0
	s_nop 0
	s_nop 0
	s_nop 0
	s_nop 0
	s_nop 0
	s_nop 0
	s_nop 0
	s_nop 0
	s_nop 0
	s_nop 0
	s_nop 0
	s_nop 0
	s_nop 0
	s_nop 0

; #define G8_STAGE(bufoff, gbase, voff) do { _Pragma("unroll") for (int _i = 0; _i < 2; ++_i) \
;         __builtin_amdgcn_global_load_lds((const unsigned*)((const char*)(gbase) + (voff)[_i]), (LAS unsigned*)(lds + (bufoff) + ldsw + _i * 8192), 16, 0, 0); } while (0)
; #define G8_LDA(dst, b, h) do { _Pragma("unroll") for (int m = 0; m < 4; ++m) _Pragma("unroll") for (int k = 0; k < 2; ++k) dst[m][k] = *(const LAS bf16x8*)(lds + G8_SA(b, h) + aoff + m * 2048 + k * 1024); } while (0)
; #define G8_LDB(dst, b, h) do { _Pragma("unroll") for (int n = 0; n < 2; ++n) _Pragma("unroll") for (int k = 0; k < 2; ++k) dst[n][k] = *(const LAS bf16x8*)(lds + G8_SB(b, h) + boff + n * 2048 + k * 1024); } while (0)
; #define G8_MMA(ai, bj, At, Bt) do { __builtin_amdgcn_s_setprio(1); _Pragma("unroll") for (int m = 0; m < 4; ++m) _Pragma("unroll") for (int n = 0; n < 2; ++n) _Pragma("unroll") for (int k = 0; k < 2; ++k) \
;         acc[ai][bj][m][n] = __builtin_amdgcn_mfma_f32_16x16x32_bf16(Bt[n][k], At[m][k], acc[ai][bj][m][n], 0, 0, 0); __builtin_amdgcn_s_setprio(0); } while (0)
; #define G8_WAIT_L(n) asm volatile("s_waitcnt lgkmcnt(" #n ")" ::: "memory")
; #define G8_BAR __builtin_amdgcn_s_barrier()
; template <class Epi, class Sched>
; __device__ __forceinline__ void gemm_phase(LAS unsigned char* lds, const int K, const Sched& S, const Epi& E) {
;     ...
;         const bool has_next = S.next(ui + 1, nxt);
;         const char* nA = has_next ? nxt.A : cA; const char* nB = has_next ? nxt.B : cB;
; #pragma unroll 1
;         for (int t = 0; t < nt; t += 2) {
;             const bool last = (t == nt - 2);
;             const char* a1 = cA + (size_t)(t + 1) * kstep;
;             const char* a2 = last ? nA : cA + (size_t)(t + 2) * kstep; const char* b2 = last ? nB : cB + (size_t)(t + 2) * kstep;
;             const char* a3 = a2 + kstep; const char* b3 = b2 + kstep;
;             G8_LDB(B0, 0, 0); G8_SCHED; G8_LDA(At, 0, 0); G8_STAGE(G8_SA(1, 1), a1, oc[1]);
;             if (last && has_next) S.aoff(nxt, tid, oc);
;             G8_WAIT_L(8); G8_BAR; G8_WAIT_L(0); G8_MMA(0, 0, At, B0); G8_BAR; G8_SCHED;
;             G8_LDB(B1, 0, 1); G8_STAGE(G8_SB(0, 0), b2, voffB);
;             G8_BAR; G8_WAIT_L(0); G8_MMA(0, 1, At, B1); G8_BAR;
;             G8_LDA(At, 0, 1); G8_STAGE(G8_SA(0, 0), a2, oc[0]);
;             G8_BAR; G8_WAIT_L(0); G8_MMA(1, 0, At, B0); G8_BAR; G8_SCHED;
.LBB0_2252:
	s_add_i32 s60, s22, 2
	s_add_u32 s24, s12, 0x80
	s_addc_u32 s23, s13, 0
	s_add_i32 s61, 0, 0x10000
	v_add_u32_e32 v144, s61, v148
	ds_read_b128 v[152:155], v144
	ds_read_b128 v[156:159], v144 offset:1024
	ds_read_b128 v[160:163], v144 offset:2048
	ds_read_b128 v[164:167], v144 offset:3072
	s_cmp_eq_u32 s51, s22
	s_cselect_b32 s22, s0, s24
	s_cselect_b32 s23, s1, s23
	s_cselect_b32 s25, s11, s59
	s_cselect_b32 s24, s10, s58
	v_lshl_add_u64 v[144:145], s[12:13], 0, v[140:141]
	s_add_i32 m0, s44, 0xc000
	ds_read_b128 v[168:171], v150
	ds_read_b128 v[172:175], v150 offset:1024
	ds_read_b128 v[176:179], v150 offset:2048
	ds_read_b128 v[180:183], v150 offset:3072
	ds_read_b128 v[184:187], v150 offset:4096
	ds_read_b128 v[188:191], v150 offset:5120
	ds_read_b128 v[192:195], v150 offset:6144
	ds_read_b128 v[196:199], v150 offset:7168
	global_load_lds_dwordx4 v[144:145], off
	v_lshl_add_u64 v[144:145], s[12:13], 0, v[142:143]
	s_add_i32 m0, s44, 0xe000
	s_nop 0
	global_load_lds_dwordx4 v[144:145], off
	s_waitcnt lgkmcnt(8)
	s_barrier
	s_waitcnt lgkmcnt(0)
	s_nop 0
	s_waitcnt lgkmcnt(0)
	v_mfma_f32_16x16x32_bf16 v[126:129], v[152:155], v[168:171], v[126:129]
	v_mfma_f32_16x16x32_bf16 v[122:125], v[160:163], v[168:171], v[122:125]
	v_mfma_f32_16x16x32_bf16 v[110:113], v[152:155], v[176:179], v[110:113]
	v_mfma_f32_16x16x32_bf16 v[106:109], v[160:163], v[176:179], v[106:109]
	v_mfma_f32_16x16x32_bf16 v[94:97], v[152:155], v[184:187], v[94:97]
	v_mfma_f32_16x16x32_bf16 v[90:93], v[160:163], v[184:187], v[90:93]
	v_mfma_f32_16x16x32_bf16 v[78:81], v[152:155], v[192:195], v[78:81]
	v_mfma_f32_16x16x32_bf16 v[74:77], v[160:163], v[192:195], v[74:77]
	v_mfma_f32_16x16x32_bf16 v[126:129], v[156:159], v[172:175], v[126:129]
	v_mfma_f32_16x16x32_bf16 v[122:125], v[164:167], v[172:175], v[122:125]
	v_mfma_f32_16x16x32_bf16 v[110:113], v[156:159], v[180:183], v[110:113]
	v_mfma_f32_16x16x32_bf16 v[106:109], v[164:167], v[180:183], v[106:109]
	v_mfma_f32_16x16x32_bf16 v[94:97], v[156:159], v[188:191], v[94:97]
	v_mfma_f32_16x16x32_bf16 v[90:93], v[164:167], v[188:191], v[90:93]
	v_mfma_f32_16x16x32_bf16 v[78:81], v[156:159], v[196:199], v[78:81]
	v_mfma_f32_16x16x32_bf16 v[74:77], v[164:167], v[196:199], v[74:77]
	s_nop 0
	s_barrier
	s_add_i32 s62, 0, 0x14000
	v_add_u32_e32 v144, s62, v148
	s_add_i32 s61, s61, s43
	ds_read_b128 v[216:219], v144
	ds_read_b128 v[220:223], v144 offset:1024
	ds_read_b128 v[224:227], v144 offset:2048
	ds_read_b128 v[228:231], v144 offset:3072
	v_lshl_add_u64 v[144:145], s[24:25], 0, v[0:1]
	s_mov_b32 m0, s61
	v_lshl_add_u64 v[200:201], s[24:25], 0, v[130:131]
	global_load_lds_dwordx4 v[144:145], off
	s_add_i32 m0, s61, 0x2000
	s_nop 0
	global_load_lds_dwordx4 v[200:201], off
	s_barrier
	s_waitcnt lgkmcnt(0)
	s_nop 0
	s_waitcnt lgkmcnt(0)
	v_mfma_f32_16x16x32_bf16 v[118:121], v[216:219], v[168:171], v[118:121]
	v_mfma_f32_16x16x32_bf16 v[114:117], v[224:227], v[168:171], v[114:117]
	v_mfma_f32_16x16x32_bf16 v[102:105], v[216:219], v[176:179], v[102:105]
	v_mfma_f32_16x16x32_bf16 v[98:101], v[224:227], v[176:179], v[98:101]
	v_mfma_f32_16x16x32_bf16 v[86:89], v[216:219], v[184:187], v[86:89]
	v_mfma_f32_16x16x32_bf16 v[82:85], v[224:227], v[184:187], v[82:85]
	v_mfma_f32_16x16x32_bf16 v[70:73], v[216:219], v[192:195], v[70:73]
	v_mfma_f32_16x16x32_bf16 v[66:69], v[224:227], v[192:195], v[66:69]
	v_mfma_f32_16x16x32_bf16 v[118:121], v[220:223], v[172:175], v[118:121]
	v_mfma_f32_16x16x32_bf16 v[114:117], v[228:231], v[172:175], v[114:117]
	v_mfma_f32_16x16x32_bf16 v[102:105], v[220:223], v[180:183], v[102:105]
	v_mfma_f32_16x16x32_bf16 v[98:101], v[228:231], v[180:183], v[98:101]
	v_mfma_f32_16x16x32_bf16 v[86:89], v[220:223], v[188:191], v[86:89]
	v_mfma_f32_16x16x32_bf16 v[82:85], v[228:231], v[188:191], v[82:85]
	v_mfma_f32_16x16x32_bf16 v[70:73], v[220:223], v[196:199], v[70:73]
	v_mfma_f32_16x16x32_bf16 v[66:69], v[228:231], v[196:199], v[66:69]
	s_nop 0
	s_mov_b32 m0, s44
	v_lshl_add_u64 v[232:233], s[22:23], 0, v[132:133]
	s_barrier
	ds_read_b128 v[168:171], v150 offset:16384
	ds_read_b128 v[172:175], v150 offset:17408
	ds_read_b128 v[176:179], v150 offset:18432
	ds_read_b128 v[180:183], v150 offset:19456
	ds_read_b128 v[184:187], v150 offset:20480
	ds_read_b128 v[188:191], v150 offset:21504
	ds_read_b128 v[192:195], v150 offset:22528
	ds_read_b128 v[196:199], v150 offset:23552
	global_load_lds_dwordx4 v[232:233], off
	v_lshl_add_u64 v[234:235], s[22:23], 0, v[136:137]
	s_mov_b32 m0, s45
	s_nop 0
	global_load_lds_dwordx4 v[234:235], off
	s_barrier
	s_waitcnt lgkmcnt(0)
	s_nop 0
	s_waitcnt lgkmcnt(0)
	v_mfma_f32_16x16x32_bf16 v[62:65], v[152:155], v[168:171], v[62:65]
	v_mfma_f32_16x16x32_bf16 v[58:61], v[160:163], v[168:171], v[58:61]
	v_mfma_f32_16x16x32_bf16 v[46:49], v[152:155], v[176:179], v[46:49]
	v_mfma_f32_16x16x32_bf16 v[42:45], v[160:163], v[176:179], v[42:45]
	v_mfma_f32_16x16x32_bf16 v[30:33], v[152:155], v[184:187], v[30:33]
	v_mfma_f32_16x16x32_bf16 v[26:29], v[160:163], v[184:187], v[26:29]
	v_mfma_f32_16x16x32_bf16 v[14:17], v[152:155], v[192:195], v[14:17]
	v_mfma_f32_16x16x32_bf16 v[10:13], v[160:163], v[192:195], v[10:13]
	v_mfma_f32_16x16x32_bf16 v[62:65], v[156:159], v[172:175], v[62:65]
	v_mfma_f32_16x16x32_bf16 v[58:61], v[164:167], v[172:175], v[58:61]
	v_mfma_f32_16x16x32_bf16 v[46:49], v[156:159], v[180:183], v[46:49]
	v_mfma_f32_16x16x32_bf16 v[42:45], v[164:167], v[180:183], v[42:45]
	v_mfma_f32_16x16x32_bf16 v[30:33], v[156:159], v[188:191], v[30:33]
	v_mfma_f32_16x16x32_bf16 v[26:29], v[164:167], v[188:191], v[26:29]
	v_mfma_f32_16x16x32_bf16 v[14:17], v[156:159], v[196:199], v[14:17]
	v_mfma_f32_16x16x32_bf16 v[10:13], v[164:167], v[196:199], v[10:13]
	s_nop 0
	s_barrier
; #define G8_STAGE(bufoff, gbase, voff) do { _Pragma("unroll") for (int _i = 0; _i < 2; ++_i) \
;         __builtin_amdgcn_global_load_lds((const unsigned*)((const char*)(gbase) + (voff)[_i]), (LAS unsigned*)(lds + (bufoff) + ldsw + _i * 8192), 16, 0, 0); } while (0)
; #define G8_LDA(dst, b, h) do { _Pragma("unroll") for (int m = 0; m < 4; ++m) _Pragma("unroll") for (int k = 0; k < 2; ++k) dst[m][k] = *(const LAS bf16x8*)(lds + G8_SA(b, h) + aoff + m * 2048 + k * 1024); } while (0)
; #define G8_LDB(dst, b, h) do { _Pragma("unroll") for (int n = 0; n < 2; ++n) _Pragma("unroll") for (int k = 0; k < 2; ++k) dst[n][k] = *(const LAS bf16x8*)(lds + G8_SB(b, h) + boff + n * 2048 + k * 1024); } while (0)
; #define G8_MMA(ai, bj, At, Bt) do { __builtin_amdgcn_s_setprio(1); _Pragma("unroll") for (int m = 0; m < 4; ++m) _Pragma("unroll") for (int n = 0; n < 2; ++n) _Pragma("unroll") for (int k = 0; k < 2; ++k) \
;         acc[ai][bj][m][n] = __builtin_amdgcn_mfma_f32_16x16x32_bf16(Bt[n][k], At[m][k], acc[ai][bj][m][n], 0, 0, 0); __builtin_amdgcn_s_setprio(0); } while (0)
; #define G8_WAIT_V(n) asm volatile("s_waitcnt vmcnt(" #n ")" ::: "memory")
; #define G8_WAIT_L(n) asm volatile("s_waitcnt lgkmcnt(" #n ")" ::: "memory")
; #define G8_BAR __builtin_amdgcn_s_barrier()
; #define G8_SCHED __builtin_amdgcn_sched_barrier(0)
; template <class Epi, class Sched>
; __device__ __forceinline__ void gemm_phase(LAS unsigned char* lds, const int K, const Sched& S, const Epi& E) {
;     ...
;             G8_STAGE(G8_SB(0, 1), b2 + hstep, voffB);
;             G8_WAIT_V(6); G8_BAR; G8_MMA(1, 1, At, B1); G8_BAR;
;             G8_LDB(B0, 1, 0); G8_SCHED; G8_LDA(At, 1, 0); G8_STAGE(G8_SA(0, 1), a2, oc[1]);
;             G8_WAIT_L(8); G8_BAR; G8_WAIT_L(0); G8_MMA(0, 0, At, B0); G8_BAR; G8_SCHED;
;             G8_LDB(B1, 1, 1); G8_STAGE(G8_SB(1, 0), b3, voffB);
;             G8_BAR; G8_WAIT_L(0); G8_MMA(0, 1, At, B1); G8_BAR;
;             G8_LDA(At, 1, 1); G8_STAGE(G8_SA(1, 0), a3, oc[0]);
	s_add_u32 s24, s24, s42
	s_addc_u32 s25, s25, 0
	s_add_i32 s61, s62, s43
	v_lshl_add_u64 v[236:237], s[24:25], 0, v[0:1]
	s_mov_b32 m0, s61
	v_lshl_add_u64 v[238:239], s[24:25], 0, v[130:131]
	global_load_lds_dwordx4 v[236:237], off
	s_add_i32 m0, s61, 0x2000
	s_nop 0
	global_load_lds_dwordx4 v[238:239], off
	s_waitcnt vmcnt(6)
	s_barrier
	s_nop 0
	v_mfma_f32_16x16x32_bf16 v[54:57], v[216:219], v[168:171], v[54:57]
	v_mfma_f32_16x16x32_bf16 v[50:53], v[224:227], v[168:171], v[50:53]
	v_mfma_f32_16x16x32_bf16 v[38:41], v[216:219], v[176:179], v[38:41]
	v_mfma_f32_16x16x32_bf16 v[34:37], v[224:227], v[176:179], v[34:37]
	v_mfma_f32_16x16x32_bf16 v[22:25], v[216:219], v[184:187], v[22:25]
	v_mfma_f32_16x16x32_bf16 v[18:21], v[224:227], v[184:187], v[18:21]
	v_mfma_f32_16x16x32_bf16 v[6:9], v[216:219], v[192:195], v[6:9]
	v_mfma_f32_16x16x32_bf16 v[2:5], v[224:227], v[192:195], v[2:5]
	v_mfma_f32_16x16x32_bf16 v[54:57], v[220:223], v[172:175], v[54:57]
	v_mfma_f32_16x16x32_bf16 v[50:53], v[228:231], v[172:175], v[50:53]
	v_mfma_f32_16x16x32_bf16 v[38:41], v[220:223], v[180:183], v[38:41]
	v_mfma_f32_16x16x32_bf16 v[34:37], v[228:231], v[180:183], v[34:37]
	v_mfma_f32_16x16x32_bf16 v[22:25], v[220:223], v[188:191], v[22:25]
	v_mfma_f32_16x16x32_bf16 v[18:21], v[228:231], v[188:191], v[18:21]
	v_mfma_f32_16x16x32_bf16 v[6:9], v[220:223], v[196:199], v[6:9]
	v_mfma_f32_16x16x32_bf16 v[2:5], v[228:231], v[196:199], v[2:5]
	s_nop 0
	s_add_i32 s24, 0, 0x18000
	v_add_u32_e32 v151, s24, v148
	s_barrier
	ds_read_b128 v[152:155], v151
	ds_read_b128 v[156:159], v151 offset:1024
	ds_read_b128 v[160:163], v151 offset:2048
	ds_read_b128 v[164:167], v151 offset:3072
	s_mov_b32 m0, s46
	v_lshl_add_u64 v[216:217], s[22:23], 0, v[134:135]
	ds_read_b128 v[168:171], v150 offset:32768
	ds_read_b128 v[172:175], v150 offset:33792
	ds_read_b128 v[176:179], v150 offset:34816
	ds_read_b128 v[180:183], v150 offset:35840
	ds_read_b128 v[184:187], v150 offset:36864
	ds_read_b128 v[188:191], v150 offset:37888
	ds_read_b128 v[192:195], v150 offset:38912
	ds_read_b128 v[196:199], v150 offset:39936
	global_load_lds_dwordx4 v[216:217], off
	v_lshl_add_u64 v[216:217], s[22:23], 0, v[138:139]
	s_mov_b32 m0, s47
	s_nop 0
	global_load_lds_dwordx4 v[216:217], off
	s_waitcnt lgkmcnt(8)
	s_barrier
	s_waitcnt lgkmcnt(0)
	s_nop 0
	s_waitcnt lgkmcnt(0)
	v_mfma_f32_16x16x32_bf16 v[126:129], v[152:155], v[168:171], v[126:129]
	v_mfma_f32_16x16x32_bf16 v[122:125], v[160:163], v[168:171], v[122:125]
	v_mfma_f32_16x16x32_bf16 v[110:113], v[152:155], v[176:179], v[110:113]
	v_mfma_f32_16x16x32_bf16 v[106:109], v[160:163], v[176:179], v[106:109]
	v_mfma_f32_16x16x32_bf16 v[94:97], v[152:155], v[184:187], v[94:97]
	v_mfma_f32_16x16x32_bf16 v[90:93], v[160:163], v[184:187], v[90:93]
	v_mfma_f32_16x16x32_bf16 v[78:81], v[152:155], v[192:195], v[78:81]
	v_mfma_f32_16x16x32_bf16 v[74:77], v[160:163], v[192:195], v[74:77]
	v_mfma_f32_16x16x32_bf16 v[126:129], v[156:159], v[172:175], v[126:129]
	v_mfma_f32_16x16x32_bf16 v[122:125], v[164:167], v[172:175], v[122:125]
	v_mfma_f32_16x16x32_bf16 v[110:113], v[156:159], v[180:183], v[110:113]
	v_mfma_f32_16x16x32_bf16 v[106:109], v[164:167], v[180:183], v[106:109]
	v_mfma_f32_16x16x32_bf16 v[94:97], v[156:159], v[188:191], v[94:97]
	v_mfma_f32_16x16x32_bf16 v[90:93], v[164:167], v[188:191], v[90:93]
	v_mfma_f32_16x16x32_bf16 v[78:81], v[156:159], v[196:199], v[78:81]
	v_mfma_f32_16x16x32_bf16 v[74:77], v[164:167], v[196:199], v[74:77]
	s_nop 0
	s_barrier
	s_add_i32 s22, 0, 0x1c000
	s_add_i32 s23, s24, s43
	v_add_u32_e32 v151, s22, v148
	v_lshl_add_u64 v[144:145], v[144:145], 0, s[18:19]
	s_mov_b32 m0, s23
	ds_read_b128 v[216:219], v151
	ds_read_b128 v[220:223], v151 offset:1024
	ds_read_b128 v[224:227], v151 offset:2048
	ds_read_b128 v[228:231], v151 offset:3072
	global_load_lds_dwordx4 v[144:145], off
	v_lshl_add_u64 v[144:145], v[200:201], 0, s[18:19]
	s_add_i32 m0, s23, 0x2000
	s_nop 0
	global_load_lds_dwordx4 v[144:145], off
	s_barrier
	s_waitcnt lgkmcnt(0)
	s_nop 0
	s_waitcnt lgkmcnt(0)
	v_mfma_f32_16x16x32_bf16 v[118:121], v[216:219], v[168:171], v[118:121]
	v_mfma_f32_16x16x32_bf16 v[114:117], v[224:227], v[168:171], v[114:117]
	v_mfma_f32_16x16x32_bf16 v[102:105], v[216:219], v[176:179], v[102:105]
	v_mfma_f32_16x16x32_bf16 v[98:101], v[224:227], v[176:179], v[98:101]
	v_mfma_f32_16x16x32_bf16 v[86:89], v[216:219], v[184:187], v[86:89]
	v_mfma_f32_16x16x32_bf16 v[82:85], v[224:227], v[184:187], v[82:85]
	v_mfma_f32_16x16x32_bf16 v[70:73], v[216:219], v[192:195], v[70:73]
	v_mfma_f32_16x16x32_bf16 v[66:69], v[224:227], v[192:195], v[66:69]
	v_mfma_f32_16x16x32_bf16 v[118:121], v[220:223], v[172:175], v[118:121]
	v_mfma_f32_16x16x32_bf16 v[114:117], v[228:231], v[172:175], v[114:117]
	v_mfma_f32_16x16x32_bf16 v[102:105], v[220:223], v[180:183], v[102:105]
	v_mfma_f32_16x16x32_bf16 v[98:101], v[228:231], v[180:183], v[98:101]
	v_mfma_f32_16x16x32_bf16 v[86:89], v[220:223], v[188:191], v[86:89]
	v_mfma_f32_16x16x32_bf16 v[82:85], v[228:231], v[188:191], v[82:85]
	v_mfma_f32_16x16x32_bf16 v[70:73], v[220:223], v[196:199], v[70:73]
	v_mfma_f32_16x16x32_bf16 v[66:69], v[228:231], v[196:199], v[66:69]
	s_nop 0
	s_mov_b32 m0, s48
	v_lshl_add_u64 v[144:145], v[232:233], 0, s[18:19]
	s_barrier
	ds_read_b128 v[168:171], v150 offset:49152
	ds_read_b128 v[172:175], v150 offset:50176
	ds_read_b128 v[176:179], v150 offset:51200
	ds_read_b128 v[180:183], v150 offset:52224
	ds_read_b128 v[184:187], v150 offset:53248
	ds_read_b128 v[188:191], v150 offset:54272
	ds_read_b128 v[192:195], v150 offset:55296
	ds_read_b128 v[196:199], v150 offset:56320
	global_load_lds_dwordx4 v[144:145], off
	v_lshl_add_u64 v[144:145], v[234:235], 0, s[18:19]
	s_mov_b32 m0, s49
	s_nop 0
	global_load_lds_dwordx4 v[144:145], off
	s_barrier
; #define G8_STAGE(bufoff, gbase, voff) do { _Pragma("unroll") for (int _i = 0; _i < 2; ++_i) \
;         __builtin_amdgcn_global_load_lds((const unsigned*)((const char*)(gbase) + (voff)[_i]), (LAS unsigned*)(lds + (bufoff) + ldsw + _i * 8192), 16, 0, 0); } while (0)
; #define G8_MMA(ai, bj, At, Bt) do { __builtin_amdgcn_s_setprio(1); _Pragma("unroll") for (int m = 0; m < 4; ++m) _Pragma("unroll") for (int n = 0; n < 2; ++n) _Pragma("unroll") for (int k = 0; k < 2; ++k) \
;         acc[ai][bj][m][n] = __builtin_amdgcn_mfma_f32_16x16x32_bf16(Bt[n][k], At[m][k], acc[ai][bj][m][n], 0, 0, 0); __builtin_amdgcn_s_setprio(0); } while (0)
; #define G8_WAIT_V(n) asm volatile("s_waitcnt vmcnt(" #n ")" ::: "memory")
; #define G8_WAIT_L(n) asm volatile("s_waitcnt lgkmcnt(" #n ")" ::: "memory")
; #define G8_BAR __builtin_amdgcn_s_barrier()
; #define G8_SCHED __builtin_amdgcn_sched_barrier(0)
; template <class Epi, class Sched>
; __device__ __forceinline__ void gemm_phase(LAS unsigned char* lds, const int K, const Sched& S, const Epi& E) {
;     ...
;             G8_BAR; G8_WAIT_L(0); G8_MMA(1, 0, At, B0); G8_BAR; G8_SCHED;
;             G8_STAGE(G8_SB(1, 1), b3 + hstep, voffB);
;             G8_WAIT_V(6); G8_BAR; G8_MMA(1, 1, At, B1); G8_BAR;
;         }
	s_waitcnt lgkmcnt(0)
	s_nop 0
	s_waitcnt lgkmcnt(0)
	v_mfma_f32_16x16x32_bf16 v[62:65], v[152:155], v[168:171], v[62:65]
	v_mfma_f32_16x16x32_bf16 v[58:61], v[160:163], v[168:171], v[58:61]
	v_mfma_f32_16x16x32_bf16 v[46:49], v[152:155], v[176:179], v[46:49]
	v_mfma_f32_16x16x32_bf16 v[42:45], v[160:163], v[176:179], v[42:45]
	v_mfma_f32_16x16x32_bf16 v[30:33], v[152:155], v[184:187], v[30:33]
	v_mfma_f32_16x16x32_bf16 v[26:29], v[160:163], v[184:187], v[26:29]
	v_mfma_f32_16x16x32_bf16 v[14:17], v[152:155], v[192:195], v[14:17]
	v_mfma_f32_16x16x32_bf16 v[10:13], v[160:163], v[192:195], v[10:13]
	v_mfma_f32_16x16x32_bf16 v[62:65], v[156:159], v[172:175], v[62:65]
	v_mfma_f32_16x16x32_bf16 v[58:61], v[164:167], v[172:175], v[58:61]
	v_mfma_f32_16x16x32_bf16 v[46:49], v[156:159], v[180:183], v[46:49]
	v_mfma_f32_16x16x32_bf16 v[42:45], v[164:167], v[180:183], v[42:45]
	v_mfma_f32_16x16x32_bf16 v[30:33], v[156:159], v[188:191], v[30:33]
	v_mfma_f32_16x16x32_bf16 v[26:29], v[164:167], v[188:191], v[26:29]
	v_mfma_f32_16x16x32_bf16 v[14:17], v[156:159], v[196:199], v[14:17]
	v_mfma_f32_16x16x32_bf16 v[10:13], v[164:167], v[196:199], v[10:13]
	s_nop 0
	s_barrier
	s_add_i32 s22, s22, s43
	v_lshl_add_u64 v[144:145], v[236:237], 0, s[18:19]
	s_mov_b32 m0, s22
	s_nop 0
	global_load_lds_dwordx4 v[144:145], off
	v_lshl_add_u64 v[144:145], v[238:239], 0, s[18:19]
	s_add_i32 m0, s22, 0x2000
	s_nop 0
	global_load_lds_dwordx4 v[144:145], off
	s_waitcnt vmcnt(6)
	s_barrier
	s_nop 0
	v_mfma_f32_16x16x32_bf16 v[54:57], v[216:219], v[168:171], v[54:57]
	v_mfma_f32_16x16x32_bf16 v[50:53], v[224:227], v[168:171], v[50:53]
	v_mfma_f32_16x16x32_bf16 v[38:41], v[216:219], v[176:179], v[38:41]
	v_mfma_f32_16x16x32_bf16 v[34:37], v[224:227], v[176:179], v[34:37]
	v_mfma_f32_16x16x32_bf16 v[22:25], v[216:219], v[184:187], v[22:25]
	v_mfma_f32_16x16x32_bf16 v[18:21], v[224:227], v[184:187], v[18:21]
	v_mfma_f32_16x16x32_bf16 v[6:9], v[216:219], v[192:195], v[6:9]
	v_mfma_f32_16x16x32_bf16 v[2:5], v[224:227], v[192:195], v[2:5]
	v_mfma_f32_16x16x32_bf16 v[54:57], v[220:223], v[172:175], v[54:57]
	v_mfma_f32_16x16x32_bf16 v[50:53], v[228:231], v[172:175], v[50:53]
	v_mfma_f32_16x16x32_bf16 v[38:41], v[220:223], v[180:183], v[38:41]
	v_mfma_f32_16x16x32_bf16 v[34:37], v[228:231], v[180:183], v[34:37]
	v_mfma_f32_16x16x32_bf16 v[22:25], v[220:223], v[188:191], v[22:25]
	v_mfma_f32_16x16x32_bf16 v[18:21], v[228:231], v[188:191], v[18:21]
	v_mfma_f32_16x16x32_bf16 v[6:9], v[220:223], v[196:199], v[6:9]
	v_mfma_f32_16x16x32_bf16 v[2:5], v[228:231], v[196:199], v[2:5]
	s_nop 0
	s_add_u32 s12, s12, 0x100
	s_addc_u32 s13, s13, 0
	s_add_u32 s58, s58, 0x100
	s_addc_u32 s59, s59, 0
	s_cmp_ge_u32 s60, s50
	s_mov_b32 s22, s60
	s_barrier
	s_cbranch_scc0 .LBB0_2252
; __device__ __forceinline__ unsigned cvt_pk_bf16(float lo, float hi) { unsigned r; asm volatile("v_cvt_pk_bf16_f32 %0, %1, %2" : "=v"(r) : "v"(lo), "v"(hi)); return r; }
;     __device__ __forceinline__ void operator()(const f32x4 (&acc)[2][2][4][2], const Unit& u, int wr, int wc, int fr, int fq) const {
;         const int row0 = u.pm * BM + wr * 64 + fr, col0 = u.pn * BM + wc * 32 + 8 * fq;
; #pragma unroll
;         for (int ai = 0; ai < 2; ++ai)
; #pragma unroll
;             for (int m = 0; m < 4; ++m) { bf16_t* rowp = O + (size_t)(row0 + ai * HALF + m * 16) * ldc + col0;
; #pragma unroll
;                 for (int bj = 0; bj < 2; ++bj) { const f32x4 v0 = acc[ai][bj][m][0], v1 = acc[ai][bj][m][1];
;                     u32x4 w; w[0] = cvt_pk_bf16(v0[0], v0[1]); w[1] = cvt_pk_bf16(v0[2], v0[3]); w[2] = cvt_pk_bf16(v1[0], v1[1]); w[3] = cvt_pk_bf16(v1[2], v1[3]);
;                     *(u32x4*)(rowp + bj * HALF) = w; } }
;     }
; template <class Epi, class Sched>
; __device__ __forceinline__ void gemm_phase(LAS unsigned char* lds, const int K, const Sched& S, const Epi& E) {
;     ...
;         E(acc, cur, wr, wc, fr, fq);
;         if (!has_next) break;
;         cur = nxt; cA = nA; cB = nB; ++ui;
;         E.init(acc, cur, wc, fq);
	s_nop 0
	s_nop 0
	s_nop 0
	s_nop 0
	s_nop 0
	s_nop 0
	s_nop 0
	s_nop 0
	s_nop 0
	v_lshl_add_u32 v152, s56, 8, v147
	v_lshl_or_b32 v144, s57, 8, v149
	v_ashrrev_i32_e32 v153, 31, v152
	v_ashrrev_i32_e32 v145, 31, v144
	v_lshlrev_b64 v[154:155], 11, v[152:153]
	v_lshl_add_u64 v[154:155], s[4:5], 0, v[154:155]
	v_lshlrev_b64 v[156:157], 1, v[144:145]
	v_lshl_add_u64 v[144:145], v[154:155], 0, v[156:157]
	v_cvt_pk_bf16_f32 v126, v126, v127
	v_cvt_pk_bf16_f32 v127, v128, v129
	v_cvt_pk_bf16_f32 v128, v122, v123
	v_cvt_pk_bf16_f32 v129, v124, v125
	global_store_dwordx4 v[144:145], v[126:129], off
	v_cvt_pk_bf16_f32 v118, v118, v119
	v_cvt_pk_bf16_f32 v119, v120, v121
	v_cvt_pk_bf16_f32 v120, v114, v115
	v_or_b32_e32 v114, 16, v152
	v_ashrrev_i32_e32 v115, 31, v114
	v_lshlrev_b64 v[114:115], 11, v[114:115]
	v_lshl_add_u64 v[114:115], s[4:5], 0, v[114:115]
	v_lshl_add_u64 v[114:115], v[114:115], 0, v[156:157]
	v_cvt_pk_bf16_f32 v121, v116, v117
	global_store_dwordx4 v[144:145], v[118:121], off offset:256
	v_cvt_pk_bf16_f32 v110, v110, v111
	v_cvt_pk_bf16_f32 v111, v112, v113
	v_cvt_pk_bf16_f32 v112, v106, v107
	v_cvt_pk_bf16_f32 v113, v108, v109
	global_store_dwordx4 v[114:115], v[110:113], off
	v_cvt_pk_bf16_f32 v102, v102, v103
	v_cvt_pk_bf16_f32 v103, v104, v105
	v_cvt_pk_bf16_f32 v104, v98, v99
	v_or_b32_e32 v98, 32, v152
	v_ashrrev_i32_e32 v99, 31, v98
	v_lshlrev_b64 v[98:99], 11, v[98:99]
	v_lshl_add_u64 v[98:99], s[4:5], 0, v[98:99]
	v_lshl_add_u64 v[98:99], v[98:99], 0, v[156:157]
	v_cvt_pk_bf16_f32 v105, v100, v101
	global_store_dwordx4 v[114:115], v[102:105], off offset:256
	v_cvt_pk_bf16_f32 v94, v94, v95
	v_cvt_pk_bf16_f32 v95, v96, v97
	v_cvt_pk_bf16_f32 v96, v90, v91
	v_cvt_pk_bf16_f32 v97, v92, v93
	global_store_dwordx4 v[98:99], v[94:97], off
	v_cvt_pk_bf16_f32 v86, v86, v87
	v_cvt_pk_bf16_f32 v87, v88, v89
	v_cvt_pk_bf16_f32 v88, v82, v83
	v_or_b32_e32 v82, 48, v152
	v_ashrrev_i32_e32 v83, 31, v82
	v_lshlrev_b64 v[82:83], 11, v[82:83]
	v_lshl_add_u64 v[82:83], s[4:5], 0, v[82:83]
	v_lshl_add_u64 v[82:83], v[82:83], 0, v[156:157]
	s_mov_b64 s[0:1], 0x40000
	v_cvt_pk_bf16_f32 v89, v84, v85
	global_store_dwordx4 v[98:99], v[86:89], off offset:256
	v_cvt_pk_bf16_f32 v78, v78, v79
	v_cvt_pk_bf16_f32 v79, v80, v81
	v_cvt_pk_bf16_f32 v80, v74, v75
	v_cvt_pk_bf16_f32 v81, v76, v77
	global_store_dwordx4 v[82:83], v[78:81], off
	v_cvt_pk_bf16_f32 v70, v70, v71
	v_cvt_pk_bf16_f32 v71, v72, v73
	v_cvt_pk_bf16_f32 v72, v66, v67
	v_cvt_pk_bf16_f32 v73, v68, v69
	global_store_dwordx4 v[82:83], v[70:73], off offset:256
	v_lshl_add_u64 v[66:67], v[144:145], 0, s[0:1]
	v_cvt_pk_bf16_f32 v62, v62, v63
	v_cvt_pk_bf16_f32 v63, v64, v65
	v_cvt_pk_bf16_f32 v64, v58, v59
	v_add_co_u32_e64 v58, s[0:1], s82, v144
	v_cvt_pk_bf16_f32 v65, v60, v61
	s_and_b64 vcc, exec, vcc
	s_nop 0
	v_addc_co_u32_e64 v59, s[0:1], 0, v145, s[0:1]
	s_mov_b64 s[0:1], 0x48000
	global_store_dwordx4 v[58:59], v[62:65], off
	v_cvt_pk_bf16_f32 v54, v54, v55
	v_cvt_pk_bf16_f32 v55, v56, v57
	v_cvt_pk_bf16_f32 v56, v50, v51
	v_lshl_add_u64 v[50:51], v[144:145], 0, s[0:1]
	s_mov_b32 s0, 0x48000
	v_cvt_pk_bf16_f32 v57, v52, v53
	global_store_dwordx4 v[66:67], v[54:57], off offset:256
	v_cvt_pk_bf16_f32 v46, v46, v47
	v_cvt_pk_bf16_f32 v47, v48, v49
	v_cvt_pk_bf16_f32 v48, v42, v43
	v_add_co_u32_e64 v42, s[0:1], s0, v144
	v_cvt_pk_bf16_f32 v49, v44, v45
	s_nop 1
	v_addc_co_u32_e64 v43, s[0:1], 0, v145, s[0:1]
	s_mov_b64 s[0:1], 0x50000
	global_store_dwordx4 v[42:43], v[46:49], off
	v_cvt_pk_bf16_f32 v38, v38, v39
	v_cvt_pk_bf16_f32 v39, v40, v41
	v_cvt_pk_bf16_f32 v40, v34, v35
	v_lshl_add_u64 v[34:35], v[144:145], 0, s[0:1]
	s_mov_b32 s0, 0x50000
	v_cvt_pk_bf16_f32 v41, v36, v37
	global_store_dwordx4 v[50:51], v[38:41], off offset:256
	v_cvt_pk_bf16_f32 v30, v30, v31
	v_cvt_pk_bf16_f32 v31, v32, v33
	v_cvt_pk_bf16_f32 v32, v26, v27
	v_add_co_u32_e64 v26, s[0:1], s0, v144
	v_cvt_pk_bf16_f32 v33, v28, v29
	s_nop 1
	v_addc_co_u32_e64 v27, s[0:1], 0, v145, s[0:1]
	s_mov_b64 s[0:1], 0x58000
	global_store_dwordx4 v[26:27], v[30:33], off
	v_cvt_pk_bf16_f32 v22, v22, v23
	v_cvt_pk_bf16_f32 v23, v24, v25
	v_cvt_pk_bf16_f32 v24, v18, v19
	v_lshl_add_u64 v[18:19], v[144:145], 0, s[0:1]
	s_mov_b32 s0, 0x58000
	v_cvt_pk_bf16_f32 v25, v20, v21
	global_store_dwordx4 v[34:35], v[22:25], off offset:256
	v_cvt_pk_bf16_f32 v14, v14, v15
	v_cvt_pk_bf16_f32 v15, v16, v17
	v_cvt_pk_bf16_f32 v16, v10, v11
	v_add_co_u32_e64 v10, s[0:1], s0, v144
	v_cvt_pk_bf16_f32 v17, v12, v13
	s_nop 1
	v_addc_co_u32_e64 v11, s[0:1], 0, v145, s[0:1]
	global_store_dwordx4 v[10:11], v[14:17], off
	v_cvt_pk_bf16_f32 v6, v6, v7
	v_cvt_pk_bf16_f32 v7, v8, v9
	v_cvt_pk_bf16_f32 v8, v2, v3
	v_cvt_pk_bf16_f32 v9, v4, v5
	s_mov_b64 s[0:1], -1
	global_store_dwordx4 v[18:19], v[6:9], off offset:256
	s_cbranch_vccz .LBB0_2244
	v_lshl_or_b32 v2, s54, 8, v149
	v_ashrrev_i32_e32 v3, 31, v2
	v_lshl_add_u64 v[6:7], v[2:3], 2, s[2:3]
	global_load_dwordx4 v[10:13], v[6:7], off offset:16
	global_load_dwordx4 v[14:17], v[6:7], off
	global_load_dwordx4 v[2:5], v[6:7], off offset:528
	s_nop 0
	global_load_dwordx4 v[6:9], v[6:7], off offset:512
	s_mov_b64 s[0:1], 0
	s_branch .LBB0_2244

; #define G8_WAIT_V(n) asm volatile("s_waitcnt vmcnt(" #n ")" ::: "memory")
; #define G8_BAR __builtin_amdgcn_s_barrier()
; template <class Epi, class Sched>
; __device__ __forceinline__ void gemm_phase(LAS unsigned char* lds, const int K, const Sched& S, const Epi& E) {
;     ...
;     G8_WAIT_V(0);
;     if (wr == 0) G8_BAR;
;     G8_BAR;
.LBB0_2269:
	v_readlane_b32 s46, v254, 41
	s_barrier
	s_setprio 0
	s_nop 0
	s_nop 0
	s_nop 0
	s_nop 0
	s_nop 0
	s_nop 0
	s_nop 0
	s_nop 0
	s_nop 0
	s_nop 0
	s_nop 0
	s_nop 0
	s_nop 0
	s_nop 0
	s_nop 0

; #define G8_STAGE(bufoff, gbase, voff) do { _Pragma("unroll") for (int _i = 0; _i < 2; ++_i) \
;         __builtin_amdgcn_global_load_lds((const unsigned*)((const char*)(gbase) + (voff)[_i]), (LAS unsigned*)(lds + (bufoff) + ldsw + _i * 8192), 16, 0, 0); } while (0)
; #define G8_WAIT_V(n) asm volatile("s_waitcnt vmcnt(" #n ")" ::: "memory")
; #define G8_BAR __builtin_amdgcn_s_barrier()
; template <class Epi, class Sched>
; __device__ __forceinline__ void gemm_phase(LAS unsigned char* lds, const int K, const Sched& S, const Epi& E) {
;     int tid_ = S.tid0; asm volatile("" : "+v"(tid_));
;     const int tid = tid_, wid = __builtin_amdgcn_readfirstlane(tid >> 6), lane = tid & 63, wr = wid >> 2, wc = wid & 3, fr = lane & 15, fq = lane >> 4;
;     const int nt = K / BK;
;     unsigned voffB[2];
; #pragma unroll
;     for (int i = 0; i < 2; ++i) { int R, C; stage_rc(tid * 16 + i * 8192, R, C); const int Rb = Epi::PERM ? ((R & ~31) + perm32(R & 31)) : R;
;         voffB[i] = (unsigned)(Rb * K + C) * 2u; }
;     const size_t kstep = (size_t)(BK * 2);
;     const size_t hstep = (size_t)HALF * K * 2;
;     const unsigned ldsw = (unsigned)wid * 1024u;
;     const int aoff = lds_byte(wr * 64 + fr, fq * 8), boff = lds_byte(wc * 32 + fr, fq * 8);
;     ...
;     Unit cur, nxt; int ui = 0;
;     if (!S.next(0, cur)) return;
;     f32x4 acc[2][2][4][2];
;     E.init(acc, cur, wc, fq);
;     bf16x8 At[4][2], B0[2][2], B1[2][2];
;     unsigned oc[2][2];
;     S.aoff(cur, tid, oc);
;     const char* cA = cur.A; const char* cB = cur.B;
;     G8_STAGE(G8_SB(0, 0), cB, voffB); G8_STAGE(G8_SA(0, 0), cA, oc[0]); G8_STAGE(G8_SB(0, 1), cB + hstep, voffB); G8_STAGE(G8_SA(0, 1), cA, oc[1]);
;     if (wr == 1) G8_BAR;
;     G8_WAIT_V(4); G8_BAR;
;     G8_STAGE(G8_SB(1, 0), cB + kstep, voffB); G8_STAGE(G8_SA(1, 0), cA + kstep, oc[0]); G8_STAGE(G8_SB(1, 1), cB + hstep + kstep, voffB);
;     G8_WAIT_V(6); G8_BAR;
;     __device__ __forceinline__ void aoff(const g8::Unit& u, int tid, unsigned (&o)[2][2]) const {
; #pragma unroll
;         for (int i = 0; i < 2; ++i) { int R, C; g8::stage_rc(tid * 16 + i * 8192, R, C);
; #pragma unroll
;             for (int h = 0; h < 2; ++h) { int s = tab[u.aux * 256 + h * 128 + R]; s = s < 0 ? 0 : s; const int row = mode ? s : (s < TK ? (s >> 3) : s - TK);
;                 o[h][i] = (unsigned)(row * K + C) * 2u; } }
;     }
.LBB0_2518:
	v_bfe_i32 v3, v10, 27, 1
	v_lshlrev_b32_e32 v0, 4, v10
	v_lshrrev_b32_e32 v3, 22, v3
	v_add_u32_e32 v3, v0, v3
	v_and_b32_e32 v3, 0xfffffc00, v3
	v_sub_u32_e32 v3, v0, v3
	v_lshrrev_b32_e32 v4, 4, v3
	v_bitop3_b32 v3, v4, v3, 32 bitop3:0x6c
	v_ashrrev_i32_e32 v5, 31, v3
	v_ashrrev_i32_e32 v2, 31, v10
	v_lshrrev_b32_e32 v5, 26, v5
	v_lshrrev_b32_e32 v2, 26, v2
	v_add_u32_e32 v5, v3, v5
	v_add_u32_e32 v2, v10, v2
	v_ashrrev_i32_e32 v6, 6, v5
	v_and_b32_e32 v5, 0xc0, v5
	v_ashrrev_i32_e32 v2, 6, v2
	v_sub_u32_e32 v3, v3, v5
	v_lshlrev_b32_e32 v4, 3, v2
	v_lshlrev_b32_e32 v2, 5, v2
	v_ashrrev_i16_sdwa v3, v203, sext(v3) dst_sel:DWORD dst_unused:UNUSED_PAD src0_sel:DWORD src1_sel:BYTE_0
	v_and_b32_e32 v2, 32, v2
	v_bfe_i32 v3, v3, 0, 16
	v_add_u32_e32 v0, 0x2000, v0
	v_add_lshl_u32 v192, v2, v3, 1
	v_ashrrev_i32_e32 v2, 31, v0
	v_lshrrev_b32_e32 v2, 22, v2
	v_add_u32_e32 v2, v0, v2
	v_and_b32_e32 v4, -16, v4
	v_ashrrev_i32_e32 v2, 10, v2
	v_add_u32_e32 v7, v6, v4
	v_mul_i32_i24_e32 v3, 0x400, v2
	v_lshlrev_b32_e32 v5, 1, v7
	v_lshrrev_b32_e32 v8, 2, v7
	v_and_b32_e32 v9, 3, v6
	s_mov_b32 s9, 0x1fffe0
	v_sub_u32_e32 v0, v0, v3
	v_and_b32_e32 v5, 24, v5
	v_and_b32_e32 v8, 4, v8
	v_and_or_b32 v7, v7, s9, v9
	v_lshrrev_b32_e32 v3, 4, v0
	v_or3_b32 v5, v7, v8, v5
	v_bitop3_b32 v0, v3, v0, 32 bitop3:0x6c
	v_lshl_add_u32 v178, v5, 11, v192
	v_ashrrev_i32_e32 v5, 31, v0
	v_lshrrev_b32_e32 v5, 26, v5
	v_add_u32_e32 v5, v0, v5
	v_ashrrev_i32_e32 v7, 6, v5
	v_and_b32_e32 v5, 0xc0, v5
	v_sub_u32_e32 v0, v0, v5
	v_lshlrev_b32_e32 v3, 3, v2
	v_lshlrev_b32_e32 v2, 5, v2
	v_ashrrev_i16_sdwa v0, v203, sext(v0) dst_sel:DWORD dst_unused:UNUSED_PAD src0_sel:DWORD src1_sel:BYTE_0
	v_and_b32_e32 v2, 32, v2
	v_bfe_i32 v0, v0, 0, 16
	v_lshlrev_b32_e32 v194, 2, v6
	s_add_i32 s10, 0, 0x20000
	v_lshlrev_b32_e32 v195, 2, v4
	v_add_lshl_u32 v193, v2, v0, 1
	v_add3_u32 v0, s10, v194, v195
	v_and_b32_e32 v3, -16, v3
	ds_read_b32 v0, v0
	v_add_u32_e32 v8, v7, v3
	v_lshlrev_b32_e32 v5, 1, v8
	v_lshrrev_b32_e32 v9, 2, v8
	v_and_b32_e32 v11, 3, v7
	v_readlane_b32 s11, v253, 52
	v_lshlrev_b32_e32 v196, 2, v7
	v_lshlrev_b32_e32 v197, 2, v3
	v_and_b32_e32 v5, 24, v5
	v_and_b32_e32 v9, 4, v9
	v_and_or_b32 v8, v8, s9, v11
	v_add3_u32 v2, s11, v194, v195
	v_add3_u32 v3, s10, v196, v197
	v_add3_u32 v4, s11, v196, v197
	v_or3_b32 v5, v8, v9, v5
	ds_read_b32 v2, v2
	ds_read_b32 v3, v3
	ds_read_b32 v4, v4
	v_lshl_add_u32 v180, v5, 11, v193
	s_waitcnt lgkmcnt(3)
	v_max_i32_e32 v5, 0, v0
	s_ashr_i32 s9, s40, 6
	v_lshrrev_b32_e32 v6, 3, v5
	v_add_u32_e32 v5, 0x1e0000, v5
	v_cmp_gt_i32_e32 vcc, s33, v0
	s_lshl_b32 s41, s9, 10
	s_add_i32 s42, s41, 0
	v_cndmask_b32_e32 v0, v5, v6, vcc
	s_waitcnt lgkmcnt(2)
	v_max_i32_e32 v5, 0, v2
	v_lshrrev_b32_e32 v6, 3, v5
	v_add_u32_e32 v5, 0x1e0000, v5
	v_cmp_gt_i32_e32 vcc, s33, v2
	s_add_i32 s43, s42, 0x10000
	s_mov_b32 m0, s43
	v_cndmask_b32_e32 v2, v5, v6, vcc
	v_lshl_add_u32 v184, v2, 11, v192
	s_waitcnt lgkmcnt(1)
	v_max_i32_e32 v2, 0, v3
	s_add_i32 s44, s42, 0x12000
	v_lshrrev_b32_e32 v5, 3, v2
	v_add_u32_e32 v2, 0x1e0000, v2
	v_cmp_gt_i32_e32 vcc, s33, v3
	global_load_lds_dwordx4 v178, s[24:25]
	s_mov_b32 m0, s44
	s_ashr_i32 s8, s40, 8
	v_lshl_add_u32 v0, v0, 11, v192
	v_cndmask_b32_e32 v2, v2, v5, vcc
	global_load_lds_dwordx4 v180, s[24:25]
	s_mov_b32 m0, s42
	s_add_i32 s45, s42, 0x2000
	v_lshl_add_u32 v182, v2, 11, v193
	global_load_lds_dwordx4 v0, s[0:1]
	s_mov_b32 m0, s45
	s_add_u32 s10, s24, 0x40000
	s_waitcnt lgkmcnt(0)
	v_max_i32_e32 v2, 0, v4
	global_load_lds_dwordx4 v182, s[0:1]
	s_addc_u32 s11, s25, 0
	s_add_i32 m0, s42, 0x14000
	v_lshrrev_b32_e32 v3, 3, v2
	v_add_u32_e32 v2, 0x1e0000, v2
	v_cmp_gt_i32_e32 vcc, s33, v4
	global_load_lds_dwordx4 v178, s[10:11]
	s_add_i32 m0, s42, 0x16000
	s_add_i32 s46, s42, 0x4000
	v_cndmask_b32_e32 v2, v2, v3, vcc
	global_load_lds_dwordx4 v180, s[10:11]
	s_mov_b32 m0, s46
	s_add_i32 s47, s42, 0x6000
	v_lshl_add_u32 v186, v2, 11, v193
	global_load_lds_dwordx4 v184, s[0:1]
	s_mov_b32 m0, s47
	v_mov_b32_e32 v179, v1
	global_load_lds_dwordx4 v186, s[0:1]
	v_mov_b32_e32 v181, v1
	v_mov_b32_e32 v183, v1
	v_lshl_add_u64 v[8:9], s[24:25], 0, v[178:179]
	v_lshl_add_u64 v[6:7], s[24:25], 0, v[180:181]
	v_lshl_add_u64 v[4:5], s[0:1], 0, v[0:1]
	s_cmp_lg_u32 s8, 1
	v_lshl_add_u64 v[2:3], s[0:1], 0, v[182:183]
	s_cbranch_scc1 .LBB0_2520
	s_barrier
	s_setprio 1
	s_nop 0
	s_nop 0
	s_nop 0
	s_nop 0
	s_nop 0
	s_nop 0
	s_nop 0
	s_nop 0
	s_nop 0
	s_nop 0
	s_nop 0
	s_nop 0
	s_nop 0
	s_nop 0
	s_nop 0

; #define G8_STAGE(bufoff, gbase, voff) do { _Pragma("unroll") for (int _i = 0; _i < 2; ++_i) \
;         __builtin_amdgcn_global_load_lds((const unsigned*)((const char*)(gbase) + (voff)[_i]), (LAS unsigned*)(lds + (bufoff) + ldsw + _i * 8192), 16, 0, 0); } while (0)
; #define G8_LDA(dst, b, h) do { _Pragma("unroll") for (int m = 0; m < 4; ++m) _Pragma("unroll") for (int k = 0; k < 2; ++k) dst[m][k] = *(const LAS bf16x8*)(lds + G8_SA(b, h) + aoff + m * 2048 + k * 1024); } while (0)
; #define G8_LDB(dst, b, h) do { _Pragma("unroll") for (int n = 0; n < 2; ++n) _Pragma("unroll") for (int k = 0; k < 2; ++k) dst[n][k] = *(const LAS bf16x8*)(lds + G8_SB(b, h) + boff + n * 2048 + k * 1024); } while (0)
; #define G8_MMA(ai, bj, At, Bt) do { __builtin_amdgcn_s_setprio(1); _Pragma("unroll") for (int m = 0; m < 4; ++m) _Pragma("unroll") for (int n = 0; n < 2; ++n) _Pragma("unroll") for (int k = 0; k < 2; ++k) \
;         acc[ai][bj][m][n] = __builtin_amdgcn_mfma_f32_16x16x32_bf16(Bt[n][k], At[m][k], acc[ai][bj][m][n], 0, 0, 0); __builtin_amdgcn_s_setprio(0); } while (0)
; #define G8_WAIT_V(n) asm volatile("s_waitcnt vmcnt(" #n ")" ::: "memory")
; #define G8_WAIT_L(n) asm volatile("s_waitcnt lgkmcnt(" #n ")" ::: "memory")
; #define G8_BAR __builtin_amdgcn_s_barrier()
; #define G8_SCHED __builtin_amdgcn_sched_barrier(0)
; template <class Epi, class Sched>
; __device__ __forceinline__ void gemm_phase(LAS unsigned char* lds, const int K, const Sched& S, const Epi& E) {
;     ...
;             G8_WAIT_L(8); G8_BAR; G8_WAIT_L(0); G8_MMA(0, 0, At, B0); G8_BAR; G8_SCHED;
;             G8_LDB(B1, 0, 1); G8_STAGE(G8_SB(0, 0), b2, voffB);
;             G8_BAR; G8_WAIT_L(0); G8_MMA(0, 1, At, B1); G8_BAR;
;             G8_LDA(At, 0, 1); G8_STAGE(G8_SA(0, 0), a2, oc[0]);
;             G8_BAR; G8_WAIT_L(0); G8_MMA(1, 0, At, B0); G8_BAR; G8_SCHED;
;             G8_STAGE(G8_SB(0, 1), b2 + hstep, voffB);
;             G8_WAIT_V(6); G8_BAR; G8_MMA(1, 1, At, B1); G8_BAR;
.LBB0_2526:
	s_add_u32 s34, s22, 0x80
	s_waitcnt lgkmcnt(8)
	s_barrier
	s_waitcnt lgkmcnt(0)
	s_addc_u32 s35, s23, 0
	s_and_b64 s[24:25], s[24:25], exec
	s_cselect_b32 s35, s1, s35
	s_cselect_b32 s34, s0, s34
	s_cselect_b32 s25, s13, s56
	s_cselect_b32 s24, s12, s55
	s_nop 0
	s_waitcnt lgkmcnt(0)
	v_mfma_f32_16x16x32_bf16 v[126:129], v[130:133], v[170:173], v[126:129]
	v_mfma_f32_16x16x32_bf16 v[122:125], v[138:141], v[170:173], v[122:125]
	v_mfma_f32_16x16x32_bf16 v[110:113], v[130:133], v[162:165], v[110:113]
	v_mfma_f32_16x16x32_bf16 v[106:109], v[138:141], v[162:165], v[106:109]
	v_mfma_f32_16x16x32_bf16 v[94:97], v[130:133], v[154:157], v[94:97]
	v_mfma_f32_16x16x32_bf16 v[90:93], v[138:141], v[154:157], v[90:93]
	v_mfma_f32_16x16x32_bf16 v[78:81], v[130:133], v[146:149], v[78:81]
	v_mfma_f32_16x16x32_bf16 v[74:77], v[138:141], v[146:149], v[74:77]
	v_mfma_f32_16x16x32_bf16 v[126:129], v[134:137], v[174:177], v[126:129]
	v_mfma_f32_16x16x32_bf16 v[122:125], v[142:145], v[174:177], v[122:125]
	v_mfma_f32_16x16x32_bf16 v[110:113], v[134:137], v[166:169], v[110:113]
	v_mfma_f32_16x16x32_bf16 v[106:109], v[142:145], v[166:169], v[106:109]
	v_mfma_f32_16x16x32_bf16 v[94:97], v[134:137], v[158:161], v[94:97]
	v_mfma_f32_16x16x32_bf16 v[90:93], v[142:145], v[158:161], v[90:93]
	v_mfma_f32_16x16x32_bf16 v[78:81], v[134:137], v[150:153], v[78:81]
	v_mfma_f32_16x16x32_bf16 v[74:77], v[142:145], v[150:153], v[74:77]
	s_nop 0
	s_barrier
	s_add_i32 s60, 0, 0x14000
	s_mov_b32 m0, s43
	v_add_u32_e32 v183, s60, v198
	v_lshl_add_u64 v[232:233], s[24:25], 0, v[178:179]
	ds_read_b128 v[216:219], v183
	ds_read_b128 v[220:223], v183 offset:1024
	ds_read_b128 v[224:227], v183 offset:2048
	ds_read_b128 v[228:231], v183 offset:3072
	global_load_lds_dwordx4 v[232:233], off
	v_lshl_add_u64 v[234:235], s[24:25], 0, v[180:181]
	s_mov_b32 m0, s44
	s_nop 0
	global_load_lds_dwordx4 v[234:235], off
	s_barrier
	s_waitcnt lgkmcnt(0)
	s_nop 0
	s_waitcnt lgkmcnt(0)
	v_mfma_f32_16x16x32_bf16 v[118:121], v[216:219], v[170:173], v[118:121]
	v_mfma_f32_16x16x32_bf16 v[114:117], v[224:227], v[170:173], v[114:117]
	v_mfma_f32_16x16x32_bf16 v[102:105], v[216:219], v[162:165], v[102:105]
	v_mfma_f32_16x16x32_bf16 v[98:101], v[224:227], v[162:165], v[98:101]
	v_mfma_f32_16x16x32_bf16 v[86:89], v[216:219], v[154:157], v[86:89]
	v_mfma_f32_16x16x32_bf16 v[82:85], v[224:227], v[154:157], v[82:85]
	v_mfma_f32_16x16x32_bf16 v[70:73], v[216:219], v[146:149], v[70:73]
	v_mfma_f32_16x16x32_bf16 v[66:69], v[224:227], v[146:149], v[66:69]
	v_mfma_f32_16x16x32_bf16 v[118:121], v[220:223], v[174:177], v[118:121]
	v_mfma_f32_16x16x32_bf16 v[114:117], v[228:231], v[174:177], v[114:117]
	v_mfma_f32_16x16x32_bf16 v[102:105], v[220:223], v[166:169], v[102:105]
	v_mfma_f32_16x16x32_bf16 v[98:101], v[228:231], v[166:169], v[98:101]
	v_mfma_f32_16x16x32_bf16 v[86:89], v[220:223], v[158:161], v[86:89]
	v_mfma_f32_16x16x32_bf16 v[82:85], v[228:231], v[158:161], v[82:85]
	v_mfma_f32_16x16x32_bf16 v[70:73], v[220:223], v[150:153], v[70:73]
	v_mfma_f32_16x16x32_bf16 v[66:69], v[228:231], v[150:153], v[66:69]
	s_nop 0
	s_mov_b32 m0, s42
	s_barrier
	ds_read_b128 v[146:149], v200 offset:16384
	ds_read_b128 v[150:153], v200 offset:17408
	ds_read_b128 v[154:157], v200 offset:18432
	ds_read_b128 v[158:161], v200 offset:19456
	ds_read_b128 v[162:165], v200 offset:20480
	ds_read_b128 v[166:169], v200 offset:21504
	ds_read_b128 v[170:173], v200 offset:22528
	ds_read_b128 v[174:177], v200 offset:23552
	global_load_lds_dwordx4 v0, s[34:35]
	s_mov_b32 m0, s45
	v_mov_b32_e32 v183, v1
	global_load_lds_dwordx4 v182, s[34:35]
	s_barrier
	s_waitcnt lgkmcnt(0)
	v_lshl_add_u64 v[236:237], s[34:35], 0, v[0:1]
	v_lshl_add_u64 v[238:239], s[34:35], 0, v[182:183]
	s_nop 0
	s_waitcnt lgkmcnt(0)
	v_mfma_f32_16x16x32_bf16 v[62:65], v[130:133], v[146:149], v[62:65]
	v_mfma_f32_16x16x32_bf16 v[58:61], v[138:141], v[146:149], v[58:61]
	v_mfma_f32_16x16x32_bf16 v[46:49], v[130:133], v[154:157], v[46:49]
	v_mfma_f32_16x16x32_bf16 v[42:45], v[138:141], v[154:157], v[42:45]
	v_mfma_f32_16x16x32_bf16 v[30:33], v[130:133], v[162:165], v[30:33]
	v_mfma_f32_16x16x32_bf16 v[26:29], v[138:141], v[162:165], v[26:29]
	v_mfma_f32_16x16x32_bf16 v[14:17], v[130:133], v[170:173], v[14:17]
	v_mfma_f32_16x16x32_bf16 v[10:13], v[138:141], v[170:173], v[10:13]
	v_mfma_f32_16x16x32_bf16 v[62:65], v[134:137], v[150:153], v[62:65]
	v_mfma_f32_16x16x32_bf16 v[58:61], v[142:145], v[150:153], v[58:61]
	v_mfma_f32_16x16x32_bf16 v[46:49], v[134:137], v[158:161], v[46:49]
	v_mfma_f32_16x16x32_bf16 v[42:45], v[142:145], v[158:161], v[42:45]
	v_mfma_f32_16x16x32_bf16 v[30:33], v[134:137], v[166:169], v[30:33]
	v_mfma_f32_16x16x32_bf16 v[26:29], v[142:145], v[166:169], v[26:29]
	v_mfma_f32_16x16x32_bf16 v[14:17], v[134:137], v[174:177], v[14:17]
	v_mfma_f32_16x16x32_bf16 v[10:13], v[142:145], v[174:177], v[10:13]
	s_nop 0
	s_barrier
	s_add_u32 s58, s24, 0x40000
	s_addc_u32 s59, s25, 0
	s_add_i32 s60, s60, s41
	v_lshl_add_u64 v[130:131], s[58:59], 0, v[178:179]
	s_mov_b32 m0, s60
	s_nop 0
	global_load_lds_dwordx4 v[130:131], off
	v_lshl_add_u64 v[130:131], s[58:59], 0, v[180:181]
	s_add_i32 m0, s60, 0x2000
	s_nop 0
	global_load_lds_dwordx4 v[130:131], off
	s_waitcnt vmcnt(6)
	s_barrier
; #define G8_STAGE(bufoff, gbase, voff) do { _Pragma("unroll") for (int _i = 0; _i < 2; ++_i) \
;         __builtin_amdgcn_global_load_lds((const unsigned*)((const char*)(gbase) + (voff)[_i]), (LAS unsigned*)(lds + (bufoff) + ldsw + _i * 8192), 16, 0, 0); } while (0)
; #define G8_LDA(dst, b, h) do { _Pragma("unroll") for (int m = 0; m < 4; ++m) _Pragma("unroll") for (int k = 0; k < 2; ++k) dst[m][k] = *(const LAS bf16x8*)(lds + G8_SA(b, h) + aoff + m * 2048 + k * 1024); } while (0)
; #define G8_LDB(dst, b, h) do { _Pragma("unroll") for (int n = 0; n < 2; ++n) _Pragma("unroll") for (int k = 0; k < 2; ++k) dst[n][k] = *(const LAS bf16x8*)(lds + G8_SB(b, h) + boff + n * 2048 + k * 1024); } while (0)
; #define G8_MMA(ai, bj, At, Bt) do { __builtin_amdgcn_s_setprio(1); _Pragma("unroll") for (int m = 0; m < 4; ++m) _Pragma("unroll") for (int n = 0; n < 2; ++n) _Pragma("unroll") for (int k = 0; k < 2; ++k) \
;         acc[ai][bj][m][n] = __builtin_amdgcn_mfma_f32_16x16x32_bf16(Bt[n][k], At[m][k], acc[ai][bj][m][n], 0, 0, 0); __builtin_amdgcn_s_setprio(0); } while (0)
; #define G8_WAIT_V(n) asm volatile("s_waitcnt vmcnt(" #n ")" ::: "memory")
; #define G8_WAIT_L(n) asm volatile("s_waitcnt lgkmcnt(" #n ")" ::: "memory")
; #define G8_BAR __builtin_amdgcn_s_barrier()
; #define G8_SCHED __builtin_amdgcn_sched_barrier(0)
; template <class Epi, class Sched>
; __device__ __forceinline__ void gemm_phase(LAS unsigned char* lds, const int K, const Sched& S, const Epi& E) {
;     ...
;             G8_WAIT_V(6); G8_BAR; G8_MMA(1, 1, At, B1); G8_BAR;
;             G8_LDB(B0, 1, 0); G8_SCHED; G8_LDA(At, 1, 0); G8_STAGE(G8_SA(0, 1), a2, oc[1]);
;             G8_WAIT_L(8); G8_BAR; G8_WAIT_L(0); G8_MMA(0, 0, At, B0); G8_BAR; G8_SCHED;
;             G8_LDB(B1, 1, 1); G8_STAGE(G8_SB(1, 0), b3, voffB);
	s_nop 0
	v_mfma_f32_16x16x32_bf16 v[54:57], v[216:219], v[146:149], v[54:57]
	v_mfma_f32_16x16x32_bf16 v[50:53], v[224:227], v[146:149], v[50:53]
	v_mfma_f32_16x16x32_bf16 v[38:41], v[216:219], v[154:157], v[38:41]
	v_mfma_f32_16x16x32_bf16 v[34:37], v[224:227], v[154:157], v[34:37]
	v_mfma_f32_16x16x32_bf16 v[22:25], v[216:219], v[162:165], v[22:25]
	v_mfma_f32_16x16x32_bf16 v[18:21], v[224:227], v[162:165], v[18:21]
	v_mfma_f32_16x16x32_bf16 v[6:9], v[216:219], v[170:173], v[6:9]
	v_mfma_f32_16x16x32_bf16 v[2:5], v[224:227], v[170:173], v[2:5]
	v_mfma_f32_16x16x32_bf16 v[54:57], v[220:223], v[150:153], v[54:57]
	v_mfma_f32_16x16x32_bf16 v[50:53], v[228:231], v[150:153], v[50:53]
	v_mfma_f32_16x16x32_bf16 v[38:41], v[220:223], v[158:161], v[38:41]
	v_mfma_f32_16x16x32_bf16 v[34:37], v[228:231], v[158:161], v[34:37]
	v_mfma_f32_16x16x32_bf16 v[22:25], v[220:223], v[166:169], v[22:25]
	v_mfma_f32_16x16x32_bf16 v[18:21], v[228:231], v[166:169], v[18:21]
	v_mfma_f32_16x16x32_bf16 v[6:9], v[220:223], v[174:177], v[6:9]
	v_mfma_f32_16x16x32_bf16 v[2:5], v[228:231], v[174:177], v[2:5]
	s_nop 0
	s_add_i32 s58, 0, 0x18000
	v_add_u32_e32 v142, s58, v198
	s_barrier
	ds_read_b128 v[130:133], v142
	ds_read_b128 v[134:137], v142 offset:1024
	ds_read_b128 v[138:141], v142 offset:2048
	ds_read_b128 v[142:145], v142 offset:3072
	s_mov_b32 m0, s46
	v_lshl_add_u64 v[190:191], s[34:35], 0, v[190:191]
	ds_read_b128 v[146:149], v200 offset:32768
	ds_read_b128 v[150:153], v200 offset:33792
	ds_read_b128 v[154:157], v200 offset:34816
	ds_read_b128 v[158:161], v200 offset:35840
	ds_read_b128 v[162:165], v200 offset:36864
	ds_read_b128 v[166:169], v200 offset:37888
	ds_read_b128 v[170:173], v200 offset:38912
	ds_read_b128 v[174:177], v200 offset:39936
	global_load_lds_dwordx4 v[190:191], off
	v_lshl_add_u64 v[190:191], s[34:35], 0, v[186:187]
	s_mov_b32 m0, s47
	s_nop 0
	global_load_lds_dwordx4 v[190:191], off
	s_waitcnt lgkmcnt(8)
	s_barrier
	s_waitcnt lgkmcnt(0)
	s_nop 0
	s_waitcnt lgkmcnt(0)
	v_mfma_f32_16x16x32_bf16 v[126:129], v[130:133], v[146:149], v[126:129]
	v_mfma_f32_16x16x32_bf16 v[122:125], v[138:141], v[146:149], v[122:125]
	v_mfma_f32_16x16x32_bf16 v[110:113], v[130:133], v[154:157], v[110:113]
	v_mfma_f32_16x16x32_bf16 v[106:109], v[138:141], v[154:157], v[106:109]
	v_mfma_f32_16x16x32_bf16 v[94:97], v[130:133], v[162:165], v[94:97]
	v_mfma_f32_16x16x32_bf16 v[90:93], v[138:141], v[162:165], v[90:93]
	v_mfma_f32_16x16x32_bf16 v[78:81], v[130:133], v[170:173], v[78:81]
	v_mfma_f32_16x16x32_bf16 v[74:77], v[138:141], v[170:173], v[74:77]
	v_mfma_f32_16x16x32_bf16 v[126:129], v[134:137], v[150:153], v[126:129]
	v_mfma_f32_16x16x32_bf16 v[122:125], v[142:145], v[150:153], v[122:125]
	v_mfma_f32_16x16x32_bf16 v[110:113], v[134:137], v[158:161], v[110:113]
	v_mfma_f32_16x16x32_bf16 v[106:109], v[142:145], v[158:161], v[106:109]
	v_mfma_f32_16x16x32_bf16 v[94:97], v[134:137], v[166:169], v[94:97]
	v_mfma_f32_16x16x32_bf16 v[90:93], v[142:145], v[166:169], v[90:93]
	v_mfma_f32_16x16x32_bf16 v[78:81], v[134:137], v[174:177], v[78:81]
	v_mfma_f32_16x16x32_bf16 v[74:77], v[142:145], v[174:177], v[74:77]
	s_nop 0
	s_barrier
	s_add_i32 s34, 0, 0x1c000
	s_add_i32 s35, s58, s41
	v_add_u32_e32 v183, s34, v198
	v_lshl_add_u64 v[190:191], v[232:233], 0, s[18:19]
	s_mov_b32 m0, s35
	ds_read_b128 v[216:219], v183
	ds_read_b128 v[220:223], v183 offset:1024
	ds_read_b128 v[224:227], v183 offset:2048
	ds_read_b128 v[228:231], v183 offset:3072
	global_load_lds_dwordx4 v[190:191], off
	v_lshl_add_u64 v[190:191], v[234:235], 0, s[18:19]
	s_add_i32 m0, s35, 0x2000
	s_nop 0
	global_load_lds_dwordx4 v[190:191], off
	s_barrier
; #define G8_STAGE(bufoff, gbase, voff) do { _Pragma("unroll") for (int _i = 0; _i < 2; ++_i) \
;         __builtin_amdgcn_global_load_lds((const unsigned*)((const char*)(gbase) + (voff)[_i]), (LAS unsigned*)(lds + (bufoff) + ldsw + _i * 8192), 16, 0, 0); } while (0)
; #define G8_LDA(dst, b, h) do { _Pragma("unroll") for (int m = 0; m < 4; ++m) _Pragma("unroll") for (int k = 0; k < 2; ++k) dst[m][k] = *(const LAS bf16x8*)(lds + G8_SA(b, h) + aoff + m * 2048 + k * 1024); } while (0)
; #define G8_MMA(ai, bj, At, Bt) do { __builtin_amdgcn_s_setprio(1); _Pragma("unroll") for (int m = 0; m < 4; ++m) _Pragma("unroll") for (int n = 0; n < 2; ++n) _Pragma("unroll") for (int k = 0; k < 2; ++k) \
;         acc[ai][bj][m][n] = __builtin_amdgcn_mfma_f32_16x16x32_bf16(Bt[n][k], At[m][k], acc[ai][bj][m][n], 0, 0, 0); __builtin_amdgcn_s_setprio(0); } while (0)
; #define G8_WAIT_V(n) asm volatile("s_waitcnt vmcnt(" #n ")" ::: "memory")
; #define G8_WAIT_L(n) asm volatile("s_waitcnt lgkmcnt(" #n ")" ::: "memory")
; #define G8_BAR __builtin_amdgcn_s_barrier()
; #define G8_SCHED __builtin_amdgcn_sched_barrier(0)
; template <class Epi, class Sched>
; __device__ __forceinline__ void gemm_phase(LAS unsigned char* lds, const int K, const Sched& S, const Epi& E) {
;     ...
;             G8_BAR; G8_WAIT_L(0); G8_MMA(0, 1, At, B1); G8_BAR;
;             G8_LDA(At, 1, 1); G8_STAGE(G8_SA(1, 0), a3, oc[0]);
;             G8_BAR; G8_WAIT_L(0); G8_MMA(1, 0, At, B0); G8_BAR; G8_SCHED;
;             G8_STAGE(G8_SB(1, 1), b3 + hstep, voffB);
;             G8_WAIT_V(6); G8_BAR; G8_MMA(1, 1, At, B1); G8_BAR;
;         }
	s_waitcnt lgkmcnt(0)
	s_nop 0
	s_waitcnt lgkmcnt(0)
	v_mfma_f32_16x16x32_bf16 v[118:121], v[216:219], v[146:149], v[118:121]
	v_mfma_f32_16x16x32_bf16 v[114:117], v[224:227], v[146:149], v[114:117]
	v_mfma_f32_16x16x32_bf16 v[102:105], v[216:219], v[154:157], v[102:105]
	v_mfma_f32_16x16x32_bf16 v[98:101], v[224:227], v[154:157], v[98:101]
	v_mfma_f32_16x16x32_bf16 v[86:89], v[216:219], v[162:165], v[86:89]
	v_mfma_f32_16x16x32_bf16 v[82:85], v[224:227], v[162:165], v[82:85]
	v_mfma_f32_16x16x32_bf16 v[70:73], v[216:219], v[170:173], v[70:73]
	v_mfma_f32_16x16x32_bf16 v[66:69], v[224:227], v[170:173], v[66:69]
	v_mfma_f32_16x16x32_bf16 v[118:121], v[220:223], v[150:153], v[118:121]
	v_mfma_f32_16x16x32_bf16 v[114:117], v[228:231], v[150:153], v[114:117]
	v_mfma_f32_16x16x32_bf16 v[102:105], v[220:223], v[158:161], v[102:105]
	v_mfma_f32_16x16x32_bf16 v[98:101], v[228:231], v[158:161], v[98:101]
	v_mfma_f32_16x16x32_bf16 v[86:89], v[220:223], v[166:169], v[86:89]
	v_mfma_f32_16x16x32_bf16 v[82:85], v[228:231], v[166:169], v[82:85]
	v_mfma_f32_16x16x32_bf16 v[70:73], v[220:223], v[174:177], v[70:73]
	v_mfma_f32_16x16x32_bf16 v[66:69], v[228:231], v[174:177], v[66:69]
	s_nop 0
	s_mov_b32 m0, s49
	v_lshl_add_u64 v[190:191], v[236:237], 0, s[18:19]
	s_barrier
	ds_read_b128 v[146:149], v200 offset:49152
	ds_read_b128 v[150:153], v200 offset:50176
	ds_read_b128 v[154:157], v200 offset:51200
	ds_read_b128 v[158:161], v200 offset:52224
	ds_read_b128 v[162:165], v200 offset:53248
	ds_read_b128 v[166:169], v200 offset:54272
	ds_read_b128 v[170:173], v200 offset:55296
	ds_read_b128 v[174:177], v200 offset:56320
	global_load_lds_dwordx4 v[190:191], off
	v_lshl_add_u64 v[190:191], v[238:239], 0, s[18:19]
	s_mov_b32 m0, s50
	s_nop 0
	global_load_lds_dwordx4 v[190:191], off
	s_barrier
	s_waitcnt lgkmcnt(0)
	s_nop 0
	s_waitcnt lgkmcnt(0)
	v_mfma_f32_16x16x32_bf16 v[62:65], v[130:133], v[146:149], v[62:65]
	v_mfma_f32_16x16x32_bf16 v[58:61], v[138:141], v[146:149], v[58:61]
	v_mfma_f32_16x16x32_bf16 v[46:49], v[130:133], v[154:157], v[46:49]
	v_mfma_f32_16x16x32_bf16 v[42:45], v[138:141], v[154:157], v[42:45]
	v_mfma_f32_16x16x32_bf16 v[30:33], v[130:133], v[162:165], v[30:33]
	v_mfma_f32_16x16x32_bf16 v[26:29], v[138:141], v[162:165], v[26:29]
	v_mfma_f32_16x16x32_bf16 v[14:17], v[130:133], v[170:173], v[14:17]
	v_mfma_f32_16x16x32_bf16 v[10:13], v[138:141], v[170:173], v[10:13]
	v_mfma_f32_16x16x32_bf16 v[62:65], v[134:137], v[150:153], v[62:65]
	v_mfma_f32_16x16x32_bf16 v[58:61], v[142:145], v[150:153], v[58:61]
	v_mfma_f32_16x16x32_bf16 v[46:49], v[134:137], v[158:161], v[46:49]
	v_mfma_f32_16x16x32_bf16 v[42:45], v[142:145], v[158:161], v[42:45]
	v_mfma_f32_16x16x32_bf16 v[30:33], v[134:137], v[166:169], v[30:33]
	v_mfma_f32_16x16x32_bf16 v[26:29], v[142:145], v[166:169], v[26:29]
	v_mfma_f32_16x16x32_bf16 v[14:17], v[134:137], v[174:177], v[14:17]
	v_mfma_f32_16x16x32_bf16 v[10:13], v[142:145], v[174:177], v[10:13]
	s_nop 0
	s_barrier
	s_add_u32 s24, s24, 0x40080
	s_addc_u32 s25, s25, 0
	s_add_i32 s34, s34, s41
	v_lshl_add_u64 v[130:131], s[24:25], 0, v[178:179]
	s_mov_b32 m0, s34
	s_nop 0
	global_load_lds_dwordx4 v[130:131], off
	v_lshl_add_u64 v[130:131], s[24:25], 0, v[180:181]
	s_add_i32 m0, s34, 0x2000
	s_nop 0
	global_load_lds_dwordx4 v[130:131], off
	s_waitcnt vmcnt(6)
	s_barrier
	s_nop 0
	v_mfma_f32_16x16x32_bf16 v[54:57], v[216:219], v[146:149], v[54:57]
	v_mfma_f32_16x16x32_bf16 v[50:53], v[224:227], v[146:149], v[50:53]
	v_mfma_f32_16x16x32_bf16 v[38:41], v[216:219], v[154:157], v[38:41]
	v_mfma_f32_16x16x32_bf16 v[34:37], v[224:227], v[154:157], v[34:37]
	v_mfma_f32_16x16x32_bf16 v[22:25], v[216:219], v[162:165], v[22:25]
	v_mfma_f32_16x16x32_bf16 v[18:21], v[224:227], v[162:165], v[18:21]
	v_mfma_f32_16x16x32_bf16 v[6:9], v[216:219], v[170:173], v[6:9]
	v_mfma_f32_16x16x32_bf16 v[2:5], v[224:227], v[170:173], v[2:5]
	v_mfma_f32_16x16x32_bf16 v[54:57], v[220:223], v[150:153], v[54:57]
	v_mfma_f32_16x16x32_bf16 v[50:53], v[228:231], v[150:153], v[50:53]
	v_mfma_f32_16x16x32_bf16 v[38:41], v[220:223], v[158:161], v[38:41]
	v_mfma_f32_16x16x32_bf16 v[34:37], v[228:231], v[158:161], v[34:37]
	v_mfma_f32_16x16x32_bf16 v[22:25], v[220:223], v[166:169], v[22:25]
	v_mfma_f32_16x16x32_bf16 v[18:21], v[228:231], v[166:169], v[18:21]
	v_mfma_f32_16x16x32_bf16 v[6:9], v[220:223], v[174:177], v[6:9]
	v_mfma_f32_16x16x32_bf16 v[2:5], v[228:231], v[174:177], v[2:5]
	s_nop 0
	s_add_i32 s57, s57, 2
	s_add_u32 s22, s22, 0x100
	s_addc_u32 s23, s23, 0
	s_add_u32 s55, s55, 0x100
	s_addc_u32 s56, s56, 0
	s_cmp_gt_u32 s57, 13
	s_barrier
	s_cbranch_scc1 .LBB0_2529

; #define G8_WAIT_V(n) asm volatile("s_waitcnt vmcnt(" #n ")" ::: "memory")
; #define G8_BAR __builtin_amdgcn_s_barrier()
; template <class Epi, class Sched>
; __device__ __forceinline__ void gemm_phase(LAS unsigned char* lds, const int K, const Sched& S, const Epi& E) {
;     ...
;     G8_WAIT_V(0);
;     if (wr == 0) G8_BAR;
;     G8_BAR;
.LBB0_2551:
	s_barrier
	s_setprio 0
	s_nop 0
	s_nop 0
	s_nop 0
	s_nop 0
	s_nop 0
	s_nop 0
	s_nop 0
	s_nop 0
	s_nop 0
	s_nop 0
	s_nop 0
	s_nop 0
	s_nop 0
	s_nop 0
	s_nop 0
	s_add_i32 s14, s46, 7
	s_cmp_ge_i32 s14, s31
	s_cbranch_scc1 .LBB0_2601

; #define G8_STAGE(bufoff, gbase, voff) do { _Pragma("unroll") for (int _i = 0; _i < 2; ++_i) \
;         __builtin_amdgcn_global_load_lds((const unsigned*)((const char*)(gbase) + (voff)[_i]), (LAS unsigned*)(lds + (bufoff) + ldsw + _i * 8192), 16, 0, 0); } while (0)
; #define G8_WAIT_V(n) asm volatile("s_waitcnt vmcnt(" #n ")" ::: "memory")
; #define G8_BAR __builtin_amdgcn_s_barrier()
; template <class Epi, class Sched>
; __device__ __forceinline__ void gemm_phase(LAS unsigned char* lds, const int K, const Sched& S, const Epi& E) {
;     int tid_ = S.tid0; asm volatile("" : "+v"(tid_));
;     const int tid = tid_, wid = __builtin_amdgcn_readfirstlane(tid >> 6), lane = tid & 63, wr = wid >> 2, wc = wid & 3, fr = lane & 15, fq = lane >> 4;
;     const int nt = K / BK;
;     unsigned voffB[2];
; #pragma unroll
;     for (int i = 0; i < 2; ++i) { int R, C; stage_rc(tid * 16 + i * 8192, R, C); const int Rb = Epi::PERM ? ((R & ~31) + perm32(R & 31)) : R;
;         voffB[i] = (unsigned)(Rb * K + C) * 2u; }
;     const size_t kstep = (size_t)(BK * 2);
;     const size_t hstep = (size_t)HALF * K * 2;
;     const unsigned ldsw = (unsigned)wid * 1024u;
;     const int aoff = lds_byte(wr * 64 + fr, fq * 8), boff = lds_byte(wc * 32 + fr, fq * 8);
;     ...
;     Unit cur, nxt; int ui = 0;
;     if (!S.next(0, cur)) return;
;     f32x4 acc[2][2][4][2];
;     E.init(acc, cur, wc, fq);
;     bf16x8 At[4][2], B0[2][2], B1[2][2];
;     unsigned oc[2][2];
;     S.aoff(cur, tid, oc);
;     const char* cA = cur.A; const char* cB = cur.B;
;     G8_STAGE(G8_SB(0, 0), cB, voffB); G8_STAGE(G8_SA(0, 0), cA, oc[0]); G8_STAGE(G8_SB(0, 1), cB + hstep, voffB); G8_STAGE(G8_SA(0, 1), cA, oc[1]);
;     if (wr == 1) G8_BAR;
;     G8_WAIT_V(4); G8_BAR;
;     G8_STAGE(G8_SB(1, 0), cB + kstep, voffB); G8_STAGE(G8_SA(1, 0), cA + kstep, oc[0]); G8_STAGE(G8_SB(1, 1), cB + hstep + kstep, voffB);
;     G8_WAIT_V(6); G8_BAR;
;     __device__ __forceinline__ void aoff(const g8::Unit& u, int tid, unsigned (&o)[2][2]) const {
; #pragma unroll
;         for (int i = 0; i < 2; ++i) { int R, C; g8::stage_rc(tid * 16 + i * 8192, R, C);
; #pragma unroll
;             for (int h = 0; h < 2; ++h) { int s = tab[u.aux * 256 + h * 128 + R]; s = s < 0 ? 0 : s; const int row = mode ? s : (s < TK ? (s >> 3) : s - TK);
;                 o[h][i] = (unsigned)(row * K + C) * 2u; } }
;     }
.LBB0_2606:
	s_load_dword s48, s[86:87], 0x0
	s_andn2_b64 vcc, exec, s[2:3]
	s_cbranch_vccnz .LBB0_2669
	v_bfe_i32 v3, v10, 27, 1
	v_lshlrev_b32_e32 v0, 4, v10
	v_lshrrev_b32_e32 v3, 22, v3
	v_add_u32_e32 v3, v0, v3
	v_and_b32_e32 v3, 0xfffffc00, v3
	v_sub_u32_e32 v3, v0, v3
	v_lshrrev_b32_e32 v4, 4, v3
	v_bitop3_b32 v3, v4, v3, 32 bitop3:0x6c
	v_ashrrev_i32_e32 v5, 31, v3
	v_ashrrev_i32_e32 v2, 31, v10
	v_lshrrev_b32_e32 v5, 26, v5
	v_lshrrev_b32_e32 v2, 26, v2
	v_add_u32_e32 v5, v3, v5
	v_add_u32_e32 v2, v10, v2
	v_ashrrev_i32_e32 v6, 6, v5
	v_and_b32_e32 v5, 0xc0, v5
	v_ashrrev_i32_e32 v2, 6, v2
	v_sub_u32_e32 v3, v3, v5
	v_lshlrev_b32_e32 v4, 3, v2
	v_lshlrev_b32_e32 v2, 5, v2
	v_ashrrev_i16_sdwa v3, v203, sext(v3) dst_sel:DWORD dst_unused:UNUSED_PAD src0_sel:DWORD src1_sel:BYTE_0
	v_and_b32_e32 v2, 32, v2
	v_bfe_i32 v3, v3, 0, 16
	v_add_u32_e32 v0, 0x2000, v0
	v_add_lshl_u32 v194, v2, v3, 1
	v_ashrrev_i32_e32 v2, 31, v0
	v_lshrrev_b32_e32 v2, 22, v2
	v_add_u32_e32 v2, v0, v2
	v_and_b32_e32 v4, -16, v4
	v_ashrrev_i32_e32 v2, 10, v2
	v_add_u32_e32 v7, v6, v4
	v_mul_i32_i24_e32 v3, 0x400, v2
	v_lshlrev_b32_e32 v5, 1, v7
	v_lshrrev_b32_e32 v8, 2, v7
	v_and_b32_e32 v9, 3, v6
	s_mov_b32 s2, 0x7fffe0
	v_sub_u32_e32 v0, v0, v3
	v_and_b32_e32 v5, 24, v5
	v_and_b32_e32 v8, 4, v8
	v_and_or_b32 v7, v7, s2, v9
	v_lshrrev_b32_e32 v3, 4, v0
	v_or3_b32 v5, v7, v8, v5
	v_bitop3_b32 v0, v3, v0, 32 bitop3:0x6c
	v_lshl_add_u32 v178, v5, 9, v194
	v_ashrrev_i32_e32 v5, 31, v0
	v_lshrrev_b32_e32 v5, 26, v5
	v_add_u32_e32 v5, v0, v5
	v_ashrrev_i32_e32 v7, 6, v5
	v_and_b32_e32 v5, 0xc0, v5
	v_sub_u32_e32 v0, v0, v5
	v_lshlrev_b32_e32 v3, 3, v2
	v_lshlrev_b32_e32 v2, 5, v2
	v_ashrrev_i16_sdwa v0, v203, sext(v0) dst_sel:DWORD dst_unused:UNUSED_PAD src0_sel:DWORD src1_sel:BYTE_0
	v_and_b32_e32 v3, -16, v3
	v_and_b32_e32 v2, 32, v2
	v_bfe_i32 v0, v0, 0, 16
	v_lshlrev_b32_e32 v196, 2, v6
	s_add_i32 s10, 0, 0x20000
	v_lshlrev_b32_e32 v197, 2, v4
	v_add_u32_e32 v8, v7, v3
	v_and_b32_e32 v11, 3, v7
	v_add_lshl_u32 v195, v2, v0, 1
	v_add3_u32 v0, s10, v196, v197
	v_lshlrev_b32_e32 v5, 1, v8
	v_lshrrev_b32_e32 v9, 2, v8
	v_and_or_b32 v8, v8, s2, v11
	s_ashr_i32 s5, s49, 6
	ds_read_b32 v0, v0
	v_readlane_b32 s2, v253, 52
	v_lshlrev_b32_e32 v198, 2, v7
	v_lshlrev_b32_e32 v199, 2, v3
	s_lshl_b32 s50, s5, 10
	v_add3_u32 v2, s2, v196, v197
	v_add3_u32 v3, s10, v198, v199
	v_add3_u32 v4, s2, v198, v199
	ds_read_b32 v2, v2
	ds_read_b32 v3, v3
	ds_read_b32 v4, v4
	s_add_i32 s51, s50, 0
	v_and_b32_e32 v5, 24, v5
	v_and_b32_e32 v9, 4, v9
	s_add_i32 s52, s51, 0x10000
	v_or3_b32 v5, v8, v9, v5
	s_mov_b32 m0, s52
	s_add_i32 s53, s51, 0x12000
	v_lshl_add_u32 v180, v5, 9, v195
	s_waitcnt lgkmcnt(0)
	v_max_i32_e32 v0, 0, v0
	global_load_lds_dwordx4 v178, s[22:23]
	s_mov_b32 m0, s53
	s_ashr_i32 s4, s49, 8
	v_lshl_add_u32 v182, v0, 9, v194
	v_max_i32_e32 v0, 0, v2
	v_max_i32_e32 v2, 0, v3
	global_load_lds_dwordx4 v180, s[22:23]
	s_mov_b32 m0, s51
	s_add_i32 s54, s51, 0x2000
	v_lshl_add_u32 v184, v2, 9, v195
	global_load_lds_dwordx4 v182, s[0:1]
	s_mov_b32 m0, s54
	s_add_u32 s2, s22, 0x10000
	global_load_lds_dwordx4 v184, s[0:1]
	s_addc_u32 s3, s23, 0
	s_add_i32 m0, s51, 0x14000
	s_add_i32 s55, s51, 0x4000
	global_load_lds_dwordx4 v178, s[2:3]
	s_add_i32 m0, s51, 0x16000
	v_lshl_add_u32 v0, v0, 9, v194
	v_max_i32_e32 v2, 0, v4
	global_load_lds_dwordx4 v180, s[2:3]
	s_mov_b32 m0, s55
	s_add_i32 s56, s51, 0x6000
	v_lshl_add_u32 v186, v2, 9, v195
	global_load_lds_dwordx4 v0, s[0:1]
	s_mov_b32 m0, s56
	v_mov_b32_e32 v179, v1
	global_load_lds_dwordx4 v186, s[0:1]
	v_mov_b32_e32 v181, v1
	v_mov_b32_e32 v183, v1
	v_mov_b32_e32 v185, v1
	v_lshl_add_u64 v[8:9], s[22:23], 0, v[178:179]
	v_lshl_add_u64 v[6:7], s[22:23], 0, v[180:181]
	v_lshl_add_u64 v[4:5], s[0:1], 0, v[182:183]
	s_cmp_lg_u32 s4, 1
	v_lshl_add_u64 v[2:3], s[0:1], 0, v[184:185]
	s_cbranch_scc1 .LBB0_2609
	s_barrier
	s_setprio 1
	s_nop 0
	s_nop 0
	s_nop 0
	s_nop 0
	s_nop 0
	s_nop 0
	s_nop 0
	s_nop 0
	s_nop 0
	s_nop 0
	s_nop 0
	s_nop 0
	s_nop 0
	s_nop 0
	s_nop 0

; #define G8_STAGE(bufoff, gbase, voff) do { _Pragma("unroll") for (int _i = 0; _i < 2; ++_i) \
;         __builtin_amdgcn_global_load_lds((const unsigned*)((const char*)(gbase) + (voff)[_i]), (LAS unsigned*)(lds + (bufoff) + ldsw + _i * 8192), 16, 0, 0); } while (0)
; #define G8_LDA(dst, b, h) do { _Pragma("unroll") for (int m = 0; m < 4; ++m) _Pragma("unroll") for (int k = 0; k < 2; ++k) dst[m][k] = *(const LAS bf16x8*)(lds + G8_SA(b, h) + aoff + m * 2048 + k * 1024); } while (0)
; #define G8_LDB(dst, b, h) do { _Pragma("unroll") for (int n = 0; n < 2; ++n) _Pragma("unroll") for (int k = 0; k < 2; ++k) dst[n][k] = *(const LAS bf16x8*)(lds + G8_SB(b, h) + boff + n * 2048 + k * 1024); } while (0)
; #define G8_MMA(ai, bj, At, Bt) do { __builtin_amdgcn_s_setprio(1); _Pragma("unroll") for (int m = 0; m < 4; ++m) _Pragma("unroll") for (int n = 0; n < 2; ++n) _Pragma("unroll") for (int k = 0; k < 2; ++k) \
;         acc[ai][bj][m][n] = __builtin_amdgcn_mfma_f32_16x16x32_bf16(Bt[n][k], At[m][k], acc[ai][bj][m][n], 0, 0, 0); __builtin_amdgcn_s_setprio(0); } while (0)
; #define G8_WAIT_V(n) asm volatile("s_waitcnt vmcnt(" #n ")" ::: "memory")
; #define G8_WAIT_L(n) asm volatile("s_waitcnt lgkmcnt(" #n ")" ::: "memory")
; #define G8_BAR __builtin_amdgcn_s_barrier()
; #define G8_SCHED __builtin_amdgcn_sched_barrier(0)
; template <class Epi, class Sched>
; __device__ __forceinline__ void gemm_phase(LAS unsigned char* lds, const int K, const Sched& S, const Epi& E) {
;     ...
;             G8_WAIT_L(8); G8_BAR; G8_WAIT_L(0); G8_MMA(0, 0, At, B0); G8_BAR; G8_SCHED;
;             G8_LDB(B1, 0, 1); G8_STAGE(G8_SB(0, 0), b2, voffB);
;             G8_BAR; G8_WAIT_L(0); G8_MMA(0, 1, At, B1); G8_BAR;
;             G8_LDA(At, 0, 1); G8_STAGE(G8_SA(0, 0), a2, oc[0]);
;             G8_BAR; G8_WAIT_L(0); G8_MMA(1, 0, At, B0); G8_BAR; G8_SCHED;
;             G8_STAGE(G8_SB(0, 1), b2 + hstep, voffB);
;             G8_WAIT_V(6); G8_BAR; G8_MMA(1, 1, At, B1); G8_BAR;
.LBB0_2616:
	s_xor_b64 s[40:41], s[42:43], -1
	s_add_u32 s44, s44, 0x100
	s_addc_u32 s45, s45, 0
	s_and_b64 s[42:43], s[36:37], exec
	s_cselect_b32 s43, s1, s45
	s_cselect_b32 s42, s0, s44
	s_add_u32 s38, s22, s38
	s_addc_u32 s39, s23, s39
	s_add_u32 s38, s38, 0x100
	s_addc_u32 s39, s39, 0
	s_waitcnt lgkmcnt(8)
	s_barrier
	s_waitcnt lgkmcnt(0)
	s_and_b64 s[36:37], s[36:37], exec
	s_cselect_b32 s37, s35, s39
	s_cselect_b32 s36, s34, s38
	s_nop 0
	s_waitcnt lgkmcnt(0)
	v_mfma_f32_16x16x32_bf16 v[126:129], v[130:133], v[170:173], v[126:129]
	v_mfma_f32_16x16x32_bf16 v[122:125], v[138:141], v[170:173], v[122:125]
	v_mfma_f32_16x16x32_bf16 v[110:113], v[130:133], v[162:165], v[110:113]
	v_mfma_f32_16x16x32_bf16 v[106:109], v[138:141], v[162:165], v[106:109]
	v_mfma_f32_16x16x32_bf16 v[94:97], v[130:133], v[154:157], v[94:97]
	v_mfma_f32_16x16x32_bf16 v[90:93], v[138:141], v[154:157], v[90:93]
	v_mfma_f32_16x16x32_bf16 v[78:81], v[130:133], v[146:149], v[78:81]
	v_mfma_f32_16x16x32_bf16 v[74:77], v[138:141], v[146:149], v[74:77]
	v_mfma_f32_16x16x32_bf16 v[126:129], v[134:137], v[174:177], v[126:129]
	v_mfma_f32_16x16x32_bf16 v[122:125], v[142:145], v[174:177], v[122:125]
	v_mfma_f32_16x16x32_bf16 v[110:113], v[134:137], v[166:169], v[110:113]
	v_mfma_f32_16x16x32_bf16 v[106:109], v[142:145], v[166:169], v[106:109]
	v_mfma_f32_16x16x32_bf16 v[94:97], v[134:137], v[158:161], v[94:97]
	v_mfma_f32_16x16x32_bf16 v[90:93], v[142:145], v[158:161], v[90:93]
	v_mfma_f32_16x16x32_bf16 v[78:81], v[134:137], v[150:153], v[78:81]
	v_mfma_f32_16x16x32_bf16 v[74:77], v[142:145], v[150:153], v[74:77]
	s_nop 0
	s_barrier
	s_add_i32 s44, 0, 0x14000
	s_mov_b32 m0, s52
	v_add_u32_e32 v183, s44, v200
	v_lshl_add_u64 v[236:237], s[36:37], 0, v[178:179]
	ds_read_b128 v[220:223], v183
	ds_read_b128 v[224:227], v183 offset:1024
	ds_read_b128 v[228:231], v183 offset:2048
	ds_read_b128 v[232:235], v183 offset:3072
	global_load_lds_dwordx4 v[236:237], off
	v_lshl_add_u64 v[238:239], s[36:37], 0, v[180:181]
	s_mov_b32 m0, s53
	s_nop 0
	global_load_lds_dwordx4 v[238:239], off
	s_barrier
	s_waitcnt lgkmcnt(0)
	s_nop 0
	s_waitcnt lgkmcnt(0)
	v_mfma_f32_16x16x32_bf16 v[118:121], v[220:223], v[170:173], v[118:121]
	v_mfma_f32_16x16x32_bf16 v[114:117], v[228:231], v[170:173], v[114:117]
	v_mfma_f32_16x16x32_bf16 v[102:105], v[220:223], v[162:165], v[102:105]
	v_mfma_f32_16x16x32_bf16 v[98:101], v[228:231], v[162:165], v[98:101]
	v_mfma_f32_16x16x32_bf16 v[86:89], v[220:223], v[154:157], v[86:89]
	v_mfma_f32_16x16x32_bf16 v[82:85], v[228:231], v[154:157], v[82:85]
	v_mfma_f32_16x16x32_bf16 v[70:73], v[220:223], v[146:149], v[70:73]
	v_mfma_f32_16x16x32_bf16 v[66:69], v[228:231], v[146:149], v[66:69]
	v_mfma_f32_16x16x32_bf16 v[118:121], v[224:227], v[174:177], v[118:121]
	v_mfma_f32_16x16x32_bf16 v[114:117], v[232:235], v[174:177], v[114:117]
	v_mfma_f32_16x16x32_bf16 v[102:105], v[224:227], v[166:169], v[102:105]
	v_mfma_f32_16x16x32_bf16 v[98:101], v[232:235], v[166:169], v[98:101]
	v_mfma_f32_16x16x32_bf16 v[86:89], v[224:227], v[158:161], v[86:89]
	v_mfma_f32_16x16x32_bf16 v[82:85], v[232:235], v[158:161], v[82:85]
	v_mfma_f32_16x16x32_bf16 v[70:73], v[224:227], v[150:153], v[70:73]
	v_mfma_f32_16x16x32_bf16 v[66:69], v[232:235], v[150:153], v[66:69]
	s_nop 0
	s_mov_b32 m0, s51
	s_barrier
	ds_read_b128 v[146:149], v216 offset:16384
	ds_read_b128 v[150:153], v216 offset:17408
	ds_read_b128 v[154:157], v216 offset:18432
	ds_read_b128 v[158:161], v216 offset:19456
	ds_read_b128 v[162:165], v216 offset:20480
	ds_read_b128 v[166:169], v216 offset:21504
	ds_read_b128 v[170:173], v216 offset:22528
	ds_read_b128 v[174:177], v216 offset:23552
	global_load_lds_dwordx4 v182, s[42:43]
	s_mov_b32 m0, s54
	v_mov_b32_e32 v183, v1
	global_load_lds_dwordx4 v184, s[42:43]
	s_barrier
	s_waitcnt lgkmcnt(0)
	v_mov_b32_e32 v185, v1
	v_lshl_add_u64 v[240:241], s[42:43], 0, v[182:183]
	v_lshl_add_u64 v[242:243], s[42:43], 0, v[184:185]
	s_nop 0
	s_waitcnt lgkmcnt(0)
	v_mfma_f32_16x16x32_bf16 v[62:65], v[130:133], v[146:149], v[62:65]
	v_mfma_f32_16x16x32_bf16 v[58:61], v[138:141], v[146:149], v[58:61]
	v_mfma_f32_16x16x32_bf16 v[46:49], v[130:133], v[154:157], v[46:49]
	v_mfma_f32_16x16x32_bf16 v[42:45], v[138:141], v[154:157], v[42:45]
	v_mfma_f32_16x16x32_bf16 v[30:33], v[130:133], v[162:165], v[30:33]
	v_mfma_f32_16x16x32_bf16 v[26:29], v[138:141], v[162:165], v[26:29]
	v_mfma_f32_16x16x32_bf16 v[14:17], v[130:133], v[170:173], v[14:17]
	v_mfma_f32_16x16x32_bf16 v[10:13], v[138:141], v[170:173], v[10:13]
	v_mfma_f32_16x16x32_bf16 v[62:65], v[134:137], v[150:153], v[62:65]
	v_mfma_f32_16x16x32_bf16 v[58:61], v[142:145], v[150:153], v[58:61]
	v_mfma_f32_16x16x32_bf16 v[46:49], v[134:137], v[158:161], v[46:49]
	v_mfma_f32_16x16x32_bf16 v[42:45], v[142:145], v[158:161], v[42:45]
	v_mfma_f32_16x16x32_bf16 v[30:33], v[134:137], v[166:169], v[30:33]
	v_mfma_f32_16x16x32_bf16 v[26:29], v[142:145], v[166:169], v[26:29]
	v_mfma_f32_16x16x32_bf16 v[14:17], v[134:137], v[174:177], v[14:17]
	v_mfma_f32_16x16x32_bf16 v[10:13], v[142:145], v[174:177], v[10:13]
	s_nop 0
	s_barrier
	s_add_u32 s38, s36, 0x10000
	s_addc_u32 s39, s37, 0
	s_add_i32 s44, s44, s50
	v_lshl_add_u64 v[130:131], s[38:39], 0, v[178:179]
	s_mov_b32 m0, s44
	s_nop 0
	global_load_lds_dwordx4 v[130:131], off
	v_lshl_add_u64 v[130:131], s[38:39], 0, v[180:181]
	s_add_i32 m0, s44, 0x2000
	s_nop 0
	global_load_lds_dwordx4 v[130:131], off
	s_waitcnt vmcnt(6)
	s_barrier
; #define G8_STAGE(bufoff, gbase, voff) do { _Pragma("unroll") for (int _i = 0; _i < 2; ++_i) \
;         __builtin_amdgcn_global_load_lds((const unsigned*)((const char*)(gbase) + (voff)[_i]), (LAS unsigned*)(lds + (bufoff) + ldsw + _i * 8192), 16, 0, 0); } while (0)
; #define G8_LDA(dst, b, h) do { _Pragma("unroll") for (int m = 0; m < 4; ++m) _Pragma("unroll") for (int k = 0; k < 2; ++k) dst[m][k] = *(const LAS bf16x8*)(lds + G8_SA(b, h) + aoff + m * 2048 + k * 1024); } while (0)
; #define G8_LDB(dst, b, h) do { _Pragma("unroll") for (int n = 0; n < 2; ++n) _Pragma("unroll") for (int k = 0; k < 2; ++k) dst[n][k] = *(const LAS bf16x8*)(lds + G8_SB(b, h) + boff + n * 2048 + k * 1024); } while (0)
; #define G8_MMA(ai, bj, At, Bt) do { __builtin_amdgcn_s_setprio(1); _Pragma("unroll") for (int m = 0; m < 4; ++m) _Pragma("unroll") for (int n = 0; n < 2; ++n) _Pragma("unroll") for (int k = 0; k < 2; ++k) \
;         acc[ai][bj][m][n] = __builtin_amdgcn_mfma_f32_16x16x32_bf16(Bt[n][k], At[m][k], acc[ai][bj][m][n], 0, 0, 0); __builtin_amdgcn_s_setprio(0); } while (0)
; #define G8_WAIT_V(n) asm volatile("s_waitcnt vmcnt(" #n ")" ::: "memory")
; #define G8_WAIT_L(n) asm volatile("s_waitcnt lgkmcnt(" #n ")" ::: "memory")
; #define G8_BAR __builtin_amdgcn_s_barrier()
; #define G8_SCHED __builtin_amdgcn_sched_barrier(0)
; template <class Epi, class Sched>
; __device__ __forceinline__ void gemm_phase(LAS unsigned char* lds, const int K, const Sched& S, const Epi& E) {
;     ...
;             G8_WAIT_V(6); G8_BAR; G8_MMA(1, 1, At, B1); G8_BAR;
;             G8_LDB(B0, 1, 0); G8_SCHED; G8_LDA(At, 1, 0); G8_STAGE(G8_SA(0, 1), a2, oc[1]);
;             G8_WAIT_L(8); G8_BAR; G8_WAIT_L(0); G8_MMA(0, 0, At, B0); G8_BAR; G8_SCHED;
;             G8_LDB(B1, 1, 1); G8_STAGE(G8_SB(1, 0), b3, voffB);
	s_nop 0
	v_mfma_f32_16x16x32_bf16 v[54:57], v[220:223], v[146:149], v[54:57]
	v_mfma_f32_16x16x32_bf16 v[50:53], v[228:231], v[146:149], v[50:53]
	v_mfma_f32_16x16x32_bf16 v[38:41], v[220:223], v[154:157], v[38:41]
	v_mfma_f32_16x16x32_bf16 v[34:37], v[228:231], v[154:157], v[34:37]
	v_mfma_f32_16x16x32_bf16 v[22:25], v[220:223], v[162:165], v[22:25]
	v_mfma_f32_16x16x32_bf16 v[18:21], v[228:231], v[162:165], v[18:21]
	v_mfma_f32_16x16x32_bf16 v[6:9], v[220:223], v[170:173], v[6:9]
	v_mfma_f32_16x16x32_bf16 v[2:5], v[228:231], v[170:173], v[2:5]
	v_mfma_f32_16x16x32_bf16 v[54:57], v[224:227], v[150:153], v[54:57]
	v_mfma_f32_16x16x32_bf16 v[50:53], v[232:235], v[150:153], v[50:53]
	v_mfma_f32_16x16x32_bf16 v[38:41], v[224:227], v[158:161], v[38:41]
	v_mfma_f32_16x16x32_bf16 v[34:37], v[232:235], v[158:161], v[34:37]
	v_mfma_f32_16x16x32_bf16 v[22:25], v[224:227], v[166:169], v[22:25]
	v_mfma_f32_16x16x32_bf16 v[18:21], v[232:235], v[166:169], v[18:21]
	v_mfma_f32_16x16x32_bf16 v[6:9], v[224:227], v[174:177], v[6:9]
	v_mfma_f32_16x16x32_bf16 v[2:5], v[232:235], v[174:177], v[2:5]
	s_nop 0
	s_add_i32 s38, 0, 0x18000
	v_add_u32_e32 v142, s38, v200
	s_barrier
	ds_read_b128 v[130:133], v142
	ds_read_b128 v[134:137], v142 offset:1024
	ds_read_b128 v[138:141], v142 offset:2048
	ds_read_b128 v[142:145], v142 offset:3072
	s_mov_b32 m0, s55
	v_lshl_add_u64 v[220:221], s[42:43], 0, v[0:1]
	ds_read_b128 v[146:149], v216 offset:32768
	ds_read_b128 v[150:153], v216 offset:33792
	ds_read_b128 v[154:157], v216 offset:34816
	ds_read_b128 v[158:161], v216 offset:35840
	ds_read_b128 v[162:165], v216 offset:36864
	ds_read_b128 v[166:169], v216 offset:37888
	ds_read_b128 v[170:173], v216 offset:38912
	ds_read_b128 v[174:177], v216 offset:39936
	global_load_lds_dwordx4 v[220:221], off
	v_lshl_add_u64 v[220:221], s[42:43], 0, v[186:187]
	s_mov_b32 m0, s56
	s_nop 0
	global_load_lds_dwordx4 v[220:221], off
	s_waitcnt lgkmcnt(8)
	s_barrier
	s_waitcnt lgkmcnt(0)
	s_nop 0
	s_waitcnt lgkmcnt(0)
	v_mfma_f32_16x16x32_bf16 v[126:129], v[130:133], v[146:149], v[126:129]
	v_mfma_f32_16x16x32_bf16 v[122:125], v[138:141], v[146:149], v[122:125]
	v_mfma_f32_16x16x32_bf16 v[110:113], v[130:133], v[154:157], v[110:113]
	v_mfma_f32_16x16x32_bf16 v[106:109], v[138:141], v[154:157], v[106:109]
	v_mfma_f32_16x16x32_bf16 v[94:97], v[130:133], v[162:165], v[94:97]
	v_mfma_f32_16x16x32_bf16 v[90:93], v[138:141], v[162:165], v[90:93]
	v_mfma_f32_16x16x32_bf16 v[78:81], v[130:133], v[170:173], v[78:81]
	v_mfma_f32_16x16x32_bf16 v[74:77], v[138:141], v[170:173], v[74:77]
	v_mfma_f32_16x16x32_bf16 v[126:129], v[134:137], v[150:153], v[126:129]
	v_mfma_f32_16x16x32_bf16 v[122:125], v[142:145], v[150:153], v[122:125]
	v_mfma_f32_16x16x32_bf16 v[110:113], v[134:137], v[158:161], v[110:113]
	v_mfma_f32_16x16x32_bf16 v[106:109], v[142:145], v[158:161], v[106:109]
	v_mfma_f32_16x16x32_bf16 v[94:97], v[134:137], v[166:169], v[94:97]
	v_mfma_f32_16x16x32_bf16 v[90:93], v[142:145], v[166:169], v[90:93]
	v_mfma_f32_16x16x32_bf16 v[78:81], v[134:137], v[174:177], v[78:81]
	v_mfma_f32_16x16x32_bf16 v[74:77], v[142:145], v[174:177], v[74:77]
	s_nop 0
	s_barrier
	s_add_i32 s39, 0, 0x1c000
	s_add_i32 s38, s38, s50
	v_add_u32_e32 v183, s39, v200
	v_lshl_add_u64 v[236:237], v[236:237], 0, s[18:19]
	s_mov_b32 m0, s38
	ds_read_b128 v[220:223], v183
	ds_read_b128 v[224:227], v183 offset:1024
	ds_read_b128 v[228:231], v183 offset:2048
	ds_read_b128 v[232:235], v183 offset:3072
	global_load_lds_dwordx4 v[236:237], off
	v_lshl_add_u64 v[236:237], v[238:239], 0, s[18:19]
	s_add_i32 m0, s38, 0x2000
	s_nop 0
	global_load_lds_dwordx4 v[236:237], off
	s_barrier
; #define G8_STAGE(bufoff, gbase, voff) do { _Pragma("unroll") for (int _i = 0; _i < 2; ++_i) \
;         __builtin_amdgcn_global_load_lds((const unsigned*)((const char*)(gbase) + (voff)[_i]), (LAS unsigned*)(lds + (bufoff) + ldsw + _i * 8192), 16, 0, 0); } while (0)
; #define G8_LDA(dst, b, h) do { _Pragma("unroll") for (int m = 0; m < 4; ++m) _Pragma("unroll") for (int k = 0; k < 2; ++k) dst[m][k] = *(const LAS bf16x8*)(lds + G8_SA(b, h) + aoff + m * 2048 + k * 1024); } while (0)
; #define G8_MMA(ai, bj, At, Bt) do { __builtin_amdgcn_s_setprio(1); _Pragma("unroll") for (int m = 0; m < 4; ++m) _Pragma("unroll") for (int n = 0; n < 2; ++n) _Pragma("unroll") for (int k = 0; k < 2; ++k) \
;         acc[ai][bj][m][n] = __builtin_amdgcn_mfma_f32_16x16x32_bf16(Bt[n][k], At[m][k], acc[ai][bj][m][n], 0, 0, 0); __builtin_amdgcn_s_setprio(0); } while (0)
; #define G8_WAIT_V(n) asm volatile("s_waitcnt vmcnt(" #n ")" ::: "memory")
; #define G8_WAIT_L(n) asm volatile("s_waitcnt lgkmcnt(" #n ")" ::: "memory")
; #define G8_BAR __builtin_amdgcn_s_barrier()
; #define G8_SCHED __builtin_amdgcn_sched_barrier(0)
; template <class Epi, class Sched>
; __device__ __forceinline__ void gemm_phase(LAS unsigned char* lds, const int K, const Sched& S, const Epi& E) {
;     ...
;             G8_BAR; G8_WAIT_L(0); G8_MMA(0, 1, At, B1); G8_BAR;
;             G8_LDA(At, 1, 1); G8_STAGE(G8_SA(1, 0), a3, oc[0]);
;             G8_BAR; G8_WAIT_L(0); G8_MMA(1, 0, At, B0); G8_BAR; G8_SCHED;
;             G8_STAGE(G8_SB(1, 1), b3 + hstep, voffB);
;             G8_WAIT_V(6); G8_BAR; G8_MMA(1, 1, At, B1); G8_BAR;
;         }
	s_waitcnt lgkmcnt(0)
	s_nop 0
	s_waitcnt lgkmcnt(0)
	v_mfma_f32_16x16x32_bf16 v[118:121], v[220:223], v[146:149], v[118:121]
	v_mfma_f32_16x16x32_bf16 v[114:117], v[228:231], v[146:149], v[114:117]
	v_mfma_f32_16x16x32_bf16 v[102:105], v[220:223], v[154:157], v[102:105]
	v_mfma_f32_16x16x32_bf16 v[98:101], v[228:231], v[154:157], v[98:101]
	v_mfma_f32_16x16x32_bf16 v[86:89], v[220:223], v[162:165], v[86:89]
	v_mfma_f32_16x16x32_bf16 v[82:85], v[228:231], v[162:165], v[82:85]
	v_mfma_f32_16x16x32_bf16 v[70:73], v[220:223], v[170:173], v[70:73]
	v_mfma_f32_16x16x32_bf16 v[66:69], v[228:231], v[170:173], v[66:69]
	v_mfma_f32_16x16x32_bf16 v[118:121], v[224:227], v[150:153], v[118:121]
	v_mfma_f32_16x16x32_bf16 v[114:117], v[232:235], v[150:153], v[114:117]
	v_mfma_f32_16x16x32_bf16 v[102:105], v[224:227], v[158:161], v[102:105]
	v_mfma_f32_16x16x32_bf16 v[98:101], v[232:235], v[158:161], v[98:101]
	v_mfma_f32_16x16x32_bf16 v[86:89], v[224:227], v[166:169], v[86:89]
	v_mfma_f32_16x16x32_bf16 v[82:85], v[232:235], v[166:169], v[82:85]
	v_mfma_f32_16x16x32_bf16 v[70:73], v[224:227], v[174:177], v[70:73]
	v_mfma_f32_16x16x32_bf16 v[66:69], v[232:235], v[174:177], v[66:69]
	s_nop 0
	s_mov_b32 m0, s57
	v_lshl_add_u64 v[236:237], v[240:241], 0, s[18:19]
	s_barrier
	ds_read_b128 v[146:149], v216 offset:49152
	ds_read_b128 v[150:153], v216 offset:50176
	ds_read_b128 v[154:157], v216 offset:51200
	ds_read_b128 v[158:161], v216 offset:52224
	ds_read_b128 v[162:165], v216 offset:53248
	ds_read_b128 v[166:169], v216 offset:54272
	ds_read_b128 v[170:173], v216 offset:55296
	ds_read_b128 v[174:177], v216 offset:56320
	global_load_lds_dwordx4 v[236:237], off
	v_lshl_add_u64 v[236:237], v[242:243], 0, s[18:19]
	s_mov_b32 m0, s58
	s_nop 0
	global_load_lds_dwordx4 v[236:237], off
	s_barrier
	s_waitcnt lgkmcnt(0)
	s_nop 0
	s_waitcnt lgkmcnt(0)
	v_mfma_f32_16x16x32_bf16 v[62:65], v[130:133], v[146:149], v[62:65]
	v_mfma_f32_16x16x32_bf16 v[58:61], v[138:141], v[146:149], v[58:61]
	v_mfma_f32_16x16x32_bf16 v[46:49], v[130:133], v[154:157], v[46:49]
	v_mfma_f32_16x16x32_bf16 v[42:45], v[138:141], v[154:157], v[42:45]
	v_mfma_f32_16x16x32_bf16 v[30:33], v[130:133], v[162:165], v[30:33]
	v_mfma_f32_16x16x32_bf16 v[26:29], v[138:141], v[162:165], v[26:29]
	v_mfma_f32_16x16x32_bf16 v[14:17], v[130:133], v[170:173], v[14:17]
	v_mfma_f32_16x16x32_bf16 v[10:13], v[138:141], v[170:173], v[10:13]
	v_mfma_f32_16x16x32_bf16 v[62:65], v[134:137], v[150:153], v[62:65]
	v_mfma_f32_16x16x32_bf16 v[58:61], v[142:145], v[150:153], v[58:61]
	v_mfma_f32_16x16x32_bf16 v[46:49], v[134:137], v[158:161], v[46:49]
	v_mfma_f32_16x16x32_bf16 v[42:45], v[142:145], v[158:161], v[42:45]
	v_mfma_f32_16x16x32_bf16 v[30:33], v[134:137], v[166:169], v[30:33]
	v_mfma_f32_16x16x32_bf16 v[26:29], v[142:145], v[166:169], v[26:29]
	v_mfma_f32_16x16x32_bf16 v[14:17], v[134:137], v[174:177], v[14:17]
	v_mfma_f32_16x16x32_bf16 v[10:13], v[142:145], v[174:177], v[10:13]
	s_nop 0
	s_barrier
	s_add_u32 s36, s36, 0x10080
	s_addc_u32 s37, s37, 0
	s_add_i32 s38, s39, s50
	v_lshl_add_u64 v[130:131], s[36:37], 0, v[178:179]
	s_mov_b32 m0, s38
	s_nop 0
	global_load_lds_dwordx4 v[130:131], off
	v_lshl_add_u64 v[130:131], s[36:37], 0, v[180:181]
	s_add_i32 m0, s38, 0x2000
	s_nop 0
	global_load_lds_dwordx4 v[130:131], off
	s_waitcnt vmcnt(6)
	s_barrier
	s_nop 0
	v_mfma_f32_16x16x32_bf16 v[54:57], v[220:223], v[146:149], v[54:57]
	v_mfma_f32_16x16x32_bf16 v[50:53], v[228:231], v[146:149], v[50:53]
	v_mfma_f32_16x16x32_bf16 v[38:41], v[220:223], v[154:157], v[38:41]
	v_mfma_f32_16x16x32_bf16 v[34:37], v[228:231], v[154:157], v[34:37]
	v_mfma_f32_16x16x32_bf16 v[22:25], v[220:223], v[162:165], v[22:25]
	v_mfma_f32_16x16x32_bf16 v[18:21], v[228:231], v[162:165], v[18:21]
	v_mfma_f32_16x16x32_bf16 v[6:9], v[220:223], v[170:173], v[6:9]
	v_mfma_f32_16x16x32_bf16 v[2:5], v[228:231], v[170:173], v[2:5]
	v_mfma_f32_16x16x32_bf16 v[54:57], v[224:227], v[150:153], v[54:57]
	v_mfma_f32_16x16x32_bf16 v[50:53], v[232:235], v[150:153], v[50:53]
	v_mfma_f32_16x16x32_bf16 v[38:41], v[224:227], v[158:161], v[38:41]
	v_mfma_f32_16x16x32_bf16 v[34:37], v[232:235], v[158:161], v[34:37]
	v_mfma_f32_16x16x32_bf16 v[22:25], v[224:227], v[166:169], v[22:25]
	v_mfma_f32_16x16x32_bf16 v[18:21], v[232:235], v[166:169], v[18:21]
	v_mfma_f32_16x16x32_bf16 v[6:9], v[224:227], v[174:177], v[6:9]
	v_mfma_f32_16x16x32_bf16 v[2:5], v[232:235], v[174:177], v[2:5]
	s_nop 0
	s_mov_b64 s[42:43], 0
	s_mov_b64 s[36:37], -1
	s_and_b64 vcc, exec, s[40:41]
	s_barrier
	s_cbranch_vccnz .LBB0_2618
	s_mov_b64 s[38:39], 0x100
	s_branch .LBB0_2614

; #define G8_WAIT_V(n) asm volatile("s_waitcnt vmcnt(" #n ")" ::: "memory")
; #define G8_BAR __builtin_amdgcn_s_barrier()
; template <class Epi, class Sched>
; __device__ __forceinline__ void gemm_phase(LAS unsigned char* lds, const int K, const Sched& S, const Epi& E) {
;     ...
;     G8_WAIT_V(0);
;     if (wr == 0) G8_BAR;
;     G8_BAR;
.LBB0_2668:
	s_barrier
	s_setprio 0
	s_nop 0
	s_nop 0
	s_nop 0
	s_nop 0
	s_nop 0
	s_nop 0
	s_nop 0
	s_nop 0
	s_nop 0
	s_nop 0
	s_nop 0
	s_nop 0
	s_nop 0
	s_nop 0
	s_nop 0
